# parallel instruction-cache warm-up (branch pads every 14 instrs, waves hop through 1/16 each while the first loads are in flight) now in k_layer<1>, k_layer<2>, k_bucketsort and k_localsort
# speedup vs baseline: 1.2861x; 1.0905x over previous
.LBB1_11:
	s_or_b64 exec, exec, s[10:11]
	v_mov_b32_e32 v35, 0
	v_add_u32_e32 v1, 0x6a0, v34
	s_waitcnt lgkmcnt(0)
	v_add_u32_e32 v76, 0x4000, v34
	v_add_u32_e32 v77, 0x8000, v34
	v_add_u32_e32 v78, 0xc000, v34
	v_add_u32_e32 v79, 0x10000, v34
	v_add_u32_e32 v80, 0x14000, v34
	v_add_u32_e32 v81, 0x18000, v34
	v_add_u32_e32 v82, 0x1c000, v34
	v_add_u32_e32 v83, 0x20000, v34
	global_load_dwordx4 v[40:43], v34, s[62:63]
	global_load_dwordx4 v[44:47], v76, s[62:63]
	global_load_dwordx4 v[48:51], v77, s[62:63]
	global_load_dwordx4 v[52:55], v78, s[62:63]
	global_load_dwordx4 v[56:59], v79, s[62:63]
	global_load_dwordx4 v[60:63], v80, s[62:63]
	global_load_dwordx4 v[64:67], v81, s[62:63]
	global_load_dwordx4 v[68:71], v82, s[62:63]
	s_movk_i32 s10, 0x8e
	s_mov_b64 s[6:7], exec
	v_cmp_gt_u32_e64 s[4:5], s10, v0
	s_and_b64 exec, exec, s[4:5]
	global_load_dwordx4 v[72:75], v83, s[62:63]
	s_mov_b64 exec, s[6:7]
	v_readfirstlane_b32 s10, v0
	s_lshr_b32 s10, s10, 6
	s_cmp_eq_u32 s10, 0
	s_cbranch_scc1 .Licl_t0
	s_cmp_eq_u32 s10, 1
	s_cbranch_scc1 .Licl_t1
	s_cmp_eq_u32 s10, 2
	s_cbranch_scc1 .Licl_t2
	s_cmp_eq_u32 s10, 3
	s_cbranch_scc1 .Licl_t3
	s_cmp_eq_u32 s10, 4
	s_cbranch_scc1 .Licl_t4
	s_cmp_eq_u32 s10, 5
	s_cbranch_scc1 .Licl_t5
	s_cmp_eq_u32 s10, 6
	s_cbranch_scc1 .Licl_t6
	s_cmp_eq_u32 s10, 7
	s_cbranch_scc1 .Licl_t7
	s_cmp_eq_u32 s10, 8
	s_cbranch_scc1 .Licl_t8
	s_cmp_eq_u32 s10, 9
	s_cbranch_scc1 .Licl_t9
	s_cmp_eq_u32 s10, 10
	s_cbranch_scc1 .Licl_t10
	s_cmp_eq_u32 s10, 11
	s_cbranch_scc1 .Licl_t11
	s_cmp_eq_u32 s10, 12
	s_cbranch_scc1 .Licl_t12
	s_cmp_eq_u32 s10, 13
	s_cbranch_scc1 .Licl_t13
	s_cmp_eq_u32 s10, 14
	s_cbranch_scc1 .Licl_t14
	s_cmp_eq_u32 s10, 15
	s_cbranch_scc1 .Licl_t15
.Licl_done:
	v_add_u32_e32 v84, 0x10000, v1
	v_add_u32_e32 v85, 0x20000, v1
	s_waitcnt vmcnt(0)
	ds_write_b128 v1, v[40:43]
	ds_write_b128 v1, v[44:47] offset:16384
	ds_write_b128 v1, v[48:51] offset:32768
	ds_write_b128 v1, v[52:55] offset:49152
	ds_write_b128 v84, v[56:59]
	ds_write_b128 v84, v[60:63] offset:16384
	ds_write_b128 v84, v[64:67] offset:32768
	ds_write_b128 v84, v[68:71] offset:49152
	s_and_b64 exec, exec, s[4:5]
	ds_write_b128 v85, v[72:75]
	s_mov_b64 exec, s[6:7]
	v_cmp_lt_i32_e64 s[4:5], -1, v30
	v_mov_b32_e32 v39, 0
	v_mov_b32_e32 v36, 0
	v_lshrrev_b32_e32 v37, 6, v30
	v_mov_b32_e32 v41, 0
	s_waitcnt lgkmcnt(0)
	s_barrier
	s_and_saveexec_b64 s[6:7], s[4:5]
	s_cbranch_execz .LBB1_15
	s_mov_b32 s8, 0xaaaaaaab
	v_mul_hi_u32 v39, v26, s8
	v_lshrrev_b32_e32 v39, 1, v39
	v_mov_b32_e32 v41, 0x6a0
	v_lshl_add_u32 v41, v39, 2, v41
	ds_read_b32 v44, v41
	v_mov_b32_e32 v40, 1
	v_and_b32_e32 v41, 0x3fffffc, v37
	ds_add_rtn_u32 v41, v41, v40
	v_mad_u64_u32 v[42:43], s[8:9], v39, -3, v[26:27]
	v_mul_lo_u32 v39, v42, 10
	s_waitcnt lgkmcnt(1)
	v_lshrrev_b32_e32 v39, v39, v44
	v_and_b32_e32 v39, 0x3ff, v39
.LBB1_15:
	s_or_b64 exec, exec, s[6:7]
	v_cmp_lt_i32_e64 s[6:7], -1, v31
	v_lshrrev_b32_e32 v42, 6, v31
	v_mov_b32_e32 v43, 0
	s_and_saveexec_b64 s[8:9], s[6:7]
	s_cbranch_execz .LBB1_17
	s_mov_b32 s10, 0xaaaaaaab
	v_mul_hi_u32 v36, v27, s10
	v_lshrrev_b32_e32 v44, 1, v36
	v_mov_b32_e32 v36, 0x6a0
	v_lshl_add_u32 v36, v44, 2, v36
	ds_read_b32 v46, v36
	v_mov_b32_e32 v43, 1
	v_and_b32_e32 v36, 0x3fffffc, v42
	s_branch .Licl_s0

.Licl_s0:
	v_mov_b32_e32 v40, v27
	ds_add_rtn_u32 v36, v36, v43
	s_waitcnt lgkmcnt(2)
	v_mad_u64_u32 v[44:45], s[10:11], v44, -3, v[40:41]
	v_mul_lo_u32 v40, v44, 10
	s_waitcnt lgkmcnt(1)
	v_lshrrev_b32_e32 v40, v40, v46
	v_and_b32_e32 v43, 0x3ff, v40
.LBB1_17:
	s_or_b64 exec, exec, s[8:9]
	v_cmp_lt_i32_e64 s[8:9], -1, v32
	v_mov_b32_e32 v45, 0
	v_mov_b32_e32 v40, 0
	v_lshrrev_b32_e32 v44, 6, v32
	v_mov_b32_e32 v47, 0
	s_branch .Licl_s1

.Licl_s1:
	s_and_saveexec_b64 s[10:11], s[8:9]
	s_cbranch_execz .LBB1_19
	s_mov_b32 s12, 0xaaaaaaab
	v_mul_hi_u32 v45, v28, s12
	v_lshrrev_b32_e32 v45, 1, v45
	v_mov_b32_e32 v47, 0x6a0
	v_lshl_add_u32 v47, v45, 2, v47
	ds_read_b32 v50, v47
	v_mov_b32_e32 v46, 1
	v_and_b32_e32 v47, 0x3fffffc, v44
	ds_add_rtn_u32 v47, v47, v46
	v_mad_u64_u32 v[48:49], s[12:13], v45, -3, v[28:29]
	v_mul_lo_u32 v45, v48, 10
	s_waitcnt lgkmcnt(1)
	s_branch .Licl_s2

.Licl_s2:
	v_lshrrev_b32_e32 v45, v45, v50
	v_and_b32_e32 v45, 0x3ff, v45
.LBB1_19:
	s_or_b64 exec, exec, s[10:11]
	v_cmp_lt_i32_e64 s[10:11], -1, v33
	v_lshrrev_b32_e32 v48, 6, v33
	v_mov_b32_e32 v49, 0
	s_and_saveexec_b64 s[12:13], s[10:11]
	s_cbranch_execz .LBB1_21
	s_mov_b32 s14, 0xaaaaaaab
	v_mul_hi_u32 v40, v29, s14
	v_lshrrev_b32_e32 v50, 1, v40
	v_mov_b32_e32 v40, 0x6a0
	v_lshl_add_u32 v40, v50, 2, v40
	ds_read_b32 v52, v40
	s_branch .Licl_s3

.Licl_s3:
	v_mov_b32_e32 v49, 1
	v_and_b32_e32 v40, 0x3fffffc, v48
	v_mov_b32_e32 v46, v29
	ds_add_rtn_u32 v40, v40, v49
	s_waitcnt lgkmcnt(2)
	v_mad_u64_u32 v[50:51], s[14:15], v50, -3, v[46:47]
	v_mul_lo_u32 v46, v50, 10
	s_waitcnt lgkmcnt(1)
	v_lshrrev_b32_e32 v46, v46, v52
	v_and_b32_e32 v49, 0x3ff, v46
.LBB1_21:
	s_or_b64 exec, exec, s[12:13]
	v_cmp_lt_i32_e64 s[12:13], -1, v10
	v_mov_b32_e32 v51, 0
	v_mov_b32_e32 v46, 0
	s_branch .Licl_s4

.Licl_s4:
	v_lshrrev_b32_e32 v50, 6, v10
	v_mov_b32_e32 v53, 0
	s_and_saveexec_b64 s[14:15], s[12:13]
	s_cbranch_execz .LBB1_23
	s_mov_b32 s16, 0xaaaaaaab
	v_mul_hi_u32 v51, v14, s16
	v_lshrrev_b32_e32 v51, 1, v51
	v_mov_b32_e32 v53, 0x6a0
	v_lshl_add_u32 v53, v51, 2, v53
	ds_read_b32 v56, v53
	v_mov_b32_e32 v52, 1
	v_and_b32_e32 v53, 0x3fffffc, v50
	ds_add_rtn_u32 v53, v53, v52
	v_mad_u64_u32 v[54:55], s[16:17], v51, -3, v[14:15]
	s_branch .Licl_s5

.Licl_s5:
	v_mul_lo_u32 v51, v54, 10
	s_waitcnt lgkmcnt(1)
	v_lshrrev_b32_e32 v51, v51, v56
	v_and_b32_e32 v51, 0x3ff, v51
.LBB1_23:
	s_or_b64 exec, exec, s[14:15]
	v_cmp_lt_i32_e64 s[14:15], -1, v11
	v_lshrrev_b32_e32 v54, 6, v11
	v_mov_b32_e32 v55, 0
	s_and_saveexec_b64 s[16:17], s[14:15]
	s_cbranch_execz .LBB1_25
	s_mov_b32 s18, 0xaaaaaaab
	v_mul_hi_u32 v46, v15, s18
	v_lshrrev_b32_e32 v56, 1, v46
	v_mov_b32_e32 v46, 0x6a0
	s_branch .Licl_s6

.Licl_s6:
	v_lshl_add_u32 v46, v56, 2, v46
	ds_read_b32 v58, v46
	v_mov_b32_e32 v55, 1
	v_and_b32_e32 v46, 0x3fffffc, v54
	v_mov_b32_e32 v52, v15
	ds_add_rtn_u32 v46, v46, v55
	s_waitcnt lgkmcnt(2)
	v_mad_u64_u32 v[56:57], s[18:19], v56, -3, v[52:53]
	v_mul_lo_u32 v52, v56, 10
	s_waitcnt lgkmcnt(1)
	v_lshrrev_b32_e32 v52, v52, v58
	v_and_b32_e32 v55, 0x3ff, v52
.LBB1_25:
	s_or_b64 exec, exec, s[16:17]
	v_cmp_lt_i32_e64 s[16:17], -1, v12
	s_branch .Licl_s7

.Licl_s7:
	v_mov_b32_e32 v57, 0
	v_mov_b32_e32 v52, 0
	v_lshrrev_b32_e32 v56, 6, v12
	v_mov_b32_e32 v59, 0
	s_and_saveexec_b64 s[18:19], s[16:17]
	s_cbranch_execz .LBB1_27
	s_mov_b32 s20, 0xaaaaaaab
	v_mul_hi_u32 v57, v16, s20
	v_lshrrev_b32_e32 v57, 1, v57
	v_mov_b32_e32 v59, 0x6a0
	v_lshl_add_u32 v59, v57, 2, v59
	ds_read_b32 v62, v59
	v_mov_b32_e32 v58, 1
	v_and_b32_e32 v59, 0x3fffffc, v56
	s_branch .Licl_s8

.Licl_s8:
	ds_add_rtn_u32 v59, v59, v58
	v_mad_u64_u32 v[60:61], s[20:21], v57, -3, v[16:17]
	v_mul_lo_u32 v57, v60, 10
	s_waitcnt lgkmcnt(1)
	v_lshrrev_b32_e32 v57, v57, v62
	v_and_b32_e32 v57, 0x3ff, v57
.LBB1_27:
	s_or_b64 exec, exec, s[18:19]
	v_cmp_lt_i32_e64 s[18:19], -1, v13
	v_lshrrev_b32_e32 v60, 6, v13
	v_mov_b32_e32 v61, 0
	s_and_saveexec_b64 s[20:21], s[18:19]
	s_cbranch_execz .LBB1_29
	s_mov_b32 s22, 0xaaaaaaab
	v_mul_hi_u32 v52, v17, s22
	s_branch .Licl_s9

.Licl_s9:
	v_lshrrev_b32_e32 v62, 1, v52
	v_mov_b32_e32 v52, 0x6a0
	v_lshl_add_u32 v52, v62, 2, v52
	ds_read_b32 v64, v52
	v_mov_b32_e32 v61, 1
	v_and_b32_e32 v52, 0x3fffffc, v60
	v_mov_b32_e32 v58, v17
	ds_add_rtn_u32 v52, v52, v61
	s_waitcnt lgkmcnt(2)
	v_mad_u64_u32 v[62:63], s[22:23], v62, -3, v[58:59]
	v_mul_lo_u32 v58, v62, 10
	s_waitcnt lgkmcnt(1)
	v_lshrrev_b32_e32 v58, v58, v64
	v_and_b32_e32 v61, 0x3ff, v58
.LBB1_29:
	s_or_b64 exec, exec, s[20:21]
	s_branch .Licl_s10

.Licl_s10:
	v_cmp_lt_i32_e64 s[20:21], -1, v22
	v_mov_b32_e32 v63, 0
	v_mov_b32_e32 v58, 0
	v_lshrrev_b32_e32 v62, 6, v22
	v_mov_b32_e32 v65, 0
	s_and_saveexec_b64 s[22:23], s[20:21]
	s_cbranch_execz .LBB1_31
	s_mov_b32 s24, 0xaaaaaaab
	v_mul_hi_u32 v63, v18, s24
	v_lshrrev_b32_e32 v63, 1, v63
	v_mov_b32_e32 v65, 0x6a0
	v_lshl_add_u32 v65, v63, 2, v65
	ds_read_b32 v68, v65
	v_mov_b32_e32 v64, 1
	s_branch .Licl_s11

.Licl_s11:
	v_and_b32_e32 v65, 0x3fffffc, v62
	ds_add_rtn_u32 v65, v65, v64
	v_mad_u64_u32 v[66:67], s[24:25], v63, -3, v[18:19]
	v_mul_lo_u32 v63, v66, 10
	s_waitcnt lgkmcnt(1)
	v_lshrrev_b32_e32 v63, v63, v68
	v_and_b32_e32 v63, 0x3ff, v63
.LBB1_31:
	s_or_b64 exec, exec, s[22:23]
	v_cmp_lt_i32_e64 s[22:23], -1, v23
	v_lshrrev_b32_e32 v66, 6, v23
	v_mov_b32_e32 v67, 0
	s_and_saveexec_b64 s[24:25], s[22:23]
	s_cbranch_execz .LBB1_33
	s_mov_b32 s26, 0xaaaaaaab
	s_branch .Licl_s12

.Licl_s12:
	v_mul_hi_u32 v58, v19, s26
	v_lshrrev_b32_e32 v68, 1, v58
	v_mov_b32_e32 v58, 0x6a0
	v_lshl_add_u32 v58, v68, 2, v58
	ds_read_b32 v70, v58
	v_mov_b32_e32 v67, 1
	v_and_b32_e32 v58, 0x3fffffc, v66
	v_mov_b32_e32 v64, v19
	ds_add_rtn_u32 v58, v58, v67
	s_waitcnt lgkmcnt(2)
	v_mad_u64_u32 v[68:69], s[26:27], v68, -3, v[64:65]
	v_mul_lo_u32 v64, v68, 10
	s_waitcnt lgkmcnt(1)
	v_lshrrev_b32_e32 v64, v64, v70
	s_branch .Licl_s13

.Licl_s13:
	v_and_b32_e32 v67, 0x3ff, v64
.LBB1_33:
	s_or_b64 exec, exec, s[24:25]
	v_cmp_lt_i32_e64 s[24:25], -1, v24
	v_mov_b32_e32 v69, 0
	v_mov_b32_e32 v64, 0
	v_lshrrev_b32_e32 v68, 6, v24
	v_mov_b32_e32 v71, 0
	s_and_saveexec_b64 s[26:27], s[24:25]
	s_cbranch_execz .LBB1_35
	s_mov_b32 s28, 0xaaaaaaab
	v_mul_hi_u32 v69, v20, s28
	v_lshrrev_b32_e32 v69, 1, v69
	v_mov_b32_e32 v71, 0x6a0
	v_lshl_add_u32 v71, v69, 2, v71
	s_branch .Licl_s14

.Licl_s14:
	ds_read_b32 v74, v71
	v_mov_b32_e32 v70, 1
	v_and_b32_e32 v71, 0x3fffffc, v68
	ds_add_rtn_u32 v71, v71, v70
	v_mad_u64_u32 v[72:73], s[28:29], v69, -3, v[20:21]
	v_mul_lo_u32 v69, v72, 10
	s_waitcnt lgkmcnt(1)
	v_lshrrev_b32_e32 v69, v69, v74
	v_and_b32_e32 v69, 0x3ff, v69
.LBB1_35:
	s_or_b64 exec, exec, s[26:27]
	v_cmp_lt_i32_e64 s[26:27], -1, v25
	v_lshrrev_b32_e32 v72, 6, v25
	v_mov_b32_e32 v73, 0
	s_and_saveexec_b64 s[28:29], s[26:27]
	s_branch .Licl_s15

.Licl_s15:
	s_cbranch_execz .LBB1_37
	s_mov_b32 s30, 0xaaaaaaab
	v_mul_hi_u32 v64, v21, s30
	v_lshrrev_b32_e32 v74, 1, v64
	v_mov_b32_e32 v64, 0x6a0
	v_lshl_add_u32 v64, v74, 2, v64
	ds_read_b32 v76, v64
	v_mov_b32_e32 v73, 1
	v_and_b32_e32 v64, 0x3fffffc, v72
	v_mov_b32_e32 v70, v21
	ds_add_rtn_u32 v64, v64, v73
	s_waitcnt lgkmcnt(2)
	v_mad_u64_u32 v[74:75], s[30:31], v74, -3, v[70:71]
	v_mul_lo_u32 v70, v74, 10
	s_branch .Licl_s16

.Licl_s16:
	s_waitcnt lgkmcnt(1)
	v_lshrrev_b32_e32 v70, v70, v76
	v_and_b32_e32 v73, 0x3ff, v70
.LBB1_37:
	s_or_b64 exec, exec, s[28:29]
	v_cmp_lt_i32_e64 s[28:29], -1, v2
	v_mov_b32_e32 v75, 0
	v_mov_b32_e32 v70, 0
	v_lshrrev_b32_e32 v74, 6, v2
	v_mov_b32_e32 v77, 0
	s_and_saveexec_b64 s[30:31], s[28:29]
	s_cbranch_execz .LBB1_39
	s_mov_b32 s34, 0xaaaaaaab
	v_mul_hi_u32 v75, v6, s34
	v_lshrrev_b32_e32 v75, 1, v75
	s_branch .Licl_s17

.Licl_s17:
	v_mov_b32_e32 v77, 0x6a0
	v_lshl_add_u32 v77, v75, 2, v77
	ds_read_b32 v80, v77
	v_mov_b32_e32 v76, 1
	v_and_b32_e32 v77, 0x3fffffc, v74
	ds_add_rtn_u32 v77, v77, v76
	v_mad_u64_u32 v[78:79], s[34:35], v75, -3, v[6:7]
	v_mul_lo_u32 v75, v78, 10
	s_waitcnt lgkmcnt(1)
	v_lshrrev_b32_e32 v75, v75, v80
	v_and_b32_e32 v75, 0x3ff, v75
.LBB1_39:
	s_or_b64 exec, exec, s[30:31]
	v_cmp_lt_i32_e64 s[30:31], -1, v3
	v_lshrrev_b32_e32 v78, 6, v3
	s_branch .Licl_s18

.Licl_s18:
	v_mov_b32_e32 v79, 0
	s_and_saveexec_b64 s[34:35], s[30:31]
	s_cbranch_execz .LBB1_41
	s_mov_b32 s36, 0xaaaaaaab
	v_mul_hi_u32 v70, v7, s36
	v_lshrrev_b32_e32 v80, 1, v70
	v_mov_b32_e32 v70, 0x6a0
	v_lshl_add_u32 v70, v80, 2, v70
	ds_read_b32 v82, v70
	v_mov_b32_e32 v79, 1
	v_and_b32_e32 v70, 0x3fffffc, v78
	v_mov_b32_e32 v76, v7
	ds_add_rtn_u32 v70, v70, v79
	s_waitcnt lgkmcnt(2)
	s_branch .Licl_s19

.Licl_s19:
	v_mad_u64_u32 v[80:81], s[36:37], v80, -3, v[76:77]
	v_mul_lo_u32 v76, v80, 10
	s_waitcnt lgkmcnt(1)
	v_lshrrev_b32_e32 v76, v76, v82
	v_and_b32_e32 v79, 0x3ff, v76
.LBB1_41:
	s_or_b64 exec, exec, s[34:35]
	v_cmp_lt_i32_e64 s[34:35], -1, v4
	v_mov_b32_e32 v81, 0
	v_mov_b32_e32 v76, 0
	v_lshrrev_b32_e32 v80, 6, v4
	v_mov_b32_e32 v82, 0
	s_and_saveexec_b64 s[36:37], s[34:35]
	s_cbranch_execz .LBB1_43
	s_mov_b32 s38, 0xaaaaaaab
	s_branch .Licl_s20

.Licl_s20:
	v_mul_hi_u32 v81, v8, s38
	v_lshrrev_b32_e32 v81, 1, v81
	v_mov_b32_e32 v83, 0x6a0
	v_lshl_add_u32 v83, v81, 2, v83
	ds_read_b32 v83, v83
	v_mov_b32_e32 v82, 1
	v_and_b32_e32 v84, 0x3fffffc, v80
	ds_add_rtn_u32 v82, v84, v82
	v_mad_u64_u32 v[84:85], s[38:39], v81, -3, v[8:9]
	v_mul_lo_u32 v81, v84, 10
	s_waitcnt lgkmcnt(1)
	v_lshrrev_b32_e32 v81, v81, v83
	v_and_b32_e32 v81, 0x3ff, v81
.LBB1_43:
	s_or_b64 exec, exec, s[36:37]
	s_branch .Licl_s21

.Licl_s21:
	v_cmp_lt_i32_e64 s[36:37], -1, v5
	v_lshrrev_b32_e32 v83, 6, v5
	v_mov_b32_e32 v84, 0
	s_and_saveexec_b64 s[38:39], s[36:37]
	s_cbranch_execz .LBB1_45
	s_mov_b32 s40, 0xaaaaaaab
	v_mul_hi_u32 v76, v9, s40
	v_lshrrev_b32_e32 v86, 1, v76
	v_mov_b32_e32 v76, 0x6a0
	v_lshl_add_u32 v76, v86, 2, v76
	ds_read_b32 v87, v76
	v_mov_b32_e32 v85, 1
	v_and_b32_e32 v76, 0x3fffffc, v83
	v_mov_b32_e32 v84, v9
	s_branch .Licl_s22

.Licl_s22:
	ds_add_rtn_u32 v76, v76, v85
	v_mad_u64_u32 v[84:85], s[40:41], v86, -3, v[84:85]
	v_mul_lo_u32 v84, v84, 10
	s_waitcnt lgkmcnt(1)
	v_lshrrev_b32_e32 v84, v84, v87
	v_and_b32_e32 v84, 0x3ff, v84
.LBB1_45:
	s_or_b64 exec, exec, s[38:39]
	v_mov_b32_e32 v85, 0
	s_waitcnt lgkmcnt(0)
	s_barrier
	s_and_saveexec_b64 s[38:39], s[50:51]
	ds_read_b32 v85, v38
	s_or_b64 exec, exec, s[38:39]
	s_waitcnt lgkmcnt(0)
	s_branch .Licl_s23

.Licl_s23:
	v_mov_b32_e32 v86, v85
	v_and_b32_e32 v92, 63, v0
	v_lshrrev_b32_e32 v90, 6, v0
	v_add_u32_dpp v86, v86, v86 row_shr:1 row_mask:0xf bank_mask:0xf
	v_lshlrev_b32_e32 v90, 2, v90
	v_cmp_eq_u32_e64 s[52:53], 63, v92
	v_add_u32_dpp v86, v86, v86 row_shr:2 row_mask:0xf bank_mask:0xf
	v_cmp_lt_u32_e64 s[48:49], 63, v0
	v_cmp_gt_u32_e64 s[54:55], 16, v0
	v_add_u32_dpp v86, v86, v86 row_shr:4 row_mask:0xf bank_mask:0xf
	s_nop 1
	v_add_u32_dpp v86, v86, v86 row_shr:8 row_mask:0xf bank_mask:0xf
	s_nop 1
	v_add_u32_dpp v86, v86, v86 row_bcast:15 row_mask:0xa bank_mask:0xf
	s_branch .Licl_s24

.Licl_s24:
	s_nop 1
	v_add_u32_dpp v86, v86, v86 row_bcast:31 row_mask:0xc bank_mask:0xf
	s_and_saveexec_b64 s[46:47], s[52:53]
	ds_write_b32 v90, v86 offset:1568
	s_mov_b64 exec, s[46:47]
	s_waitcnt lgkmcnt(0)
	s_barrier
	s_and_saveexec_b64 s[46:47], s[54:55]
	s_cbranch_execz .Lls_scan2_done
	v_lshlrev_b32_e32 v92, 2, v92
	ds_read_b32 v87, v92 offset:1568
	s_waitcnt lgkmcnt(0)
	s_nop 1
	v_add_u32_dpp v87, v87, v87 row_shr:1 row_mask:0xf bank_mask:0xf
	s_branch .Licl_s25

.Licl_s25:
	s_nop 1
	v_add_u32_dpp v87, v87, v87 row_shr:2 row_mask:0xf bank_mask:0xf
	s_nop 1
	v_add_u32_dpp v87, v87, v87 row_shr:4 row_mask:0xf bank_mask:0xf
	s_nop 1
	v_add_u32_dpp v87, v87, v87 row_shr:8 row_mask:0xf bank_mask:0xf
	ds_write_b32 v92, v87 offset:1632
.Lls_scan2_done:
	s_or_b64 exec, exec, s[46:47]
	v_mov_b32_e32 v87, 0
	s_waitcnt lgkmcnt(0)
	v_mov_b32_e32 v88, 0
	s_barrier
	s_and_saveexec_b64 s[38:39], s[48:49]
	ds_read_b32 v88, v90 offset:1628
	s_or_b64 exec, exec, s[38:39]
	s_branch .Licl_s26

.Licl_s26:
	ds_read_b32 v87, v87 offset:1692
	s_mul_i32 s40, s2, 0x188
	s_and_saveexec_b64 s[38:39], s[50:51]
	s_cbranch_execz .LBB1_58
	v_sub_u32_e32 v85, v86, v85
	s_waitcnt lgkmcnt(1)
	v_add_u32_e32 v85, v88, v85
	v_add_u32_e32 v88, s40, v0
	v_mov_b32_e32 v89, 0
	v_lshl_add_u64 v[88:89], v[88:89], 2, s[60:61]
	ds_write_b32 v38, v85
	global_store_dword v[88:89], v85, off
.LBB1_58:
	s_or_b64 exec, exec, s[38:39]
	s_mov_b32 s41, 0
	s_branch .Licl_s27

.Licl_s27:
	v_cmp_eq_u32_e64 s[38:39], 0, v0
	s_and_saveexec_b64 s[42:43], s[38:39]
	s_cbranch_execz .LBB1_60
	s_lshl_b64 s[38:39], s[40:41], 2
	s_add_u32 s38, s60, s38
	s_addc_u32 s39, s61, s39
	v_mov_b32_e32 v38, 0
	s_waitcnt lgkmcnt(0)
	global_store_dword v38, v87, s[38:39] offset:1564
.LBB1_60:
	s_or_b64 exec, exec, s[42:43]
	s_waitcnt lgkmcnt(0)
	s_barrier
	s_and_saveexec_b64 s[38:39], s[4:5]
	s_cbranch_execnz .LBB1_98
	s_or_b64 exec, exec, s[38:39]
	s_branch .Licl_s28

.Licl_s28:
	s_and_saveexec_b64 s[4:5], s[6:7]
	s_cbranch_execnz .LBB1_99

.LBB1_66:
	s_or_b64 exec, exec, s[4:5]
	s_branch .Licl_s29

.Licl_s29:
	s_and_saveexec_b64 s[4:5], s[16:17]
	s_cbranch_execnz .LBB1_104

.Licl_s30:
	s_and_saveexec_b64 s[4:5], s[26:27]
	s_cbranch_execnz .LBB1_109

.LBB1_76:
	v_and_b32_e32 v2, 0x3fffffc, v83
	s_branch .Licl_s31

.Licl_s31:
	ds_read_b32 v2, v2
	v_and_b32_e32 v3, 0xff, v5
	v_mov_b32_e32 v4, 0x6a0
	v_mad_u32_u24 v3, v3, 3, s64
	v_lshl_or_b32 v3, v3, 17, v9
	s_waitcnt lgkmcnt(0)
	v_add_u32_e32 v2, v76, v2
	v_lshl_add_u32 v5, v2, 2, v4
	v_lshl_add_u32 v2, v2, 1, v4
	v_add_u32_e32 v2, 0x10000, v2
	ds_write_b32 v5, v3
	ds_write_b16 v2, v84
.LBB1_77:
	s_or_b64 exec, exec, s[4:5]
	s_lshl_b32 s4, s2, 14
	s_branch .Licl_s32

.Licl_s32:
	s_mov_b32 s5, 0
	s_waitcnt lgkmcnt(0)
	s_barrier
	s_and_saveexec_b64 s[6:7], vcc
	s_cbranch_execz .LBB1_80
	s_lshl_b64 s[8:9], s[4:5], 2
	s_add_u32 s8, s56, s8
	s_addc_u32 s9, s57, s9
	v_lshl_add_u64 v[2:3], s[8:9], 0, v[34:35]
	s_mov_b64 s[8:9], 0
	s_mov_b64 s[10:11], 0x4000
	v_mov_b32_e32 v4, v0
.LBB1_79:
	ds_read_b128 v[6:9], v1
	v_add_u32_e32 v4, 0x400, v4
	s_branch .Licl_s33

.Licl_s33:
	v_cmp_le_i32_e32 vcc, s33, v4
	v_add_u32_e32 v1, 0x4000, v1
	s_or_b64 s[8:9], vcc, s[8:9]
	s_waitcnt lgkmcnt(0)
	global_store_dwordx4 v[2:3], v[6:9], off
	v_lshl_add_u64 v[2:3], v[2:3], 0, s[10:11]
	s_andn2_b64 exec, exec, s[8:9]
	s_cbranch_execnz .LBB1_79
.LBB1_80:
	s_or_b64 exec, exec, s[6:7]
	s_ashr_i32 s3, s3, 3
	v_cmp_gt_i32_e32 vcc, s3, v0
	s_and_saveexec_b64 s[6:7], vcc
	s_cbranch_execz .LBB1_83
	s_lshl_b64 s[4:5], s[4:5], 1
	s_branch .Licl_s34

.Licl_s34:
	s_add_u32 s4, s58, s4
	s_addc_u32 s5, s59, s5
	v_add_u32_e32 v1, 0x6a0, v34
	v_lshl_add_u64 v[2:3], s[4:5], 0, v[34:35]
	v_add_u32_e32 v1, 0x10000, v1
	s_mov_b64 s[4:5], 0
	s_mov_b64 s[8:9], 0x4000
	v_mov_b32_e32 v4, v0
.LBB1_82:
	ds_read_b128 v[6:9], v1
	v_add_u32_e32 v4, 0x400, v4
	v_cmp_le_i32_e32 vcc, s3, v4
	v_add_u32_e32 v1, 0x4000, v1
	s_or_b64 s[4:5], vcc, s[4:5]
	s_waitcnt lgkmcnt(0)
	s_branch .Licl_s35

.Licl_s35:
	global_store_dwordx4 v[2:3], v[6:9], off
	v_lshl_add_u64 v[2:3], v[2:3], 0, s[8:9]
	s_andn2_b64 exec, exec, s[4:5]
	s_cbranch_execnz .LBB1_82

.LBB1_98:
	v_and_b32_e32 v37, 0x3fffffc, v37
	ds_read_b32 v37, v37
	v_and_b32_e32 v30, 0xff, v30
	v_mad_u32_u24 v30, v30, 3, s64
	v_mov_b32_e32 v38, 0x6a0
	v_lshl_or_b32 v26, v30, 17, v26
	s_waitcnt lgkmcnt(0)
	v_add_u32_e32 v30, v41, v37
	v_lshl_add_u32 v37, v30, 2, v38
	ds_write_b32 v37, v26
	v_lshl_add_u32 v26, v30, 1, v38
	v_add_u32_e32 v26, 0x10000, v26
	ds_write_b16 v26, v39
	s_or_b64 exec, exec, s[38:39]
	s_branch .Licl_s36

.Licl_s36:
	s_and_saveexec_b64 s[4:5], s[6:7]
	s_cbranch_execz .LBB1_62
.LBB1_99:
	v_and_b32_e32 v26, 0x3fffffc, v42
	ds_read_b32 v26, v26
	v_and_b32_e32 v30, 0xff, v31
	v_mov_b32_e32 v31, 0x6a0
	v_mad_u32_u24 v30, v30, 3, s64
	v_lshl_or_b32 v27, v30, 17, v27
	s_waitcnt lgkmcnt(0)
	v_add_u32_e32 v26, v36, v26
	v_lshl_add_u32 v30, v26, 2, v31
	v_lshl_add_u32 v26, v26, 1, v31
	v_add_u32_e32 v26, 0x10000, v26
	ds_write_b32 v30, v27
	s_branch .Licl_s37

.Licl_s37:
	ds_write_b16 v26, v43
	s_or_b64 exec, exec, s[4:5]
	s_and_saveexec_b64 s[4:5], s[8:9]
	s_cbranch_execz .LBB1_63
.LBB1_100:
	v_and_b32_e32 v26, 0x3fffffc, v44
	ds_read_b32 v26, v26
	v_and_b32_e32 v27, 0xff, v32
	v_mov_b32_e32 v30, 0x6a0
	v_mad_u32_u24 v27, v27, 3, s64
	v_lshl_or_b32 v27, v27, 17, v28
	s_waitcnt lgkmcnt(0)
	v_add_u32_e32 v26, v47, v26
	v_lshl_add_u32 v28, v26, 2, v30
	v_lshl_add_u32 v26, v26, 1, v30
	s_branch .Licl_s38

.Licl_s38:
	v_add_u32_e32 v26, 0x10000, v26
	ds_write_b32 v28, v27
	ds_write_b16 v26, v45
	s_or_b64 exec, exec, s[4:5]
	s_and_saveexec_b64 s[4:5], s[10:11]
	s_cbranch_execz .LBB1_64
.LBB1_101:
	v_and_b32_e32 v26, 0x3fffffc, v48
	ds_read_b32 v26, v26
	v_and_b32_e32 v27, 0xff, v33
	v_mov_b32_e32 v28, 0x6a0
	v_mad_u32_u24 v27, v27, 3, s64
	v_lshl_or_b32 v27, v27, 17, v29
	s_waitcnt lgkmcnt(0)
	v_add_u32_e32 v26, v40, v26
	s_branch .Licl_s39

.Licl_s39:
	v_lshl_add_u32 v29, v26, 2, v28
	v_lshl_add_u32 v26, v26, 1, v28
	v_add_u32_e32 v26, 0x10000, v26
	ds_write_b32 v29, v27
	ds_write_b16 v26, v49
	s_or_b64 exec, exec, s[4:5]
	s_and_saveexec_b64 s[4:5], s[12:13]
	s_cbranch_execz .LBB1_65
.LBB1_102:
	v_and_b32_e32 v26, 0x3fffffc, v50
	ds_read_b32 v26, v26
	v_and_b32_e32 v10, 0xff, v10
	v_mad_u32_u24 v10, v10, 3, s64
	v_mov_b32_e32 v27, 0x6a0
	v_lshl_or_b32 v10, v10, 17, v14
	s_branch .Licl_s40

.Licl_s40:
	s_waitcnt lgkmcnt(0)
	v_add_u32_e32 v14, v53, v26
	v_lshl_add_u32 v26, v14, 2, v27
	ds_write_b32 v26, v10
	v_lshl_add_u32 v10, v14, 1, v27
	v_add_u32_e32 v10, 0x10000, v10
	ds_write_b16 v10, v51
	s_or_b64 exec, exec, s[4:5]
	s_and_saveexec_b64 s[4:5], s[14:15]
	s_cbranch_execz .LBB1_66
.LBB1_103:
	v_and_b32_e32 v10, 0x3fffffc, v54
	ds_read_b32 v10, v10
	v_and_b32_e32 v11, 0xff, v11
	v_mov_b32_e32 v14, 0x6a0
	s_branch .Licl_s41

.Licl_s41:
	v_mad_u32_u24 v11, v11, 3, s64
	v_lshl_or_b32 v11, v11, 17, v15
	s_waitcnt lgkmcnt(0)
	v_add_u32_e32 v10, v46, v10
	v_lshl_add_u32 v15, v10, 2, v14
	v_lshl_add_u32 v10, v10, 1, v14
	v_add_u32_e32 v10, 0x10000, v10
	ds_write_b32 v15, v11
	ds_write_b16 v10, v55
	s_or_b64 exec, exec, s[4:5]
	s_and_saveexec_b64 s[4:5], s[16:17]
	s_cbranch_execz .LBB1_67
.LBB1_104:
	v_and_b32_e32 v10, 0x3fffffc, v56
	ds_read_b32 v10, v10
	s_branch .Licl_s42

.Licl_s42:
	v_and_b32_e32 v11, 0xff, v12
	v_mov_b32_e32 v12, 0x6a0
	v_mad_u32_u24 v11, v11, 3, s64
	v_lshl_or_b32 v11, v11, 17, v16
	s_waitcnt lgkmcnt(0)
	v_add_u32_e32 v10, v59, v10
	v_lshl_add_u32 v14, v10, 2, v12
	v_lshl_add_u32 v10, v10, 1, v12
	v_add_u32_e32 v10, 0x10000, v10
	ds_write_b32 v14, v11
	ds_write_b16 v10, v57
	s_or_b64 exec, exec, s[4:5]
	s_and_saveexec_b64 s[4:5], s[18:19]
	s_cbranch_execz .LBB1_68
.LBB1_105:
	v_and_b32_e32 v10, 0x3fffffc, v60
	s_branch .Licl_s43

.Licl_s43:
	ds_read_b32 v10, v10
	v_and_b32_e32 v11, 0xff, v13
	v_mov_b32_e32 v12, 0x6a0
	v_mad_u32_u24 v11, v11, 3, s64
	v_lshl_or_b32 v11, v11, 17, v17
	s_waitcnt lgkmcnt(0)
	v_add_u32_e32 v10, v52, v10
	v_lshl_add_u32 v13, v10, 2, v12
	v_lshl_add_u32 v10, v10, 1, v12
	v_add_u32_e32 v10, 0x10000, v10
	ds_write_b32 v13, v11
	ds_write_b16 v10, v61
	s_or_b64 exec, exec, s[4:5]
	s_and_saveexec_b64 s[4:5], s[20:21]
	s_branch .Licl_s44

.LBB1_106:
	v_and_b32_e32 v10, 0x3fffffc, v62
	ds_read_b32 v10, v10
	v_and_b32_e32 v11, 0xff, v22
	v_mov_b32_e32 v12, 0x6a0
	v_mad_u32_u24 v11, v11, 3, s64
	v_lshl_or_b32 v11, v11, 17, v18
	s_waitcnt lgkmcnt(0)
	v_add_u32_e32 v10, v65, v10
	v_lshl_add_u32 v13, v10, 2, v12
	v_lshl_add_u32 v10, v10, 1, v12
	v_add_u32_e32 v10, 0x10000, v10
	ds_write_b32 v13, v11
	ds_write_b16 v10, v63
	s_branch .Licl_s45

.Licl_s45:
	s_or_b64 exec, exec, s[4:5]
	s_and_saveexec_b64 s[4:5], s[22:23]
	s_cbranch_execz .LBB1_70
.LBB1_107:
	v_and_b32_e32 v10, 0x3fffffc, v66
	ds_read_b32 v10, v10
	v_and_b32_e32 v11, 0xff, v23
	v_mov_b32_e32 v12, 0x6a0
	v_mad_u32_u24 v11, v11, 3, s64
	v_lshl_or_b32 v11, v11, 17, v19
	s_waitcnt lgkmcnt(0)
	v_add_u32_e32 v10, v58, v10
	v_lshl_add_u32 v13, v10, 2, v12
	v_lshl_add_u32 v10, v10, 1, v12
	v_add_u32_e32 v10, 0x10000, v10
	s_branch .Licl_s46

.Licl_s46:
	ds_write_b32 v13, v11
	ds_write_b16 v10, v67
	s_or_b64 exec, exec, s[4:5]
	s_and_saveexec_b64 s[4:5], s[24:25]
	s_cbranch_execz .LBB1_71
.LBB1_108:
	v_and_b32_e32 v10, 0x3fffffc, v68
	ds_read_b32 v10, v10
	v_and_b32_e32 v11, 0xff, v24
	v_mov_b32_e32 v12, 0x6a0
	v_mad_u32_u24 v11, v11, 3, s64
	v_lshl_or_b32 v11, v11, 17, v20
	s_waitcnt lgkmcnt(0)
	v_add_u32_e32 v10, v71, v10
	v_lshl_add_u32 v13, v10, 2, v12
	s_branch .Licl_s47

.Licl_s47:
	v_lshl_add_u32 v10, v10, 1, v12
	v_add_u32_e32 v10, 0x10000, v10
	ds_write_b32 v13, v11
	ds_write_b16 v10, v69
	s_or_b64 exec, exec, s[4:5]
	s_and_saveexec_b64 s[4:5], s[26:27]
	s_cbranch_execz .LBB1_72
.LBB1_109:
	v_and_b32_e32 v10, 0x3fffffc, v72
	ds_read_b32 v10, v10
	v_and_b32_e32 v11, 0xff, v25
	v_mov_b32_e32 v12, 0x6a0
	v_mad_u32_u24 v11, v11, 3, s64
	v_lshl_or_b32 v11, v11, 17, v21
	s_waitcnt lgkmcnt(0)
	s_branch .Licl_s48

.Licl_s48:
	v_add_u32_e32 v10, v64, v10
	v_lshl_add_u32 v13, v10, 2, v12
	v_lshl_add_u32 v10, v10, 1, v12
	v_add_u32_e32 v10, 0x10000, v10
	ds_write_b32 v13, v11
	ds_write_b16 v10, v73
	s_or_b64 exec, exec, s[4:5]
	s_and_saveexec_b64 s[4:5], s[28:29]
	s_cbranch_execz .LBB1_73
.LBB1_110:
	v_and_b32_e32 v10, 0x3fffffc, v74
	ds_read_b32 v10, v10
	v_and_b32_e32 v2, 0xff, v2
	v_mad_u32_u24 v2, v2, 3, s64
	v_mov_b32_e32 v11, 0x6a0
	s_branch .Licl_s49

.Licl_s49:
	v_lshl_or_b32 v2, v2, 17, v6
	s_waitcnt lgkmcnt(0)
	v_add_u32_e32 v6, v77, v10
	v_lshl_add_u32 v10, v6, 2, v11
	ds_write_b32 v10, v2
	v_lshl_add_u32 v2, v6, 1, v11
	v_add_u32_e32 v2, 0x10000, v2
	ds_write_b16 v2, v75
	s_or_b64 exec, exec, s[4:5]
	s_and_saveexec_b64 s[4:5], s[30:31]
	s_cbranch_execz .LBB1_74
.LBB1_111:
	v_and_b32_e32 v2, 0x3fffffc, v78
	ds_read_b32 v2, v2
	v_and_b32_e32 v3, 0xff, v3
	s_branch .Licl_s50

.Licl_s50:
	v_mov_b32_e32 v6, 0x6a0
	v_mad_u32_u24 v3, v3, 3, s64
	v_lshl_or_b32 v3, v3, 17, v7
	s_waitcnt lgkmcnt(0)
	v_add_u32_e32 v2, v70, v2
	v_lshl_add_u32 v7, v2, 2, v6
	v_lshl_add_u32 v2, v2, 1, v6
	v_add_u32_e32 v2, 0x10000, v2
	ds_write_b32 v7, v3
	ds_write_b16 v2, v79
	s_or_b64 exec, exec, s[4:5]
	s_and_saveexec_b64 s[4:5], s[34:35]
	s_cbranch_execz .LBB1_75

.LBB2_2:
	s_or_b64 exec, exec, s[4:5]
	v_readfirstlane_b32 s70, v0
	s_lshr_b32 s70, s70, 6
	s_cmp_eq_u32 s70, 4
	s_cbranch_scc1 .Licb_t0
	s_cmp_eq_u32 s70, 5
	s_cbranch_scc1 .Licb_t1
	s_cmp_eq_u32 s70, 6
	s_cbranch_scc1 .Licb_t2
	s_cmp_eq_u32 s70, 7
	s_cbranch_scc1 .Licb_t3
	s_cmp_eq_u32 s70, 8
	s_cbranch_scc1 .Licb_t4
	s_cmp_eq_u32 s70, 9
	s_cbranch_scc1 .Licb_t5
	s_cmp_eq_u32 s70, 10
	s_cbranch_scc1 .Licb_t6
	s_cmp_eq_u32 s70, 11
	s_cbranch_scc1 .Licb_t7
	s_cmp_eq_u32 s70, 12
	s_cbranch_scc1 .Licb_t8
	s_cmp_eq_u32 s70, 13
	s_cbranch_scc1 .Licb_t9
	s_cmp_eq_u32 s70, 14
	s_cbranch_scc1 .Licb_t10
	s_cmp_eq_u32 s70, 15
	s_cbranch_scc1 .Licb_t11
.Licb_done:
	s_movk_i32 s3, 0x300
	v_cmp_gt_u32_e32 vcc, s3, v0
	s_and_saveexec_b64 s[4:5], vcc
	v_lshlrev_b32_e32 v1, 2, v0
	v_mov_b32_e32 v2, 0
	ds_write_b32 v1, v2 offset:49152
	s_or_b64 exec, exec, s[4:5]
	s_load_dwordx4 s[56:59], s[0:1], 0x0
	s_load_dwordx4 s[52:55], s[0:1], 0x18
	v_mbcnt_lo_u32_b32 v1, -1, 0
	v_mbcnt_hi_u32_b32 v1, -1, v1
	v_and_b32_e32 v2, 63, v0
	v_add_u32_dpp v4, v4, v4 quad_perm:[1,0,3,2] row_mask:0xf bank_mask:0xf
	s_branch .Licb_s0

.Licb_s0:
	v_add_u32_dpp v5, v5, v5 quad_perm:[1,0,3,2] row_mask:0xf bank_mask:0xf
	v_cmp_eq_u32_e64 s[46:47], 0, v2
	v_cmp_gt_u32_e64 s[4:5], 2, v2
	v_add_u32_dpp v4, v4, v4 quad_perm:[2,3,0,1] row_mask:0xf bank_mask:0xf
	v_add_u32_dpp v5, v5, v5 quad_perm:[2,3,0,1] row_mask:0xf bank_mask:0xf
	v_cmp_gt_u32_e64 s[8:9], 4, v2
	v_cmp_gt_u32_e64 s[6:7], 8, v2
	v_add_u32_dpp v4, v4, v4 row_half_mirror row_mask:0xf bank_mask:0xf
	v_add_u32_dpp v5, v5, v5 row_half_mirror row_mask:0xf bank_mask:0xf
	v_cmp_gt_u32_e64 s[10:11], 16, v2
	v_cmp_gt_u32_e64 s[18:19], 32, v2
	v_add_u32_dpp v4, v4, v4 row_mirror row_mask:0xf bank_mask:0xf
	v_add_u32_dpp v5, v5, v5 row_mirror row_mask:0xf bank_mask:0xf
	v_cmp_eq_u32_e64 s[14:15], 63, v2
	s_branch .Licb_s1

.Licb_s1:
	v_add_u32_e32 v3, -1, v1
	v_cndmask_b32_e64 v3, v3, v1, s[46:47]
	v_lshlrev_b32_e32 v3, 2, v3
	v_readlane_b32 s20, v4, 0
	v_readlane_b32 s21, v4, 16
	v_readlane_b32 s22, v4, 32
	v_readlane_b32 s23, v4, 48
	v_readlane_b32 s24, v5, 0
	v_readlane_b32 s25, v5, 16
	v_readlane_b32 s26, v5, 32
	v_readlane_b32 s27, v5, 48
	v_add_u32_e32 v6, -2, v1
	v_cndmask_b32_e64 v6, v6, v1, s[4:5]
	v_lshlrev_b32_e32 v6, 2, v6
	s_branch .Licb_s2

.Licb_s2:
	v_add_u32_e32 v7, -4, v1
	v_cndmask_b32_e64 v7, v7, v1, s[8:9]
	v_lshlrev_b32_e32 v7, 2, v7
	v_add_u32_e32 v40, -8, v1
	v_cndmask_b32_e64 v40, v40, v1, s[6:7]
	v_lshlrev_b32_e32 v40, 2, v40
	v_add_u32_e32 v43, -16, v1
	v_cndmask_b32_e64 v43, v43, v1, s[10:11]
	v_lshlrev_b32_e32 v43, 2, v43
	v_subrev_u32_e32 v44, 32, v1
	v_cndmask_b32_e64 v44, v44, v1, s[18:19]
	v_lshlrev_b32_e32 v44, 2, v44
	s_add_i32 s20, s20, s21
	s_add_i32 s22, s22, s23
	s_branch .Licb_s3

.Licb_s3:
	s_add_i32 s20, s20, s22
	s_add_i32 s24, s24, s25
	s_add_i32 s26, s26, s27
	s_add_i32 s24, s24, s26
	v_lshrrev_b32_e32 v1, 6, v0
	v_lshlrev_b32_e32 v8, 2, v1
	v_lshlrev_b32_e32 v9, 3, v1
	v_mov_b32_e32 v10, s20
	v_mov_b32_e32 v11, s24
	s_and_saveexec_b64 s[18:19], s[46:47]
	ds_write_b64 v9, v[10:11] offset:54016
	v_mov_b32_e32 v12, 0
	ds_write_b32 v12, v12 offset:54144
	s_mov_b64 exec, s[18:19]
	s_branch .Licb_s4

.Licb_s4:
	v_cmp_lt_u32_e64 s[12:13], 63, v0
	v_cmp_gt_u32_e64 s[16:17], 64, v0
	v_mov_b32_e32 v39, 0
	s_waitcnt lgkmcnt(0)
	s_barrier
	ds_read_b128 v[10:13], v39 offset:54016
	ds_read_b128 v[14:17], v39 offset:54032
	s_waitcnt lgkmcnt(0)
	v_add_u32_e32 v4, v10, v12
	v_add_u32_e32 v5, v11, v13
	v_add3_u32 v4, v4, v14, v16
	v_add3_u32 v5, v5, v15, v17
	s_nop 0
	v_readfirstlane_b32 s50, v4
	s_branch .Licb_s5

.Licb_s5:
	v_readfirstlane_b32 s33, v5
	ds_read_b32 v53, v8 offset:53120
	v_or_b32_e32 v9, 0xcf80, v8
	v_mov_b32_e32 v47, 0
	v_mov_b32_e32 v46, 0
	s_waitcnt lgkmcnt(0)
	v_cmp_lt_i32_e64 s[44:45], v2, v53
	s_and_saveexec_b64 s[0:1], s[44:45]
	s_cbranch_execz .LBB2_20
	ds_read_b32 v4, v8 offset:52224
	v_lshl_or_b32 v10, v1, 14, v2
	v_mov_b32_e32 v11, 0
	s_waitcnt lgkmcnt(0)
	v_ashrrev_i32_e32 v5, 31, v4
	s_branch .Licb_s6

.Licb_s6:
	v_lshl_add_u64 v[4:5], v[10:11], 0, v[4:5]
	v_lshl_add_u64 v[10:11], v[4:5], 2, s[56:57]
	v_lshl_add_u64 v[4:5], v[4:5], 1, s[58:59]
	global_load_dword v46, v[10:11], off nt
	global_load_ushort v47, v[4:5], off nt
.LBB2_20:
	s_or_b64 exec, exec, s[0:1]
	ds_read_b32 v52, v9 offset:64
	v_lshlrev_b32_e32 v4, 14, v1
	v_mov_b32_e32 v41, 0
	s_waitcnt lgkmcnt(0)
	v_cmp_lt_i32_e64 s[42:43], v2, v52
	s_and_saveexec_b64 s[0:1], s[42:43]
	s_cbranch_execz .LBB2_22
	ds_read_b32 v10, v8 offset:52288
	s_branch .Licb_s7

.Licb_s7:
	s_mov_b32 s3, 0x40000
	v_mov_b32_e32 v13, 0
	v_or3_b32 v12, v4, v2, s3
	s_waitcnt lgkmcnt(0)
	v_ashrrev_i32_e32 v11, 31, v10
	v_lshl_add_u64 v[10:11], v[12:13], 0, v[10:11]
	v_lshl_add_u64 v[12:13], v[10:11], 2, s[56:57]
	v_lshl_add_u64 v[10:11], v[10:11], 1, s[58:59]
	global_load_dword v41, v[12:13], off nt
	global_load_ushort v39, v[10:11], off nt
.LBB2_22:
	s_or_b64 exec, exec, s[0:1]
	ds_read_b32 v51, v9 offset:128
	v_mov_b32_e32 v32, 0
	v_mov_b32_e32 v37, 0
	s_branch .Licb_s8

.Licb_s8:
	v_mov_b32_e32 v36, 0
	s_waitcnt lgkmcnt(0)
	v_cmp_lt_i32_e64 s[40:41], v2, v51
	s_and_saveexec_b64 s[0:1], s[40:41]
	s_cbranch_execz .LBB2_24
	ds_read_b32 v10, v8 offset:52352
	s_mov_b32 s3, 0x80000
	v_mov_b32_e32 v13, 0
	v_or3_b32 v12, v4, v2, s3
	s_waitcnt lgkmcnt(0)
	v_ashrrev_i32_e32 v11, 31, v10
	v_lshl_add_u64 v[10:11], v[12:13], 0, v[10:11]
	v_lshl_add_u64 v[12:13], v[10:11], 2, s[56:57]
	v_lshl_add_u64 v[10:11], v[10:11], 1, s[58:59]
	s_branch .Licb_s9

.Licb_s9:
	global_load_dword v36, v[12:13], off nt
	global_load_ushort v37, v[10:11], off nt
.LBB2_24:
	s_or_b64 exec, exec, s[0:1]
	ds_read_b32 v50, v9 offset:192
	v_mov_b32_e32 v34, 0
	s_waitcnt lgkmcnt(0)
	v_cmp_lt_i32_e64 s[38:39], v2, v50
	s_and_saveexec_b64 s[0:1], s[38:39]
	s_cbranch_execz .LBB2_26
	ds_read_b32 v10, v8 offset:52416
	s_mov_b32 s3, 0xc0000
	v_mov_b32_e32 v13, 0
	v_or3_b32 v12, v4, v2, s3
	s_waitcnt lgkmcnt(0)
	s_branch .Licb_s10

.Licb_s10:
	v_ashrrev_i32_e32 v11, 31, v10
	v_lshl_add_u64 v[10:11], v[12:13], 0, v[10:11]
	v_lshl_add_u64 v[12:13], v[10:11], 2, s[56:57]
	v_lshl_add_u64 v[10:11], v[10:11], 1, s[58:59]
	global_load_dword v34, v[12:13], off nt
	global_load_ushort v32, v[10:11], off nt
.LBB2_26:
	s_or_b64 exec, exec, s[0:1]
	ds_read_b32 v49, v9 offset:256
	v_mov_b32_e32 v27, 0
	v_mov_b32_e32 v30, 0
	v_mov_b32_e32 v29, 0
	s_waitcnt lgkmcnt(0)
	v_cmp_lt_i32_e64 s[36:37], v2, v49
	s_and_saveexec_b64 s[0:1], s[36:37]
	s_branch .Licb_s11

.Licb_s11:
	s_cbranch_execz .LBB2_28
	ds_read_b32 v10, v8 offset:52480
	s_mov_b32 s3, 0x100000
	v_mov_b32_e32 v13, 0
	v_or3_b32 v12, v4, v2, s3
	s_waitcnt lgkmcnt(0)
	v_ashrrev_i32_e32 v11, 31, v10
	v_lshl_add_u64 v[10:11], v[12:13], 0, v[10:11]
	v_lshl_add_u64 v[12:13], v[10:11], 2, s[56:57]
	v_lshl_add_u64 v[10:11], v[10:11], 1, s[58:59]
	global_load_dword v29, v[12:13], off nt
	global_load_ushort v30, v[10:11], off nt
.LBB2_28:
	s_or_b64 exec, exec, s[0:1]
	ds_read_b32 v48, v9 offset:320
	s_branch .Licb_s12

.Licb_s12:
	v_mov_b32_e32 v28, 0
	s_waitcnt lgkmcnt(0)
	v_cmp_lt_i32_e64 s[34:35], v2, v48
	s_and_saveexec_b64 s[0:1], s[34:35]
	s_cbranch_execz .LBB2_30
	ds_read_b32 v10, v8 offset:52544
	s_mov_b32 s3, 0x140000
	v_mov_b32_e32 v13, 0
	v_or3_b32 v12, v4, v2, s3
	s_waitcnt lgkmcnt(0)
	v_ashrrev_i32_e32 v11, 31, v10
	v_lshl_add_u64 v[10:11], v[12:13], 0, v[10:11]
	v_lshl_add_u64 v[12:13], v[10:11], 2, s[56:57]
	v_lshl_add_u64 v[10:11], v[10:11], 1, s[58:59]
	s_branch .Licb_s13

.Licb_s13:
	global_load_dword v28, v[12:13], off nt
	global_load_ushort v27, v[10:11], off nt
.LBB2_30:
	s_or_b64 exec, exec, s[0:1]
	ds_read_b32 v45, v9 offset:384
	v_mov_b32_e32 v23, 0
	v_mov_b32_e32 v26, 0
	v_mov_b32_e32 v25, 0
	s_waitcnt lgkmcnt(0)
	v_cmp_lt_i32_e64 s[30:31], v2, v45
	s_and_saveexec_b64 s[0:1], s[30:31]
	s_cbranch_execz .LBB2_32
	ds_read_b32 v10, v8 offset:52608
	s_mov_b32 s3, 0x180000
	v_mov_b32_e32 v13, 0
	s_branch .Licb_s14

.Licb_s14:
	v_or3_b32 v12, v4, v2, s3
	s_waitcnt lgkmcnt(0)
	v_ashrrev_i32_e32 v11, 31, v10
	v_lshl_add_u64 v[10:11], v[12:13], 0, v[10:11]
	v_lshl_add_u64 v[12:13], v[10:11], 2, s[56:57]
	v_lshl_add_u64 v[10:11], v[10:11], 1, s[58:59]
	global_load_dword v25, v[12:13], off nt
	global_load_ushort v26, v[10:11], off nt
.LBB2_32:
	s_or_b64 exec, exec, s[0:1]
	ds_read_b32 v42, v9 offset:448
	v_mov_b32_e32 v24, 0
	s_waitcnt lgkmcnt(0)
	v_cmp_lt_i32_e64 s[28:29], v2, v42
	s_and_saveexec_b64 s[0:1], s[28:29]
	s_branch .Licb_s15

.Licb_s15:
	s_cbranch_execz .LBB2_34
	ds_read_b32 v10, v8 offset:52672
	s_mov_b32 s3, 0x1c0000
	v_mov_b32_e32 v13, 0
	v_or3_b32 v12, v4, v2, s3
	s_waitcnt lgkmcnt(0)
	v_ashrrev_i32_e32 v11, 31, v10
	v_lshl_add_u64 v[10:11], v[12:13], 0, v[10:11]
	v_lshl_add_u64 v[12:13], v[10:11], 2, s[56:57]
	v_lshl_add_u64 v[10:11], v[10:11], 1, s[58:59]
	global_load_dword v24, v[12:13], off nt
	global_load_ushort v23, v[10:11], off nt
.LBB2_34:
	s_or_b64 exec, exec, s[0:1]
	ds_read_b32 v38, v9 offset:512
	s_branch .Licb_s16

.Licb_s16:
	v_mov_b32_e32 v19, 0
	v_mov_b32_e32 v22, 0
	v_mov_b32_e32 v21, 0
	s_waitcnt lgkmcnt(0)
	v_cmp_lt_i32_e64 s[26:27], v2, v38
	s_and_saveexec_b64 s[0:1], s[26:27]
	s_cbranch_execz .LBB2_36
	ds_read_b32 v10, v8 offset:52736
	s_mov_b32 s3, 0x200000
	v_mov_b32_e32 v13, 0
	v_or3_b32 v12, v4, v2, s3
	s_waitcnt lgkmcnt(0)
	v_ashrrev_i32_e32 v11, 31, v10
	v_lshl_add_u64 v[10:11], v[12:13], 0, v[10:11]
	s_branch .Licb_s17

.Licb_s17:
	v_lshl_add_u64 v[12:13], v[10:11], 2, s[56:57]
	v_lshl_add_u64 v[10:11], v[10:11], 1, s[58:59]
	global_load_dword v21, v[12:13], off nt
	global_load_ushort v22, v[10:11], off nt
.LBB2_36:
	s_or_b64 exec, exec, s[0:1]
	ds_read_b32 v35, v9 offset:576
	v_mov_b32_e32 v20, 0
	s_waitcnt lgkmcnt(0)
	v_cmp_lt_i32_e64 s[24:25], v2, v35
	s_and_saveexec_b64 s[0:1], s[24:25]
	s_cbranch_execz .LBB2_38
	ds_read_b32 v10, v8 offset:52800
	s_mov_b32 s3, 0x240000
	v_mov_b32_e32 v13, 0
	s_branch .Licb_s18

.Licb_s18:
	v_or3_b32 v12, v4, v2, s3
	s_waitcnt lgkmcnt(0)
	v_ashrrev_i32_e32 v11, 31, v10
	v_lshl_add_u64 v[10:11], v[12:13], 0, v[10:11]
	v_lshl_add_u64 v[12:13], v[10:11], 2, s[56:57]
	v_lshl_add_u64 v[10:11], v[10:11], 1, s[58:59]
	global_load_dword v20, v[12:13], off nt
	global_load_ushort v19, v[10:11], off nt
.LBB2_38:
	s_or_b64 exec, exec, s[0:1]
	ds_read_b32 v33, v9 offset:640
	v_mov_b32_e32 v15, 0
	v_mov_b32_e32 v18, 0
	v_mov_b32_e32 v17, 0
	s_waitcnt lgkmcnt(0)
	s_branch .Licb_s19

.Licb_s19:
	v_cmp_lt_i32_e64 s[22:23], v2, v33
	s_and_saveexec_b64 s[0:1], s[22:23]
	s_cbranch_execz .LBB2_40
	ds_read_b32 v10, v8 offset:52864
	s_mov_b32 s3, 0x280000
	v_mov_b32_e32 v13, 0
	v_or3_b32 v12, v4, v2, s3
	s_waitcnt lgkmcnt(0)
	v_ashrrev_i32_e32 v11, 31, v10
	v_lshl_add_u64 v[10:11], v[12:13], 0, v[10:11]
	v_lshl_add_u64 v[12:13], v[10:11], 2, s[56:57]
	v_lshl_add_u64 v[10:11], v[10:11], 1, s[58:59]
	global_load_dword v17, v[12:13], off nt
	global_load_ushort v18, v[10:11], off nt
.LBB2_40:
	s_or_b64 exec, exec, s[0:1]
	s_branch .Licb_s20

.Licb_s20:
	ds_read_b32 v31, v9 offset:704
	v_mov_b32_e32 v16, 0
	s_waitcnt lgkmcnt(0)
	v_cmp_lt_i32_e64 s[20:21], v2, v31
	s_and_saveexec_b64 s[0:1], s[20:21]
	s_cbranch_execz .LBB2_42
	ds_read_b32 v10, v8 offset:52928
	s_mov_b32 s3, 0x2c0000
	v_mov_b32_e32 v13, 0
	v_or3_b32 v12, v4, v2, s3
	s_waitcnt lgkmcnt(0)
	v_ashrrev_i32_e32 v11, 31, v10
	v_lshl_add_u64 v[10:11], v[12:13], 0, v[10:11]
	v_lshl_add_u64 v[12:13], v[10:11], 2, s[56:57]
	s_branch .Licb_s21

.Licb_s21:
	v_lshl_add_u64 v[10:11], v[10:11], 1, s[58:59]
	global_load_dword v16, v[12:13], off nt
	global_load_ushort v15, v[10:11], off nt
.LBB2_42:
	s_or_b64 exec, exec, s[0:1]
	ds_read_b32 v55, v9 offset:768
	v_mov_b32_e32 v11, 0
	v_mov_b32_e32 v14, 0
	v_mov_b32_e32 v13, 0
	s_waitcnt lgkmcnt(0)
	v_cmp_lt_i32_e64 s[18:19], v2, v55
	s_and_saveexec_b64 s[0:1], s[18:19]
	s_cbranch_execz .LBB2_44
	ds_read_b32 v12, v8 offset:52992
	s_mov_b32 s3, 0x300000
	s_branch .Licb_s22

.Licb_s22:
	v_mov_b32_e32 v5, 0
	v_or3_b32 v4, v4, v2, s3
	s_waitcnt lgkmcnt(0)
	v_ashrrev_i32_e32 v13, 31, v12
	v_lshl_add_u64 v[4:5], v[4:5], 0, v[12:13]
	v_lshl_add_u64 v[12:13], v[4:5], 2, s[56:57]
	v_lshl_add_u64 v[4:5], v[4:5], 1, s[58:59]
	global_load_dword v13, v[12:13], off nt
	s_nop 0
	global_load_ushort v14, v[4:5], off nt
.LBB2_44:
	s_or_b64 exec, exec, s[0:1]
	v_or_b32_e32 v4, 0xd0, v1
	s_movk_i32 s0, 0xde
	v_cmp_gt_u32_e64 s[0:1], s0, v4
	s_branch .Licb_s23

.Licb_s23:
	v_mov_b32_e32 v12, 0
	s_and_saveexec_b64 s[60:61], s[0:1]
	s_cbranch_execz .LBB2_48
	ds_read_b32 v5, v9 offset:832
	v_mov_b32_e32 v12, 0
	v_mov_b32_e32 v11, 0
	s_waitcnt lgkmcnt(0)
	v_cmp_lt_i32_e64 s[48:49], v2, v5
	s_and_saveexec_b64 s[62:63], s[48:49]
	s_cbranch_execz .LBB2_47
	ds_read_b32 v10, v8 offset:53056
	v_lshl_or_b32 v4, v4, 14, v2
	v_mov_b32_e32 v5, 0
	s_waitcnt lgkmcnt(0)
	s_branch .Licb_s24

.Licb_s24:
	v_ashrrev_i32_e32 v11, 31, v10
	v_lshl_add_u64 v[4:5], v[4:5], 0, v[10:11]
	v_lshl_add_u64 v[10:11], v[4:5], 2, s[56:57]
	v_lshl_add_u64 v[4:5], v[4:5], 1, s[58:59]
	global_load_dword v12, v[10:11], off nt
	s_nop 0
	global_load_ushort v11, v[4:5], off nt

.LBB2_48:
	s_or_b64 exec, exec, s[60:61]
	s_and_b64 s[48:49], s[48:49], s[0:1]
	s_cmpk_gt_i32 s33, 0x3000
	s_cbranch_scc1 .Lbs_cnt_slow
	s_mov_b32 s71, 0
	s_cmp_eq_u64 s[44:45], -1
	s_branch .Licb_s25

.Licb_s25:
	s_cselect_b32 s70, 0x1, 0
	s_or_b32 s71, s71, s70
	s_cmp_eq_u64 s[42:43], -1
	s_cselect_b32 s70, 0x2, 0
	s_or_b32 s71, s71, s70
	s_cmp_eq_u64 s[40:41], -1
	s_cselect_b32 s70, 0x4, 0
	s_or_b32 s71, s71, s70
	s_cmp_eq_u64 s[38:39], -1
	s_cselect_b32 s70, 0x8, 0
	s_or_b32 s71, s71, s70
	s_cmp_eq_u64 s[36:37], -1
	s_cselect_b32 s70, 0x10, 0
	s_or_b32 s71, s71, s70
	s_branch .Licb_s26

.Licb_s26:
	s_cmp_eq_u64 s[34:35], -1
	s_cselect_b32 s70, 0x20, 0
	s_or_b32 s71, s71, s70
	s_cmp_eq_u64 s[30:31], -1
	s_cselect_b32 s70, 0x40, 0
	s_or_b32 s71, s71, s70
	s_cmp_eq_u64 s[28:29], -1
	s_cselect_b32 s70, 0x80, 0
	s_or_b32 s71, s71, s70
	s_cmp_eq_u64 s[26:27], -1
	s_cselect_b32 s70, 0x100, 0
	s_or_b32 s71, s71, s70
	s_cmp_eq_u64 s[24:25], -1
	s_cselect_b32 s70, 0x200, 0
	s_branch .Licb_s27

.Licb_s27:
	s_or_b32 s71, s71, s70
	s_cmp_eq_u64 s[22:23], -1
	s_cselect_b32 s70, 0x400, 0
	s_or_b32 s71, s71, s70
	s_cmp_eq_u64 s[20:21], -1
	s_cselect_b32 s70, 0x800, 0
	s_or_b32 s71, s71, s70
	s_cmp_eq_u64 s[18:19], -1
	s_cselect_b32 s70, 0x1000, 0
	s_or_b32 s71, s71, s70
	s_cmp_eq_u64 s[48:49], -1
	s_cselect_b32 s70, 0x2000, 0
	s_or_b32 s71, s71, s70
	s_mov_b64 s[60:61], s[18:19]
	s_branch .Licb_s28

.Licb_s28:
	s_mov_b64 s[78:79], 0
	s_mov_b64 s[80:81], 0
	s_mov_b64 s[6:7], exec
	s_cmp_eq_u32 s71, 0
	s_cbranch_scc1 .Lbs_fast_go
	s_ff1_i32_b32 s72, s71
	s_bitset0_b32 s71, s72
	s_lshl_b32 s73, s72, 6
	v_add_u32_e32 v58, s73, v9
	ds_read_b32 v57, v58
	v_add_u32_e32 v58, s73, v8
	ds_read_b32 v56, v58 offset:52224
	v_or_b32_e32 v58, 64, v2
	s_waitcnt lgkmcnt(0)
	s_branch .Licb_s29

.Licb_s29:
	v_readfirstlane_b32 s74, v57
	s_cmpk_gt_i32 s74, 0x80
	s_cbranch_scc1 .Lbs_cnt_slow_w
	v_cmp_lt_u32_e64 s[78:79], v58, v57
	v_add_u32_e32 v56, v56, v2
	v_lshlrev_b32_e32 v58, 10, v0
	v_and_b32_e32 v58, 0xf0000, v58
	s_lshl_b32 s73, s72, 20
	v_lshl_add_u32 v56, v56, 2, v58
	v_add_u32_e32 v58, s73, v56
	v_lshrrev_b32_e32 v57, 1, v58
	s_and_b64 exec, s[6:7], s[78:79]
	global_load_dword v56, v58, s[56:57] offset:256 nt
	global_load_ushort v57, v57, s[58:59] offset:128 nt
	s_branch .Licb_s30

.Licb_s30:
	s_mov_b64 exec, s[6:7]
	s_cmp_eq_u32 s71, 0
	s_cbranch_scc1 .Lbs_fast_go
	s_ff1_i32_b32 s72, s71
	s_bitset0_b32 s71, s72
	s_cmp_lg_u32 s71, 0
	s_cbranch_scc1 .Lbs_cnt_slow_w
	s_lshl_b32 s73, s72, 6
	v_add_u32_e32 v61, s73, v9
	ds_read_b32 v60, v61
	v_add_u32_e32 v61, s73, v8
	ds_read_b32 v59, v61 offset:52224
	v_or_b32_e32 v61, 64, v2
	s_waitcnt lgkmcnt(0)
	s_branch .Licb_s31

.Licb_s31:
	v_readfirstlane_b32 s74, v60
	s_cmpk_gt_i32 s74, 0x80
	s_cbranch_scc1 .Lbs_cnt_slow_w
	v_cmp_lt_u32_e64 s[80:81], v61, v60
	v_add_u32_e32 v59, v59, v2
	v_lshlrev_b32_e32 v61, 10, v0
	v_and_b32_e32 v61, 0xf0000, v61
	s_lshl_b32 s73, s72, 20
	v_lshl_add_u32 v59, v59, 2, v61
	v_add_u32_e32 v61, s73, v59
	v_lshrrev_b32_e32 v60, 1, v61
	s_and_b64 exec, s[6:7], s[80:81]
	global_load_dword v59, v61, s[56:57] offset:256 nt
	global_load_ushort v60, v60, s[58:59] offset:128 nt
	s_branch .Licb_s32
.Licb_t32:
	s_branch .Licb_t44
.Licb_s32:
	s_mov_b64 exec, s[6:7]
.Lbs_fast_go:
	s_waitcnt vmcnt(0)
	v_mov_b32_e32 v62, 1
	s_mov_b32 s62, 0x1ffff
	s_mov_b64 s[6:7], exec
	s_and_b64 exec, s[6:7], s[44:45]
	v_lshrrev_b32_e32 v54, 15, v46
	v_lshlrev_b32_e32 v47, 17, v47
	v_and_b32_e32 v54, 0x1fffc, v54
	v_and_or_b32 v46, v46, s62, v47
	ds_add_rtn_u32 v47, v54, v62 offset:49152
	s_and_b64 exec, s[6:7], s[42:43]
	v_lshrrev_b32_e32 v53, 15, v41
	v_lshlrev_b32_e32 v39, 17, v39
	s_branch .Licb_s33

.Licb_s33:
	v_and_b32_e32 v53, 0x1fffc, v53
	v_and_or_b32 v41, v41, s62, v39
	ds_add_rtn_u32 v39, v53, v62 offset:49152
	s_and_b64 exec, s[6:7], s[40:41]
	v_lshrrev_b32_e32 v52, 15, v36
	v_lshlrev_b32_e32 v37, 17, v37
	v_and_b32_e32 v52, 0x1fffc, v52
	v_and_or_b32 v36, v36, s62, v37
	ds_add_rtn_u32 v37, v52, v62 offset:49152
	s_and_b64 exec, s[6:7], s[38:39]
	v_lshrrev_b32_e32 v51, 15, v34
	v_lshlrev_b32_e32 v32, 17, v32
	v_and_b32_e32 v51, 0x1fffc, v51
	v_and_or_b32 v34, v34, s62, v32
	s_branch .Licb_s34

.Licb_s34:
	ds_add_rtn_u32 v32, v51, v62 offset:49152
	s_and_b64 exec, s[6:7], s[36:37]
	v_lshrrev_b32_e32 v50, 15, v29
	v_lshlrev_b32_e32 v30, 17, v30
	v_and_b32_e32 v50, 0x1fffc, v50
	v_and_or_b32 v29, v29, s62, v30
	ds_add_rtn_u32 v30, v50, v62 offset:49152
	s_and_b64 exec, s[6:7], s[34:35]
	v_lshrrev_b32_e32 v49, 15, v28
	v_lshlrev_b32_e32 v27, 17, v27
	v_and_b32_e32 v49, 0x1fffc, v49
	v_and_or_b32 v28, v28, s62, v27
	ds_add_rtn_u32 v27, v49, v62 offset:49152
	s_and_b64 exec, s[6:7], s[30:31]
	s_branch .Licb_s35

.Licb_s35:
	v_lshrrev_b32_e32 v48, 15, v25
	v_lshlrev_b32_e32 v26, 17, v26
	v_and_b32_e32 v48, 0x1fffc, v48
	v_and_or_b32 v25, v25, s62, v26
	ds_add_rtn_u32 v26, v48, v62 offset:49152
	s_and_b64 exec, s[6:7], s[28:29]
	v_lshrrev_b32_e32 v45, 15, v24
	v_lshlrev_b32_e32 v23, 17, v23
	v_and_b32_e32 v45, 0x1fffc, v45
	v_and_or_b32 v24, v24, s62, v23
	ds_add_rtn_u32 v23, v45, v62 offset:49152
	s_and_b64 exec, s[6:7], s[26:27]
	v_lshrrev_b32_e32 v42, 15, v21
	v_lshlrev_b32_e32 v22, 17, v22
	s_branch .Licb_s36

.Licb_s36:
	v_and_b32_e32 v42, 0x1fffc, v42
	v_and_or_b32 v21, v21, s62, v22
	ds_add_rtn_u32 v22, v42, v62 offset:49152
	s_and_b64 exec, s[6:7], s[24:25]
	v_lshrrev_b32_e32 v38, 15, v20
	v_lshlrev_b32_e32 v19, 17, v19
	v_and_b32_e32 v38, 0x1fffc, v38
	v_and_or_b32 v20, v20, s62, v19
	ds_add_rtn_u32 v19, v38, v62 offset:49152
	s_and_b64 exec, s[6:7], s[22:23]
	v_lshrrev_b32_e32 v35, 15, v17
	v_lshlrev_b32_e32 v18, 17, v18
	v_and_b32_e32 v35, 0x1fffc, v35
	v_and_or_b32 v17, v17, s62, v18
	s_branch .Licb_s37

.Licb_s37:
	ds_add_rtn_u32 v18, v35, v62 offset:49152
	s_and_b64 exec, s[6:7], s[20:21]
	v_lshrrev_b32_e32 v33, 15, v16
	v_lshlrev_b32_e32 v15, 17, v15
	v_and_b32_e32 v33, 0x1fffc, v33
	v_and_or_b32 v16, v16, s62, v15
	ds_add_rtn_u32 v15, v33, v62 offset:49152
	s_and_b64 exec, s[6:7], s[60:61]
	v_lshrrev_b32_e32 v31, 15, v13
	v_lshlrev_b32_e32 v14, 17, v14
	v_and_b32_e32 v31, 0x1fffc, v31
	v_and_or_b32 v13, v13, s62, v14
	ds_add_rtn_u32 v14, v31, v62 offset:49152
	s_and_b64 exec, s[6:7], s[48:49]
	s_branch .Licb_s38

.Licb_s38:
	v_lshrrev_b32_e32 v55, 15, v12
	v_lshlrev_b32_e32 v11, 17, v11
	v_and_b32_e32 v55, 0x1fffc, v55
	v_and_or_b32 v12, v12, s62, v11
	ds_add_rtn_u32 v11, v55, v62 offset:49152
	s_and_b64 exec, s[6:7], s[78:79]
	v_lshrrev_b32_e32 v58, 15, v56
	v_lshlrev_b32_e32 v57, 17, v57
	v_and_b32_e32 v58, 0x1fffc, v58
	v_and_or_b32 v56, v56, s62, v57
	ds_add_rtn_u32 v57, v58, v62 offset:49152
	s_and_b64 exec, s[6:7], s[80:81]
	v_lshrrev_b32_e32 v61, 15, v59
	v_lshlrev_b32_e32 v60, 17, v60
	s_branch .Licb_s39

.Licb_s39:
	v_and_b32_e32 v61, 0x1fffc, v61
	v_and_or_b32 v59, v59, s62, v60
	ds_add_rtn_u32 v60, v61, v62 offset:49152
	s_mov_b64 exec, s[6:7]
	s_mov_b32 s63, 1
	s_branch .Lbs_cnt_join

.Lbs_cnt_join:
	v_mov_b32_e32 v4, 0
	s_waitcnt lgkmcnt(0)
	s_barrier
	s_and_saveexec_b64 s[18:19], vcc
	v_lshlrev_b32_e32 v4, 2, v0
	ds_read_b32 v4, v4 offset:49152
	s_or_b64 exec, exec, s[18:19]
	s_waitcnt lgkmcnt(0)
	v_mov_b32_e32 v5, v4
	s_nop 1
	v_add_u32_dpp v5, v5, v5 row_shr:1 row_mask:0xf bank_mask:0xf
	s_nop 1
	v_add_u32_dpp v5, v5, v5 row_shr:2 row_mask:0xf bank_mask:0xf
	s_nop 1
	s_branch .Licb_s40

.Licb_s40:
	v_add_u32_dpp v5, v5, v5 row_shr:4 row_mask:0xf bank_mask:0xf
	s_nop 1
	v_add_u32_dpp v5, v5, v5 row_shr:8 row_mask:0xf bank_mask:0xf
	s_nop 1
	v_add_u32_dpp v5, v5, v5 row_bcast:15 row_mask:0xa bank_mask:0xf
	s_nop 1
	v_add_u32_dpp v5, v5, v5 row_bcast:31 row_mask:0xc bank_mask:0xf
	s_and_saveexec_b64 s[18:19], s[14:15]
	ds_write_b32 v8, v5 offset:54016
	s_or_b64 exec, exec, s[18:19]
	s_waitcnt lgkmcnt(0)
	s_barrier
	s_and_saveexec_b64 s[14:15], s[16:17]
	s_cbranch_execz .LBB2_128
	v_mov_b32_e32 v44, 0
	s_branch .Licb_s41

.Licb_s41:
	v_lshlrev_b32_e32 v43, 2, v2
	s_and_saveexec_b64 s[16:17], s[10:11]
	ds_read_b32 v44, v43 offset:54016
	s_or_b64 exec, exec, s[16:17]
	s_waitcnt lgkmcnt(0)
	v_mov_b32_e32 v3, v44
	s_nop 1
	v_add_u32_dpp v3, v3, v3 row_shr:1 row_mask:0xf bank_mask:0xf
	s_nop 1
	v_add_u32_dpp v3, v3, v3 row_shr:2 row_mask:0xf bank_mask:0xf
	s_nop 1
	v_add_u32_dpp v3, v3, v3 row_shr:4 row_mask:0xf bank_mask:0xf
	s_nop 1
	v_add_u32_dpp v3, v3, v3 row_shr:8 row_mask:0xf bank_mask:0xf
	s_branch .Licb_s42

.Licb_s42:
	s_and_b64 exec, exec, s[10:11]
	ds_write_b32 v43, v3 offset:54080
.LBB2_128:
	s_or_b64 exec, exec, s[14:15]
	v_mov_b32_e32 v3, 0
	s_waitcnt lgkmcnt(0)
	s_barrier
	s_and_saveexec_b64 s[4:5], s[12:13]
	ds_read_b32 v3, v8 offset:54076
	s_or_b64 exec, exec, s[4:5]
	s_and_saveexec_b64 s[4:5], vcc
	s_cbranch_execz .LBB2_132
	v_sub_u32_e32 v4, v5, v4
	s_mul_i32 s3, s2, 0x300
	s_waitcnt lgkmcnt(0)
	s_branch .Licb_s43

.Licb_s43:
	v_add_u32_e32 v3, v3, v4
	v_add_u32_e32 v4, s3, v0
	v_ashrrev_i32_e32 v5, 31, v4
	v_add_u32_e32 v6, s50, v3
	v_lshl_add_u64 v[4:5], v[4:5], 2, s[52:53]
	global_store_dword v[4:5], v6, off
	v_lshlrev_b32_e32 v4, 2, v0
	ds_write_b32 v4, v3 offset:49152
.LBB2_132:
	s_or_b64 exec, exec, s[4:5]
	s_cmpk_eq_i32 s2, 0x186
	s_cselect_b64 s[2:3], -1, 0
	v_cmp_eq_u32_e32 vcc, 0, v0
	s_and_b64 s[4:5], s[2:3], vcc
	s_and_saveexec_b64 s[2:3], s[4:5]
	s_branch .Licb_s44

.Licb_s44:
	s_cbranch_execz .LBB2_134
	s_add_i32 s4, s33, s50
	s_waitcnt lgkmcnt(0)
	v_mov_b32_e32 v3, 0x125000
	v_mov_b32_e32 v4, s4
	global_store_dword v3, v4, s[52:53] offset:1024
.LBB2_134:
	s_or_b64 exec, exec, s[2:3]
	s_waitcnt lgkmcnt(0)
	s_barrier
	s_cmp_eq_u32 s63, 0
	s_cbranch_scc1 .Lbs_slow
	v_mov_b32_e32 v3, 0
	ds_read_b32 v3, v3 offset:54144
	s_mov_b64 s[4:5], -1
	s_branch .Licb_s45

.Licb_s45:
	s_mov_b64 s[6:7], 0
	s_mov_b64 s[2:3], exec
	s_waitcnt lgkmcnt(0)
	v_readfirstlane_b32 s8, v3
	s_cmp_lg_u32 s8, 0
	s_cbranch_scc1 .Lbs_pos_atomic
	s_and_b64 exec, s[2:3], s[44:45]
	ds_read_b32 v54, v54 offset:49152
	s_and_b64 exec, s[2:3], s[42:43]
	ds_read_b32 v53, v53 offset:49152
	s_and_b64 exec, s[2:3], s[40:41]
	ds_read_b32 v52, v52 offset:49152
	s_and_b64 exec, s[2:3], s[38:39]
	ds_read_b32 v51, v51 offset:49152
	s_branch .Licb_s46

.Licb_s46:
	s_and_b64 exec, s[2:3], s[36:37]
	ds_read_b32 v50, v50 offset:49152
	s_and_b64 exec, s[2:3], s[34:35]
	ds_read_b32 v49, v49 offset:49152
	s_and_b64 exec, s[2:3], s[30:31]
	ds_read_b32 v48, v48 offset:49152
	s_and_b64 exec, s[2:3], s[28:29]
	ds_read_b32 v45, v45 offset:49152
	s_and_b64 exec, s[2:3], s[26:27]
	ds_read_b32 v42, v42 offset:49152
	s_and_b64 exec, s[2:3], s[24:25]
	ds_read_b32 v38, v38 offset:49152
	s_and_b64 exec, s[2:3], s[22:23]
	ds_read_b32 v35, v35 offset:49152
	s_branch .Licb_s47

.Licb_s47:
	s_and_b64 exec, s[2:3], s[20:21]
	ds_read_b32 v33, v33 offset:49152
	s_and_b64 exec, s[2:3], s[60:61]
	ds_read_b32 v31, v31 offset:49152
	s_and_b64 exec, s[2:3], s[48:49]
	ds_read_b32 v55, v55 offset:49152
	s_and_b64 exec, s[2:3], s[78:79]
	ds_read_b32 v58, v58 offset:49152
	s_and_b64 exec, s[2:3], s[80:81]
	ds_read_b32 v61, v61 offset:49152
	s_mov_b64 exec, s[2:3]
	s_waitcnt lgkmcnt(0)
	s_and_b64 exec, s[2:3], s[44:45]
	v_add_lshl_u32 v54, v54, v47, 2
	s_branch .Licb_s48

.Licb_s48:
	ds_write_b32 v54, v46
	s_and_b64 exec, s[2:3], s[42:43]
	v_add_lshl_u32 v53, v53, v39, 2
	ds_write_b32 v53, v41
	s_and_b64 exec, s[2:3], s[40:41]
	v_add_lshl_u32 v52, v52, v37, 2
	ds_write_b32 v52, v36
	s_and_b64 exec, s[2:3], s[38:39]
	v_add_lshl_u32 v51, v51, v32, 2
	ds_write_b32 v51, v34
	s_and_b64 exec, s[2:3], s[36:37]
	v_add_lshl_u32 v50, v50, v30, 2
	ds_write_b32 v50, v29
	s_and_b64 exec, s[2:3], s[34:35]
	s_branch .Licb_s49

.Licb_s49:
	v_add_lshl_u32 v49, v49, v27, 2
	ds_write_b32 v49, v28
	s_and_b64 exec, s[2:3], s[30:31]
	v_add_lshl_u32 v48, v48, v26, 2
	ds_write_b32 v48, v25
	s_and_b64 exec, s[2:3], s[28:29]
	v_add_lshl_u32 v45, v45, v23, 2
	ds_write_b32 v45, v24
	s_and_b64 exec, s[2:3], s[26:27]
	v_add_lshl_u32 v42, v42, v22, 2
	ds_write_b32 v42, v21
	s_and_b64 exec, s[2:3], s[24:25]
	v_add_lshl_u32 v38, v38, v19, 2
	ds_write_b32 v38, v20
	s_branch .Licb_s50

.Licb_s50:
	s_and_b64 exec, s[2:3], s[22:23]
	v_add_lshl_u32 v35, v35, v18, 2
	ds_write_b32 v35, v17
	s_and_b64 exec, s[2:3], s[20:21]
	v_add_lshl_u32 v33, v33, v15, 2
	ds_write_b32 v33, v16
	s_and_b64 exec, s[2:3], s[60:61]
	v_add_lshl_u32 v31, v31, v14, 2
	ds_write_b32 v31, v13
	s_and_b64 exec, s[2:3], s[48:49]
	v_add_lshl_u32 v55, v55, v11, 2
	ds_write_b32 v55, v12
	s_and_b64 exec, s[2:3], s[78:79]
	v_add_lshl_u32 v58, v58, v57, 2
	s_branch .Licb_s51

.Licb_s51:
	ds_write_b32 v58, v56
	s_and_b64 exec, s[2:3], s[80:81]
	v_add_lshl_u32 v61, v61, v60, 2
	ds_write_b32 v61, v59
	s_mov_b64 exec, s[2:3]
	s_branch .LBB2_317

.LBB2_317:
	s_or_b64 exec, exec, s[2:3]
	v_cmp_gt_i32_e32 vcc, s33, v0
	s_and_b64 s[0:1], s[4:5], vcc
	s_waitcnt lgkmcnt(0)
	s_barrier
	s_and_saveexec_b64 s[2:3], s[0:1]
	s_cbranch_execz .LBB2_330
	v_xad_u32 v1, v0, -1, s33
	s_movk_i32 s0, 0x3ff
	v_cmp_lt_u32_e32 vcc, s0, v1
	s_mov_b64 s[2:3], -1
	s_and_saveexec_b64 s[0:1], vcc
	s_cbranch_execz .LBB2_327
	v_lshrrev_b32_e32 v12, 10, v1
	s_branch .Licb_s52

.Licb_s52:
	v_add_u32_e32 v2, -1, v12
	v_or_b32_e32 v1, 0x400, v0
	v_lshrrev_b32_e32 v3, 1, v2
	s_mov_b32 s6, 0
	v_add_u32_e32 v14, 1, v3
	v_cmp_lt_u32_e32 vcc, 13, v2
	v_mov_b32_e32 v17, 0
	v_lshlrev_b32_e32 v13, 2, v0
	v_mov_b64_e32 v[2:3], v[0:1]
	s_and_saveexec_b64 s[2:3], vcc
	s_cbranch_execz .LBB2_323
	s_add_i32 s7, s50, 0x800
	s_add_i32 s9, s50, 0x1000
	s_add_i32 s11, s50, 0x1800
	s_branch .Licb_s53

.Licb_s53:
	s_add_i32 s13, s50, 0x2000
	s_add_i32 s15, s50, 0x2800
	s_add_i32 s17, s50, 0x3000
	s_add_i32 s19, s50, 0x3800
	v_and_b32_e32 v15, -8, v14
	s_mov_b32 s8, s7
	s_mov_b32 s10, s9
	s_mov_b32 s12, s11
	s_mov_b32 s14, s13
	s_mov_b32 s16, s15
	s_mov_b32 s18, s17
	s_mov_b32 s20, s19
	s_mov_b64 s[4:5], 0
	v_mov_b32_e32 v16, v13
	s_branch .Licb_s54

.Licb_s54:
	v_mov_b64_e32 v[2:3], v[0:1]
.LBB2_321:
	ds_read2st64_b32 v[4:5], v16 offset1:16
	v_add_u32_e32 v10, s50, v2
	ds_read2st64_b32 v[6:7], v16 offset0:32 offset1:48
	v_add_u32_e32 v15, -8, v15
	v_add_u32_e32 v8, s50, v3
	v_add_u32_e32 v18, s7, v2
	v_add_u32_e32 v20, s8, v3
	v_add_u32_e32 v24, s9, v2
	v_add_u32_e32 v26, s10, v3
	v_add_u32_e32 v30, s11, v2
	v_add_u32_e32 v32, s12, v3
	v_add_u32_e32 v36, s13, v2
	v_add_u32_e32 v38, s14, v3
	s_branch .Licb_s55

.Licb_s55:
	v_add_u32_e32 v42, s15, v2
	v_add_u32_e32 v44, s16, v3
	v_add_u32_e32 v48, s17, v2
	v_add_u32_e32 v50, s18, v3
	v_add_u32_e32 v54, s19, v2
	v_add_u32_e32 v56, s20, v3
	s_add_i32 s6, s6, 16
	v_ashrrev_i32_e32 v11, 31, v10
	v_cmp_eq_u32_e32 vcc, 0, v15
	ds_read2st64_b32 v[22:23], v16 offset0:64 offset1:80
	ds_read2st64_b32 v[28:29], v16 offset0:96 offset1:112
	ds_read2st64_b32 v[34:35], v16 offset0:128 offset1:144
	ds_read2st64_b32 v[40:41], v16 offset0:160 offset1:176
	ds_read2st64_b32 v[46:47], v16 offset0:192 offset1:208
	s_branch .Licb_s56

.Licb_s56:
	ds_read2st64_b32 v[52:53], v16 offset0:224 offset1:240
	v_add_u32_e32 v3, 0x4000, v3
	v_add_u32_e32 v2, 0x4000, v2
	v_add_u32_e32 v16, 0x10000, v16
	v_ashrrev_i32_e32 v9, 31, v8
	v_ashrrev_i32_e32 v21, 31, v20
	v_ashrrev_i32_e32 v19, 31, v18
	v_ashrrev_i32_e32 v27, 31, v26
	v_ashrrev_i32_e32 v25, 31, v24
	v_ashrrev_i32_e32 v33, 31, v32
	v_ashrrev_i32_e32 v31, 31, v30
	v_ashrrev_i32_e32 v39, 31, v38
	v_ashrrev_i32_e32 v37, 31, v36
	v_ashrrev_i32_e32 v45, 31, v44
	s_branch .Licb_s57

.Licb_s57:
	v_ashrrev_i32_e32 v43, 31, v42
	v_ashrrev_i32_e32 v51, 31, v50
	v_ashrrev_i32_e32 v49, 31, v48
	v_ashrrev_i32_e32 v57, 31, v56
	v_ashrrev_i32_e32 v55, 31, v54
	v_mov_b32_e32 v17, s6
	v_lshl_add_u64 v[10:11], v[10:11], 2, s[54:55]
	s_or_b64 s[4:5], vcc, s[4:5]
	v_lshl_add_u64 v[8:9], v[8:9], 2, s[54:55]
	v_lshl_add_u64 v[18:19], v[18:19], 2, s[54:55]
	v_lshl_add_u64 v[20:21], v[20:21], 2, s[54:55]
	v_lshl_add_u64 v[24:25], v[24:25], 2, s[54:55]
	v_lshl_add_u64 v[26:27], v[26:27], 2, s[54:55]
	v_lshl_add_u64 v[30:31], v[30:31], 2, s[54:55]
	s_branch .Licb_s58

.Licb_s58:
	v_lshl_add_u64 v[32:33], v[32:33], 2, s[54:55]
	v_lshl_add_u64 v[36:37], v[36:37], 2, s[54:55]
	v_lshl_add_u64 v[38:39], v[38:39], 2, s[54:55]
	v_lshl_add_u64 v[42:43], v[42:43], 2, s[54:55]
	v_lshl_add_u64 v[44:45], v[44:45], 2, s[54:55]
	v_lshl_add_u64 v[48:49], v[48:49], 2, s[54:55]
	v_lshl_add_u64 v[50:51], v[50:51], 2, s[54:55]
	v_lshl_add_u64 v[54:55], v[54:55], 2, s[54:55]
	v_lshl_add_u64 v[56:57], v[56:57], 2, s[54:55]
	s_waitcnt lgkmcnt(7)
	global_store_dword v[10:11], v4, off
	global_store_dword v[8:9], v5, off
	s_waitcnt lgkmcnt(6)
	global_store_dword v[18:19], v6, off
	s_branch .Licb_s59

.Licb_s59:
	global_store_dword v[20:21], v7, off
	s_waitcnt lgkmcnt(5)
	global_store_dword v[24:25], v22, off
	global_store_dword v[26:27], v23, off
	s_waitcnt lgkmcnt(4)
	global_store_dword v[30:31], v28, off
	global_store_dword v[32:33], v29, off
	s_waitcnt lgkmcnt(3)
	global_store_dword v[36:37], v34, off
	global_store_dword v[38:39], v35, off
	s_waitcnt lgkmcnt(2)
	global_store_dword v[42:43], v40, off
	global_store_dword v[44:45], v41, off
	s_waitcnt lgkmcnt(1)
	s_branch .Licb_s60

.Licb_s60:
	global_store_dword v[48:49], v46, off
	global_store_dword v[50:51], v47, off
	s_waitcnt lgkmcnt(0)
	global_store_dword v[54:55], v52, off
	global_store_dword v[56:57], v53, off
	s_andn2_b64 exec, exec, s[4:5]
	s_cbranch_execnz .LBB2_321
	s_or_b64 exec, exec, s[4:5]
.LBB2_323:
	s_or_b64 exec, exec, s[2:3]
	v_and_b32_e32 v1, 7, v14
	v_cmp_ne_u32_e32 vcc, 0, v1
	s_and_saveexec_b64 s[2:3], vcc
	s_cbranch_execz .LBB2_326
	v_lshl_or_b32 v4, v17, 12, v13
	s_branch .Licb_s61

.Licb_s61:
	s_mov_b64 s[4:5], 0
.LBB2_325:
	ds_read2st64_b32 v[6:7], v4 offset1:16
	v_add_u32_e32 v8, s50, v2
	v_add_u32_e32 v1, -1, v1
	v_add_u32_e32 v10, s50, v3
	v_ashrrev_i32_e32 v9, 31, v8
	v_cmp_eq_u32_e32 vcc, 0, v1
	v_add_u32_e32 v3, 0x800, v3
	v_add_u32_e32 v2, 0x800, v2
	v_add_u32_e32 v4, 0x2000, v4
	v_ashrrev_i32_e32 v11, 31, v10
	v_lshl_add_u64 v[8:9], v[8:9], 2, s[54:55]
	s_or_b64 s[4:5], vcc, s[4:5]
	v_lshl_add_u64 v[10:11], v[10:11], 2, s[54:55]
	s_branch .Licb_s62

.Licb_s62:
	s_waitcnt lgkmcnt(0)
	global_store_dword v[8:9], v6, off
	global_store_dword v[10:11], v7, off
	s_andn2_b64 exec, exec, s[4:5]
	s_cbranch_execnz .LBB2_325

.LBB2_327:
	s_or_b64 exec, exec, s[0:1]
	s_and_b64 exec, exec, s[2:3]
	s_cbranch_execz .LBB2_330
	v_ashrrev_i32_e32 v1, 31, v0
	s_branch .Licb_s63

.Licb_s63:
	s_ashr_i32 s51, s50, 31
	v_lshl_add_u64 v[2:3], v[0:1], 0, s[50:51]
	v_lshl_add_u64 v[2:3], v[2:3], 2, s[54:55]
	v_lshlrev_b32_e32 v1, 2, v0
	s_mov_b64 s[0:1], 0
	s_mov_b64 s[2:3], 0x1000
.LBB2_329:
	ds_read_b32 v4, v1
	v_add_u32_e32 v0, 0x400, v0
	v_cmp_le_i32_e32 vcc, s33, v0
	v_add_u32_e32 v1, 0x1000, v1
	s_or_b64 s[0:1], vcc, s[0:1]
	s_waitcnt lgkmcnt(0)
	global_store_dword v[2:3], v4, off
	v_lshl_add_u64 v[2:3], v[2:3], 0, s[2:3]
	s_branch .Licb_s64

.Licb_s64:
	s_andn2_b64 exec, exec, s[0:1]
	s_cbranch_execnz .LBB2_329

.LBB4_14:
	v_lshrrev_b32_e32 v2, 3, v0
	s_load_dwordx2 s[4:5], s[0:1], 0x40
	v_and_b32_e32 v2, 0x78, v2
	s_movk_i32 s2, 0xa0
	v_and_b32_e32 v97, 7, v0
	s_sub_i32 s0, s18, s8
	v_and_b32_e32 v1, 63, v0
	v_mov_b32_e32 v89, 0
	v_mad_u32_u24 v3, v2, s2, 0
	v_bfe_u32 v96, v0, 3, 3
	v_and_b32_e32 v99, 15, v0
	v_bfe_u32 v4, v0, 4, 2
	s_add_i32 s0, s0, 7
	v_mul_u32_u24_e32 v5, 0xa0, v97
	v_and_b32_e32 v0, 48, v0
	s_ashr_i32 s9, s0, 3
	v_cmp_eq_u32_e64 s[0:1], 0, v1
	v_mad_u32_u24 v1, v96, s2, v3
	v_lshlrev_b32_e32 v2, 3, v4
	v_add3_u32 v103, v3, v5, v0
	v_mov_b32_e32 v3, v89
	v_lshlrev_b32_e32 v98, 4, v97
	v_add_u32_e32 v0, 0, v0
	v_lshlrev_b32_e32 v88, 2, v4
	v_lshl_add_u64 v[90:91], s[22:23], 0, v[2:3]
	v_mul_u32_u24_e32 v2, 0x220, v99
	v_or_b32_e32 v100, 8, v97
	v_or_b32_e32 v101, 16, v97
	v_add_u32_e32 v102, 0, v98
	v_cmp_gt_u32_e64 s[2:3], 8, v99
	s_waitcnt lgkmcnt(0)
	v_lshl_add_u64 v[92:93], s[4:5], 0, v[88:89]
	v_lshlrev_b32_e32 v88, 2, v88
	v_add_u32_e32 v104, v1, v98
	v_add_u32_e32 v105, v0, v2
	v_add_u32_e32 v105, 0x1cd90, v105
	s_lshl_b32 s19, s36, 3
	s_add_i32 s19, s19, s8
	v_add_u32_e32 v94, s19, v96
	v_cmp_gt_i32_e64 s[4:5], s18, v94
	v_mov_b32_e32 v32, 0
	v_mov_b32_e32 v33, 0
	v_mov_b32_e32 v34, 0
	v_mov_b32_e32 v35, 0
	s_and_saveexec_b64 s[6:7], s[4:5]
	v_lshl_add_u32 v36, v94, 1, v94
	v_lshlrev_b32_e32 v36, 2, v36
	global_load_dwordx4 v[32:35], v36, s[10:11]
	s_mov_b64 exec, s[6:7]
	s_cmp_eq_u32 s36, 0
	s_cbranch_scc1 .Lic1_t0
	s_cmp_eq_u32 s36, 1
	s_cbranch_scc1 .Lic1_t1
	s_cmp_eq_u32 s36, 2
	s_cbranch_scc1 .Lic1_t2
	s_cmp_eq_u32 s36, 3
	s_cbranch_scc1 .Lic1_t3
	s_cmp_eq_u32 s36, 4
	s_cbranch_scc1 .Lic1_t4
	s_cmp_eq_u32 s36, 5
	s_cbranch_scc1 .Lic1_t5
	s_cmp_eq_u32 s36, 6
	s_cbranch_scc1 .Lic1_t6
	s_cmp_eq_u32 s36, 7
	s_cbranch_scc1 .Lic1_t7
	s_cmp_eq_u32 s36, 8
	s_cbranch_scc1 .Lic1_t8
	s_cmp_eq_u32 s36, 9
	s_cbranch_scc1 .Lic1_t9
	s_cmp_eq_u32 s36, 10
	s_cbranch_scc1 .Lic1_t10
	s_cmp_eq_u32 s36, 11
	s_cbranch_scc1 .Lic1_t11
	s_cmp_eq_u32 s36, 12
	s_cbranch_scc1 .Lic1_t12
	s_cmp_eq_u32 s36, 13
	s_cbranch_scc1 .Lic1_t13
	s_cmp_eq_u32 s36, 14
	s_cbranch_scc1 .Lic1_t14
	s_cmp_eq_u32 s36, 15
	s_cbranch_scc1 .Lic1_t15
.Lic1_done:
	s_waitcnt vmcnt(6)
	ds_write_b128 v40, v[6:9]
	s_waitcnt vmcnt(5)
	ds_write_b128 v40, v[10:13] offset:17408
	s_waitcnt vmcnt(4)
	ds_write_b128 v41, v[14:17]
	s_waitcnt vmcnt(3)
	ds_write_b128 v41, v[18:21] offset:16384
	s_waitcnt vmcnt(2)
	ds_write_b128 v41, v[22:25] offset:32768
	s_waitcnt vmcnt(1)
	ds_write_b128 v41, v[26:29] offset:49152
	s_and_saveexec_b64 s[6:7], s[34:35]
	ds_write_b128 v38, v[42:45]
	s_mov_b64 exec, s[6:7]
	s_waitcnt vmcnt(0)
	v_sub_u32_e32 v72, v33, v32
	v_sub_u32_e32 v108, v34, v33
	v_sub_u32_e32 v35, v35, v34
	v_add_lshl_u32 v37, v32, v97, 2
	v_add_lshl_u32 v38, v33, v97, 2
	v_add_lshl_u32 v39, v34, v97, 2
	v_mov_b32_e32 v36, 0x4000000
	v_mov_b32_e32 v68, 0x4000000
	v_mov_b32_e32 v74, 0x4000000
	v_mov_b32_e32 v85, 0x4000000
	v_mov_b32_e32 v84, 0x4000000
	v_mov_b32_e32 v109, 0x4000000
	v_mov_b32_e32 v107, 0x4000000
	v_mov_b32_e32 v106, 0x4000000
	v_mov_b32_e32 v95, 0x4000000
	s_mov_b64 s[6:7], exec
	v_cmp_lt_i32_e32 vcc, v97, v72
	s_and_b64 exec, exec, vcc
	global_load_dword v36, v37, s[12:13]
	v_cmp_lt_i32_e32 vcc, v100, v72
	s_and_b64 exec, exec, vcc
	global_load_dword v68, v37, s[12:13] offset:32
	v_cmp_lt_i32_e32 vcc, v101, v72
	s_and_b64 exec, exec, vcc
	global_load_dword v74, v37, s[12:13] offset:64
	s_mov_b64 exec, s[6:7]
	v_cmp_lt_i32_e32 vcc, v97, v108
	s_and_b64 exec, exec, vcc
	global_load_dword v85, v38, s[12:13]
	v_cmp_lt_i32_e32 vcc, v100, v108
	s_and_b64 exec, exec, vcc
	global_load_dword v84, v38, s[12:13] offset:32
	v_cmp_lt_i32_e32 vcc, v101, v108
	s_and_b64 exec, exec, vcc
	global_load_dword v109, v38, s[12:13] offset:64
	s_mov_b64 exec, s[6:7]
	v_cmp_lt_i32_e32 vcc, v97, v35
	s_and_b64 exec, exec, vcc
	global_load_dword v107, v39, s[12:13]
	v_cmp_lt_i32_e32 vcc, v100, v35
	s_and_b64 exec, exec, vcc
	global_load_dword v106, v39, s[12:13] offset:32
	v_cmp_lt_i32_e32 vcc, v101, v35
	s_and_b64 exec, exec, vcc
	global_load_dword v95, v39, s[12:13] offset:64
	s_mov_b64 exec, s[6:7]
	s_waitcnt lgkmcnt(0)
	s_barrier
	s_cmp_ge_i32 s36, s9
	s_cbranch_scc1 .LBB4_103
	s_branch .Lp1_after_idx

.LBB4_17:
	s_nop 0
	v_mov_b32_e32 v32, 0
	s_and_saveexec_b64 s[4:5], s[0:1]
	s_cbranch_execz .LBB4_21
	s_mov_b64 s[22:23], exec
	v_mbcnt_lo_u32_b32 v32, s22, 0
	v_mbcnt_hi_u32_b32 v32, s23, v32
	v_cmp_eq_u32_e32 vcc, 0, v32
	s_and_saveexec_b64 s[6:7], vcc
	s_bcnt1_i32_b64 s19, s[22:23]
	v_mov_b32_e32 v33, s19
	ds_add_rtn_u32 v33, v89, v33 offset:52224
	s_or_b64 exec, exec, s[6:7]
	s_waitcnt lgkmcnt(0)
	s_branch .Lic1_s0

.Lic1_s0:
	v_readfirstlane_b32 s6, v33
	s_nop 1
	v_add_u32_e32 v32, s6, v32
.LBB4_21:
	s_or_b64 exec, exec, s[4:5]
	v_readfirstlane_b32 s6, v32
	s_cmp_ge_i32 s6, s9
	s_mov_b64 s[4:5], -1
	s_cbranch_scc1 .LBB4_16
	s_lshl_b32 s19, s6, 3
	s_add_i32 s19, s19, s8
	v_add_u32_e32 v94, s19, v96
	v_cmp_gt_i32_e64 s[4:5], s18, v94
	v_mov_b32_e32 v34, 0
	v_mov_b32_e32 v35, 0
	s_branch .Lic1_s1

.Lic1_s1:
	v_mov_b32_e32 v32, 0
	v_mov_b32_e32 v33, 0
	s_and_saveexec_b64 s[6:7], s[4:5]
	s_cbranch_execz .LBB4_24
	v_lshl_add_u32 v32, v94, 1, v94
	v_ashrrev_i32_e32 v33, 31, v32
	v_lshl_add_u64 v[32:33], v[32:33], 2, s[10:11]
	global_load_dwordx4 v[32:35], v[32:33], off
.LBB4_24:
	s_or_b64 exec, exec, s[6:7]
	s_waitcnt vmcnt(0)
	v_sub_u32_e32 v72, v33, v32
	v_sub_u32_e32 v108, v34, v33
	v_sub_u32_e32 v35, v35, v34
	v_add_lshl_u32 v37, v32, v97, 2
	s_branch .Lic1_s2

.Lic1_s2:
	v_add_lshl_u32 v38, v33, v97, 2
	v_add_lshl_u32 v39, v34, v97, 2
	v_mov_b32_e32 v36, 0x4000000
	v_mov_b32_e32 v68, 0x4000000
	v_mov_b32_e32 v74, 0x4000000
	v_mov_b32_e32 v85, 0x4000000
	v_mov_b32_e32 v84, 0x4000000
	v_mov_b32_e32 v109, 0x4000000
	v_mov_b32_e32 v107, 0x4000000
	v_mov_b32_e32 v106, 0x4000000
	v_mov_b32_e32 v95, 0x4000000
	s_mov_b64 s[6:7], exec
	v_cmp_lt_i32_e32 vcc, v97, v72
	s_and_b64 exec, exec, vcc
	s_branch .Lic1_s3

.Lic1_s3:
	global_load_dword v36, v37, s[12:13]
	v_cmp_lt_i32_e32 vcc, v100, v72
	s_and_b64 exec, exec, vcc
	global_load_dword v68, v37, s[12:13] offset:32
	v_cmp_lt_i32_e32 vcc, v101, v72
	s_and_b64 exec, exec, vcc
	global_load_dword v74, v37, s[12:13] offset:64
	s_mov_b64 exec, s[6:7]
	v_cmp_lt_i32_e32 vcc, v97, v108
	s_and_b64 exec, exec, vcc
	global_load_dword v85, v38, s[12:13]
	v_cmp_lt_i32_e32 vcc, v100, v108
	s_and_b64 exec, exec, vcc
	global_load_dword v84, v38, s[12:13] offset:32
	s_branch .Lic1_s4

.Lic1_s4:
	v_cmp_lt_i32_e32 vcc, v101, v108
	s_and_b64 exec, exec, vcc
	global_load_dword v109, v38, s[12:13] offset:64
	s_mov_b64 exec, s[6:7]
	v_cmp_lt_i32_e32 vcc, v97, v35
	s_and_b64 exec, exec, vcc
	global_load_dword v107, v39, s[12:13]
	v_cmp_lt_i32_e32 vcc, v100, v35
	s_and_b64 exec, exec, vcc
	global_load_dword v106, v39, s[12:13] offset:32
	v_cmp_lt_i32_e32 vcc, v101, v35
	s_and_b64 exec, exec, vcc
	global_load_dword v95, v39, s[12:13] offset:64
	s_mov_b64 exec, s[6:7]
.Lp1_after_idx:
	v_lshlrev_b32_e32 v114, 2, v94
	s_branch .Lic1_s5

.Lic1_s5:
	s_mov_b64 s[6:7], exec
	s_and_b64 exec, exec, s[4:5]
	global_load_dword v115, v114, s[14:15]
	global_load_dword v114, v114, s[16:17]
	s_mov_b64 exec, s[6:7]
	s_waitcnt vmcnt(0)
	v_lshrrev_b32_e32 v36, 10, v36
	v_lshrrev_b32_e32 v68, 10, v68
	v_lshrrev_b32_e32 v74, 10, v74
	v_lshrrev_b32_e32 v85, 10, v85
	v_lshrrev_b32_e32 v84, 10, v84
	v_lshrrev_b32_e32 v109, 10, v109
	v_lshrrev_b32_e32 v107, 10, v107
	v_lshrrev_b32_e32 v106, 10, v106
	s_branch .Lic1_s6

.Lic1_s6:
	v_lshrrev_b32_e32 v95, 10, v95
	v_and_b32_e32 v36, 0x3fff80, v36
	v_and_b32_e32 v68, 0x3fff80, v68
	v_and_b32_e32 v74, 0x3fff80, v74
	v_and_b32_e32 v85, 0x3fff80, v85
	v_and_b32_e32 v84, 0x3fff80, v84
	v_and_b32_e32 v109, 0x3fff80, v109
	v_and_b32_e32 v107, 0x3fff80, v107
	v_and_b32_e32 v106, 0x3fff80, v106
	v_and_b32_e32 v95, 0x3fff80, v95
	v_mov_b32_dpp v41, v36 row_newbcast:6 row_mask:0xf bank_mask:0x3
	v_mov_b32_dpp v41, v36 row_newbcast:14 row_mask:0xf bank_mask:0xc
	v_add_u32_dpp v37, v36, v102 row_newbcast:0 row_mask:0xf bank_mask:0x3
	v_add_u32_dpp v37, v36, v102 row_newbcast:8 row_mask:0xf bank_mask:0xc
	s_branch .Lic1_s7

.Lic1_s7:
	v_add_u32_dpp v38, v36, v102 row_newbcast:1 row_mask:0xf bank_mask:0x3
	v_add_u32_dpp v38, v36, v102 row_newbcast:9 row_mask:0xf bank_mask:0xc
	ds_read_b128 v[60:63], v37 offset:52240
	ds_read_b128 v[52:55], v38 offset:52240
	v_add_u32_dpp v37, v36, v102 row_newbcast:2 row_mask:0xf bank_mask:0x3
	v_add_u32_dpp v37, v36, v102 row_newbcast:10 row_mask:0xf bank_mask:0xc
	v_add_u32_dpp v39, v36, v102 row_newbcast:3 row_mask:0xf bank_mask:0x3
	v_add_u32_dpp v39, v36, v102 row_newbcast:11 row_mask:0xf bank_mask:0xc
	v_mov_b32_dpp v40, v36 row_newbcast:5 row_mask:0xf bank_mask:0x3
	v_mov_b32_dpp v40, v36 row_newbcast:13 row_mask:0xf bank_mask:0xc
	v_mov_b32_dpp v42, v36 row_newbcast:7 row_mask:0xf bank_mask:0x3
	v_mov_b32_dpp v42, v36 row_newbcast:15 row_mask:0xf bank_mask:0xc
	ds_read_b128 v[64:67], v37 offset:52240
	ds_read_b128 v[56:59], v39 offset:52240
	s_branch .Lic1_s8

.Lic1_s8:
	v_add_u32_dpp v37, v36, v102 row_newbcast:4 row_mask:0xf bank_mask:0x3
	v_add_u32_dpp v37, v36, v102 row_newbcast:12 row_mask:0xf bank_mask:0xc
	v_cmp_lt_i32_e32 vcc, 8, v72
	v_add_u32_e32 v36, v102, v40
	v_add_u32_e32 v40, v102, v41
	v_add_u32_e32 v41, v102, v42
	ds_read_b128 v[44:47], v37 offset:52240
	ds_read_b128 v[36:39], v36 offset:52240
	ds_read_b128 v[48:51], v40 offset:52240
	ds_read_b128 v[40:43], v41 offset:52240
	s_cmp_lg_u64 vcc, 0
	s_cselect_b64 s[22:23], -1, 0
	v_cmp_lt_i32_e64 s[6:7], 12, v72
	s_cbranch_vccz .LBB4_44
	v_add_u32_dpp v0, v68, v102 row_newbcast:0 row_mask:0xf bank_mask:0x3
	s_branch .Lic1_s9

.Lic1_s9:
	v_add_u32_dpp v0, v68, v102 row_newbcast:8 row_mask:0xf bank_mask:0xc
	v_add_u32_dpp v8, v68, v102 row_newbcast:1 row_mask:0xf bank_mask:0x3
	v_add_u32_dpp v8, v68, v102 row_newbcast:9 row_mask:0xf bank_mask:0xc
	v_add_u32_dpp v16, v68, v102 row_newbcast:2 row_mask:0xf bank_mask:0x3
	v_add_u32_dpp v16, v68, v102 row_newbcast:10 row_mask:0xf bank_mask:0xc
	v_add_u32_dpp v24, v68, v102 row_newbcast:3 row_mask:0xf bank_mask:0x3
	v_add_u32_dpp v24, v68, v102 row_newbcast:11 row_mask:0xf bank_mask:0xc
	ds_read_b128 v[0:3], v0 offset:52240
	ds_read_b128 v[8:11], v8 offset:52240
	ds_read_b128 v[16:19], v16 offset:52240
	ds_read_b128 v[24:27], v24 offset:52240
.LBB4_44:
	s_cmp_lg_u64 s[6:7], 0
	s_cselect_b64 s[26:27], -1, 0
	s_cmp_eq_u64 s[6:7], 0
	s_branch .Lic1_s10

.Lic1_s10:
	s_cbranch_scc1 .LBB4_46
	v_add_u32_dpp v4, v68, v102 row_newbcast:4 row_mask:0xf bank_mask:0x3
	v_add_u32_dpp v4, v68, v102 row_newbcast:12 row_mask:0xf bank_mask:0xc
	v_add_u32_dpp v12, v68, v102 row_newbcast:5 row_mask:0xf bank_mask:0x3
	v_add_u32_dpp v12, v68, v102 row_newbcast:13 row_mask:0xf bank_mask:0xc
	v_add_u32_dpp v20, v68, v102 row_newbcast:6 row_mask:0xf bank_mask:0x3
	v_add_u32_dpp v20, v68, v102 row_newbcast:14 row_mask:0xf bank_mask:0xc
	v_add_u32_dpp v28, v68, v102 row_newbcast:7 row_mask:0xf bank_mask:0x3
	v_add_u32_dpp v28, v68, v102 row_newbcast:15 row_mask:0xf bank_mask:0xc
	ds_read_b128 v[4:7], v4 offset:52240
	ds_read_b128 v[12:15], v12 offset:52240
	ds_read_b128 v[20:23], v20 offset:52240
	ds_read_b128 v[28:31], v28 offset:52240
.LBB4_46:
	v_cvt_f32_i32_e32 v68, v72
	s_branch .Lic1_s11

.Lic1_s11:
	v_max_f32_e32 v68, 1.0, v68
	v_div_scale_f32 v69, s[6:7], v68, v68, 1.0
	v_rcp_f32_e32 v70, v69
	v_div_scale_f32 v71, vcc, 1.0, v68, 1.0
	v_fma_f32 v73, -v69, v70, 1.0
	v_fmac_f32_e32 v70, v73, v70
	v_mul_f32_e32 v73, v71, v70
	v_fma_f32 v75, -v69, v73, v71
	v_fmac_f32_e32 v73, v75, v70
	v_fma_f32 v69, -v69, v73, v71
	v_div_fmas_f32 v69, v69, v70, v73
	v_div_fixup_f32 v68, v69, v68, 1.0
	v_cvt_f16_f32_e32 v69, v68
	v_cvt_pk_f16_f32 v73, v68, v68
	s_branch .Lic1_s12

.Lic1_s12:
	s_andn2_b64 vcc, exec, s[22:23]
	s_waitcnt lgkmcnt(7)
	v_pk_fma_f16 v60, v69, v60, 0 op_sel_hi:[0,1,1]
	v_pk_fma_f16 v61, v69, v61, 0 op_sel_hi:[0,1,1]
	v_pk_fma_f16 v62, v69, v62, 0 op_sel_hi:[0,1,1]
	v_pk_fma_f16 v63, v69, v63, 0 op_sel_hi:[0,1,1]
	s_waitcnt lgkmcnt(6)
	v_pk_fma_f16 v55, v69, v55, v63 op_sel_hi:[0,1,1]
	v_pk_fma_f16 v54, v69, v54, v62 op_sel_hi:[0,1,1]
	v_pk_fma_f16 v53, v69, v53, v61 op_sel_hi:[0,1,1]
	v_pk_fma_f16 v52, v69, v52, v60 op_sel_hi:[0,1,1]
	s_waitcnt lgkmcnt(5)
	v_pk_fma_f16 v52, v69, v64, v52 op_sel_hi:[0,1,1]
	v_pk_fma_f16 v53, v69, v65, v53 op_sel_hi:[0,1,1]
	s_branch .Lic1_s13

.Lic1_s13:
	v_pk_fma_f16 v54, v69, v66, v54 op_sel_hi:[0,1,1]
	v_pk_fma_f16 v55, v69, v67, v55 op_sel_hi:[0,1,1]
	s_waitcnt lgkmcnt(4)
	v_pk_fma_f16 v55, v69, v59, v55 op_sel_hi:[0,1,1]
	v_pk_fma_f16 v54, v69, v58, v54 op_sel_hi:[0,1,1]
	v_pk_fma_f16 v53, v69, v57, v53 op_sel_hi:[0,1,1]
	v_pk_fma_f16 v52, v69, v56, v52 op_sel_hi:[0,1,1]
	s_waitcnt lgkmcnt(3)
	v_pk_fma_f16 v52, v69, v44, v52 op_sel_hi:[0,1,1]
	v_pk_fma_f16 v53, v69, v45, v53 op_sel_hi:[0,1,1]
	v_pk_fma_f16 v54, v69, v46, v54 op_sel_hi:[0,1,1]
	v_pk_fma_f16 v55, v69, v47, v55 op_sel_hi:[0,1,1]
	s_waitcnt lgkmcnt(2)
	v_pk_fma_f16 v55, v69, v39, v55 op_sel_hi:[0,1,1]
	s_branch .Lic1_s14

.Lic1_s14:
	v_pk_fma_f16 v54, v69, v38, v54 op_sel_hi:[0,1,1]
	v_pk_fma_f16 v53, v69, v37, v53 op_sel_hi:[0,1,1]
	v_pk_fma_f16 v52, v69, v36, v52 op_sel_hi:[0,1,1]
	s_waitcnt lgkmcnt(1)
	v_pk_fma_f16 v52, v69, v48, v52 op_sel_hi:[0,1,1]
	v_pk_fma_f16 v53, v69, v49, v53 op_sel_hi:[0,1,1]
	v_pk_fma_f16 v54, v69, v50, v54 op_sel_hi:[0,1,1]
	v_pk_fma_f16 v55, v69, v51, v55 op_sel_hi:[0,1,1]
	s_waitcnt lgkmcnt(0)
	v_pk_fma_f16 v55, v69, v43, v55 op_sel_hi:[0,1,1]
	v_pk_fma_f16 v54, v69, v42, v54 op_sel_hi:[0,1,1]
	v_pk_fma_f16 v53, v69, v41, v53 op_sel_hi:[0,1,1]
	v_pk_fma_f16 v52, v69, v40, v52 op_sel_hi:[0,1,1]
	s_cbranch_vccnz .LBB4_48
	v_pk_fma_f16 v52, v73, v0, v52
	s_branch .Lic1_s15

.Lic1_s15:
	v_pk_fma_f16 v53, v73, v1, v53
	v_pk_fma_f16 v54, v73, v2, v54
	v_pk_fma_f16 v55, v73, v3, v55
	v_pk_fma_f16 v54, v73, v10, v54
	v_pk_fma_f16 v55, v73, v11, v55
	v_pk_fma_f16 v53, v73, v9, v53
	v_pk_fma_f16 v52, v73, v8, v52
	v_pk_fma_f16 v53, v73, v17, v53
	v_pk_fma_f16 v52, v73, v16, v52
	v_pk_fma_f16 v54, v73, v18, v54
	v_pk_fma_f16 v55, v73, v19, v55
	v_pk_fma_f16 v54, v73, v26, v54
	v_pk_fma_f16 v55, v73, v27, v55
	v_pk_fma_f16 v53, v73, v25, v53
	s_branch .Lic1_s16

.Lic1_s16:
	v_pk_fma_f16 v52, v73, v24, v52
.LBB4_48:
	s_andn2_b64 vcc, exec, s[26:27]
	s_cbranch_vccnz .LBB4_50
	v_pk_fma_f16 v52, v73, v4, v52
	v_pk_fma_f16 v53, v73, v5, v53
	v_pk_fma_f16 v54, v73, v6, v54
	v_pk_fma_f16 v55, v73, v7, v55
	v_pk_fma_f16 v54, v73, v14, v54
	v_pk_fma_f16 v55, v73, v15, v55
	v_pk_fma_f16 v53, v73, v13, v53
	v_pk_fma_f16 v52, v73, v12, v52
	v_pk_fma_f16 v53, v73, v21, v53
	v_pk_fma_f16 v52, v73, v20, v52
	v_pk_fma_f16 v54, v73, v22, v54
	s_branch .Lic1_s17

.Lic1_s17:
	v_pk_fma_f16 v55, v73, v23, v55
	v_pk_fma_f16 v54, v73, v30, v54
	v_pk_fma_f16 v55, v73, v31, v55
	v_pk_fma_f16 v53, v73, v29, v53
	v_pk_fma_f16 v52, v73, v28, v52
.LBB4_50:
	v_cmp_lt_i32_e32 vcc, 16, v72
	s_cbranch_vccz .LBB4_61
	v_cmp_lt_i32_e32 vcc, 20, v72
	v_add_u32_dpp v56, v74, v102 row_newbcast:0 row_mask:0xf bank_mask:0x3
	v_add_u32_dpp v56, v74, v102 row_newbcast:8 row_mask:0xf bank_mask:0xc
	v_add_u32_dpp v57, v74, v102 row_newbcast:1 row_mask:0xf bank_mask:0x3
	v_add_u32_dpp v57, v74, v102 row_newbcast:9 row_mask:0xf bank_mask:0xc
	ds_read_b128 v[68:71], v56 offset:52240
	ds_read_b128 v[64:67], v57 offset:52240
	s_branch .Lic1_s18

.Lic1_s18:
	v_add_u32_dpp v56, v74, v102 row_newbcast:2 row_mask:0xf bank_mask:0x3
	v_add_u32_dpp v56, v74, v102 row_newbcast:10 row_mask:0xf bank_mask:0xc
	v_add_u32_dpp v57, v74, v102 row_newbcast:3 row_mask:0xf bank_mask:0x3
	v_add_u32_dpp v57, v74, v102 row_newbcast:11 row_mask:0xf bank_mask:0xc
	ds_read_b128 v[60:63], v56 offset:52240
	ds_read_b128 v[56:59], v57 offset:52240
	s_cmp_lg_u64 vcc, 0
	s_cselect_b64 s[6:7], -1, 0
	s_cbranch_vccz .LBB4_53
	v_add_u32_dpp v36, v74, v102 row_newbcast:4 row_mask:0xf bank_mask:0x3
	v_add_u32_dpp v36, v74, v102 row_newbcast:12 row_mask:0xf bank_mask:0xc
	v_add_u32_dpp v37, v74, v102 row_newbcast:5 row_mask:0xf bank_mask:0x3
	v_add_u32_dpp v37, v74, v102 row_newbcast:13 row_mask:0xf bank_mask:0xc
	v_add_u32_dpp v40, v74, v102 row_newbcast:6 row_mask:0xf bank_mask:0x3
	s_branch .Lic1_s19

.Lic1_s19:
	v_add_u32_dpp v40, v74, v102 row_newbcast:14 row_mask:0xf bank_mask:0xc
	v_add_u32_dpp v41, v74, v102 row_newbcast:7 row_mask:0xf bank_mask:0x3
	v_add_u32_dpp v41, v74, v102 row_newbcast:15 row_mask:0xf bank_mask:0xc
	ds_read_b128 v[44:47], v36 offset:52240
	ds_read_b128 v[36:39], v37 offset:52240
	ds_read_b128 v[48:51], v40 offset:52240
	ds_read_b128 v[40:43], v41 offset:52240
.LBB4_53:
	s_waitcnt lgkmcnt(3)
	v_pk_fma_f16 v52, v73, v68, v52
	v_pk_fma_f16 v53, v73, v69, v53
	v_pk_fma_f16 v54, v73, v70, v54
	v_pk_fma_f16 v55, v73, v71, v55
	s_waitcnt lgkmcnt(2)
	v_pk_fma_f16 v54, v73, v66, v54
	s_branch .Lic1_s20

.Lic1_s20:
	v_pk_fma_f16 v55, v73, v67, v55
	v_pk_fma_f16 v53, v73, v65, v53
	v_pk_fma_f16 v52, v73, v64, v52
	s_waitcnt lgkmcnt(1)
	v_pk_fma_f16 v53, v73, v61, v53
	v_pk_fma_f16 v52, v73, v60, v52
	v_pk_fma_f16 v54, v73, v62, v54
	v_pk_fma_f16 v55, v73, v63, v55
	s_waitcnt lgkmcnt(0)
	v_pk_fma_f16 v54, v73, v58, v54
	v_pk_fma_f16 v55, v73, v59, v55
	v_pk_fma_f16 v53, v73, v57, v53
	s_andn2_b64 vcc, exec, s[6:7]
	v_pk_fma_f16 v52, v73, v56, v52
	s_branch .Lic1_s21

.Lic1_s21:
	s_cbranch_vccnz .LBB4_55
	v_pk_fma_f16 v44, v73, v44, v52
	v_pk_fma_f16 v45, v73, v45, v53
	v_pk_fma_f16 v46, v73, v46, v54
	v_pk_fma_f16 v47, v73, v47, v55
	v_pk_fma_f16 v38, v73, v38, v46
	v_pk_fma_f16 v39, v73, v39, v47
	v_pk_fma_f16 v37, v73, v37, v45
	v_pk_fma_f16 v36, v73, v36, v44
	v_pk_fma_f16 v37, v73, v49, v37
	v_pk_fma_f16 v36, v73, v48, v36
	v_pk_fma_f16 v38, v73, v50, v38
	v_pk_fma_f16 v39, v73, v51, v39
	v_pk_fma_f16 v54, v73, v42, v38
	s_branch .Lic1_s22

.Lic1_s22:
	v_pk_fma_f16 v55, v73, v43, v39
	v_pk_fma_f16 v53, v73, v41, v37
	v_pk_fma_f16 v52, v73, v40, v36

.LBB4_56:
	s_waitcnt lgkmcnt(0)
	s_or_b64 exec, exec, s[6:7]
	s_nop 1
	v_add_u32_dpp v37, v36, v102 row_newbcast:0 row_mask:0xf bank_mask:0x3
	v_add_u32_dpp v37, v36, v102 row_newbcast:8 row_mask:0xf bank_mask:0xc
	v_add_u32_dpp v42, v36, v102 row_newbcast:1 row_mask:0xf bank_mask:0x3
	v_add_u32_dpp v42, v36, v102 row_newbcast:9 row_mask:0xf bank_mask:0xc
	ds_read_b128 v[38:41], v37 offset:52240
	s_branch .Lic1_s23

.Lic1_s23:
	ds_read_b128 v[42:45], v42 offset:52240
	v_add_u32_dpp v37, v36, v102 row_newbcast:2 row_mask:0xf bank_mask:0x3
	v_add_u32_dpp v37, v36, v102 row_newbcast:10 row_mask:0xf bank_mask:0xc
	v_add_u32_dpp v51, v36, v102 row_newbcast:3 row_mask:0xf bank_mask:0x3
	v_add_u32_dpp v51, v36, v102 row_newbcast:11 row_mask:0xf bank_mask:0xc
	v_mov_b32_dpp v60, v36 row_newbcast:5 row_mask:0xf bank_mask:0x3
	v_mov_b32_dpp v60, v36 row_newbcast:13 row_mask:0xf bank_mask:0xc
	ds_read_b128 v[46:49], v37 offset:52240
	ds_read_b128 v[56:59], v51 offset:52240
	v_add_u32_dpp v37, v36, v102 row_newbcast:4 row_mask:0xf bank_mask:0x3
	v_add_u32_dpp v37, v36, v102 row_newbcast:12 row_mask:0xf bank_mask:0xc
	v_mov_b32_dpp v50, v36 row_newbcast:6 row_mask:0xf bank_mask:0x3
	v_mov_b32_dpp v50, v36 row_newbcast:14 row_mask:0xf bank_mask:0xc
	v_mov_b32_dpp v36, v36 row_newbcast:7 row_mask:0xf bank_mask:0x3
	s_branch .Lic1_s24

.Lic1_s24:
	s_nop 1
	v_mov_b32_dpp v36, v36 row_newbcast:15 row_mask:0xf bank_mask:0xc
	v_add_u32_e32 v51, v102, v60
	ds_read_b128 v[60:63], v37 offset:52240
	ds_read_b128 v[64:67], v51 offset:52240
	s_add_i32 s22, s22, 8
	v_add_u32_e32 v37, v102, v50
	v_add_u32_e32 v36, v102, v36
	ds_read_b128 v[68:71], v37 offset:52240
	ds_read_b128 v[74:77], v36 offset:52240
	s_waitcnt lgkmcnt(7)
	v_pk_fma_f16 v36, v73, v38, v52
	v_pk_fma_f16 v37, v73, v39, v53
	v_pk_fma_f16 v38, v73, v40, v54
	s_branch .Lic1_s25

.Lic1_s25:
	v_pk_fma_f16 v39, v73, v41, v55
	s_waitcnt lgkmcnt(6)
	v_pk_fma_f16 v38, v73, v44, v38
	v_pk_fma_f16 v39, v73, v45, v39
	v_pk_fma_f16 v37, v73, v43, v37
	v_pk_fma_f16 v36, v73, v42, v36
	s_waitcnt lgkmcnt(5)
	v_pk_fma_f16 v37, v73, v47, v37
	v_pk_fma_f16 v36, v73, v46, v36
	v_pk_fma_f16 v38, v73, v48, v38
	v_pk_fma_f16 v39, v73, v49, v39
	s_waitcnt lgkmcnt(4)
	v_pk_fma_f16 v38, v73, v58, v38
	v_pk_fma_f16 v39, v73, v59, v39
	s_branch .Lic1_s26

.Lic1_s26:
	v_pk_fma_f16 v37, v73, v57, v37
	v_pk_fma_f16 v36, v73, v56, v36
	s_waitcnt lgkmcnt(3)
	v_pk_fma_f16 v37, v73, v61, v37
	v_pk_fma_f16 v36, v73, v60, v36
	v_pk_fma_f16 v38, v73, v62, v38
	v_pk_fma_f16 v39, v73, v63, v39
	s_waitcnt lgkmcnt(2)
	v_pk_fma_f16 v38, v73, v66, v38
	v_pk_fma_f16 v39, v73, v67, v39
	v_pk_fma_f16 v37, v73, v65, v37
	v_pk_fma_f16 v36, v73, v64, v36
	s_waitcnt lgkmcnt(1)
	v_pk_fma_f16 v37, v73, v69, v37
	s_branch .Lic1_s27

.Lic1_s27:
	v_pk_fma_f16 v36, v73, v68, v36
	v_pk_fma_f16 v38, v73, v70, v38
	v_pk_fma_f16 v39, v73, v71, v39
	s_waitcnt lgkmcnt(0)
	v_pk_fma_f16 v54, v73, v76, v38
	v_pk_fma_f16 v55, v73, v77, v39
	v_pk_fma_f16 v53, v73, v75, v37
	v_pk_fma_f16 v52, v73, v74, v36
.LBB4_57:
	s_waitcnt lgkmcnt(0)
	v_cmp_lt_i32_e32 vcc, s22, v72
	s_cbranch_vccz .LBB4_60
	v_add_u32_e32 v36, s22, v97
	v_cmp_lt_i32_e32 vcc, v36, v72
	v_mov_b32_e32 v36, 0x10000
	s_branch .Lic1_s28

.Lic1_s28:
	s_and_saveexec_b64 s[6:7], vcc
	s_cbranch_execz .LBB4_56
	v_add_u32_e32 v36, s22, v32
	v_ashrrev_i32_e32 v37, 31, v36
	v_lshl_add_u64 v[36:37], v[36:37], 2, s[12:13]
	global_load_dword v36, v[36:37], off
	s_waitcnt vmcnt(0)
	v_lshrrev_b32_e32 v36, 10, v36
	v_and_b32_e32 v36, 0x3fff80, v36
	s_branch .LBB4_56

.LBB4_61:
	ds_write_b128 v104, v[52:55]
	ds_read_b128 v[36:39], v105
	ds_read_b128 v[40:43], v103
	s_branch .Lic1_s29

.Lic1_s29:
	ds_read_b128 v[44:47], v105 offset:8704
	ds_read_b128 v[48:51], v105 offset:17408
	ds_read_b128 v[52:55], v105 offset:26112
	s_waitcnt lgkmcnt(3)
	v_mfma_f32_16x16x32_f16 v[36:39], v[36:39], v[40:43], 0
	s_waitcnt lgkmcnt(2)
	v_mfma_f32_16x16x32_f16 v[44:47], v[44:47], v[40:43], 0
	s_waitcnt lgkmcnt(1)
	v_mfma_f32_16x16x32_f16 v[48:51], v[48:51], v[40:43], 0
	s_waitcnt lgkmcnt(0)
	v_mfma_f32_16x16x32_f16 v[52:55], v[52:55], v[40:43], 0
	ds_read_b128 v[40:43], v105 offset:64
	ds_read_b128 v[56:59], v103 offset:64
	ds_read_b128 v[60:63], v105 offset:8768
	s_branch .Lic1_s30

.Lic1_s30:
	ds_read_b128 v[64:67], v105 offset:17472
	s_waitcnt lgkmcnt(2)
	v_mfma_f32_16x16x32_f16 v[36:39], v[40:43], v[56:59], v[36:39]
	v_cmp_lt_i32_e32 vcc, 8, v108
	s_cmp_lg_u64 vcc, 0
	v_add_u32_dpp v32, v85, v102 row_newbcast:0 row_mask:0xf bank_mask:0x3
	v_add_u32_dpp v32, v85, v102 row_newbcast:8 row_mask:0xf bank_mask:0xc
	s_waitcnt lgkmcnt(1)
	v_mfma_f32_16x16x32_f16 v[40:43], v[60:63], v[56:59], v[44:47]
	ds_read_b128 v[60:63], v105 offset:26176
	ds_read_b128 v[68:71], v32 offset:52240
	s_waitcnt lgkmcnt(2)
	v_mfma_f32_16x16x32_f16 v[44:47], v[64:67], v[56:59], v[48:51]
	v_add_u32_dpp v64, v85, v102 row_newbcast:1 row_mask:0xf bank_mask:0x3
	s_branch .Lic1_s31

.Lic1_s31:
	v_add_u32_dpp v64, v85, v102 row_newbcast:9 row_mask:0xf bank_mask:0xc
	s_cselect_b64 s[22:23], -1, 0
	v_cmp_lt_i32_e64 s[6:7], 12, v108
	s_waitcnt lgkmcnt(1)
	v_mfma_f32_16x16x32_f16 v[48:51], v[60:63], v[56:59], v[52:55]
	v_add_u32_dpp v32, v85, v102 row_newbcast:2 row_mask:0xf bank_mask:0x3
	v_add_u32_dpp v32, v85, v102 row_newbcast:10 row_mask:0xf bank_mask:0xc
	s_nop 0
	ds_read_b128 v[76:79], v64 offset:52240
	ds_read_b128 v[72:75], v32 offset:52240
	v_add_u32_dpp v32, v85, v102 row_newbcast:3 row_mask:0xf bank_mask:0x3
	v_add_u32_dpp v32, v85, v102 row_newbcast:11 row_mask:0xf bank_mask:0xc
	v_add_u32_dpp v52, v85, v102 row_newbcast:4 row_mask:0xf bank_mask:0x3
	v_add_u32_dpp v52, v85, v102 row_newbcast:12 row_mask:0xf bank_mask:0xc
	s_branch .Lic1_s32

.Lic1_s32:
	ds_read_b128 v[80:83], v32 offset:52240
	ds_read_b128 v[52:55], v52 offset:52240
	v_add_u32_dpp v56, v85, v102 row_newbcast:5 row_mask:0xf bank_mask:0x3
	v_add_u32_dpp v56, v85, v102 row_newbcast:13 row_mask:0xf bank_mask:0xc
	v_add_u32_dpp v57, v85, v102 row_newbcast:6 row_mask:0xf bank_mask:0x3
	v_add_u32_dpp v57, v85, v102 row_newbcast:14 row_mask:0xf bank_mask:0xc
	ds_read_b128 v[60:63], v56 offset:52240
	ds_read_b128 v[64:67], v57 offset:52240
	v_add_u32_dpp v32, v85, v102 row_newbcast:7 row_mask:0xf bank_mask:0x3
	v_add_u32_dpp v32, v85, v102 row_newbcast:15 row_mask:0xf bank_mask:0xc
	ds_read_b128 v[56:59], v32 offset:52240
	s_cbranch_vccz .LBB4_63
	v_add_u32_dpp v0, v84, v102 row_newbcast:0 row_mask:0xf bank_mask:0x3
	v_add_u32_dpp v0, v84, v102 row_newbcast:8 row_mask:0xf bank_mask:0xc
	s_branch .Lic1_s33

.Lic1_s33:
	v_add_u32_dpp v8, v84, v102 row_newbcast:1 row_mask:0xf bank_mask:0x3
	v_add_u32_dpp v8, v84, v102 row_newbcast:9 row_mask:0xf bank_mask:0xc
	v_add_u32_dpp v16, v84, v102 row_newbcast:2 row_mask:0xf bank_mask:0x3
	v_add_u32_dpp v16, v84, v102 row_newbcast:10 row_mask:0xf bank_mask:0xc
	v_add_u32_dpp v24, v84, v102 row_newbcast:3 row_mask:0xf bank_mask:0x3
	v_add_u32_dpp v24, v84, v102 row_newbcast:11 row_mask:0xf bank_mask:0xc
	ds_read_b128 v[0:3], v0 offset:52240
	ds_read_b128 v[8:11], v8 offset:52240
	ds_read_b128 v[16:19], v16 offset:52240
	ds_read_b128 v[24:27], v24 offset:52240
.LBB4_63:
	s_cmp_lg_u64 s[6:7], 0
	s_cselect_b64 s[26:27], -1, 0
	s_cmp_eq_u64 s[6:7], 0
	s_cbranch_scc1 .LBB4_65
	v_add_u32_dpp v4, v84, v102 row_newbcast:4 row_mask:0xf bank_mask:0x3
	s_branch .Lic1_s34

.Lic1_s34:
	v_add_u32_dpp v4, v84, v102 row_newbcast:12 row_mask:0xf bank_mask:0xc
	v_add_u32_dpp v12, v84, v102 row_newbcast:5 row_mask:0xf bank_mask:0x3
	v_add_u32_dpp v12, v84, v102 row_newbcast:13 row_mask:0xf bank_mask:0xc
	v_add_u32_dpp v20, v84, v102 row_newbcast:6 row_mask:0xf bank_mask:0x3
	v_add_u32_dpp v20, v84, v102 row_newbcast:14 row_mask:0xf bank_mask:0xc
	v_add_u32_dpp v28, v84, v102 row_newbcast:7 row_mask:0xf bank_mask:0x3
	v_add_u32_dpp v28, v84, v102 row_newbcast:15 row_mask:0xf bank_mask:0xc
	ds_read_b128 v[4:7], v4 offset:52240
	ds_read_b128 v[12:15], v12 offset:52240
	ds_read_b128 v[20:23], v20 offset:52240
	ds_read_b128 v[28:31], v28 offset:52240
.LBB4_65:
	v_cvt_f32_i32_e32 v32, v108
	v_max_f32_e32 v32, 1.0, v32
	v_div_scale_f32 v84, s[6:7], v32, v32, 1.0
	s_branch .Lic1_s35

.Lic1_s35:
	v_rcp_f32_e32 v85, v84
	v_div_scale_f32 v86, vcc, 1.0, v32, 1.0
	v_fma_f32 v87, -v84, v85, 1.0
	v_fmac_f32_e32 v85, v87, v85
	v_mul_f32_e32 v87, v86, v85
	v_fma_f32 v110, -v84, v87, v86
	v_fmac_f32_e32 v87, v110, v85
	v_fma_f32 v84, -v84, v87, v86
	v_div_fmas_f32 v84, v84, v85, v87
	v_div_fixup_f32 v32, v84, v32, 1.0
	v_cvt_f16_f32_e32 v84, v32
	v_cvt_pk_f16_f32 v32, v32, v32
	s_andn2_b64 vcc, exec, s[22:23]
	s_waitcnt lgkmcnt(7)
	s_branch .Lic1_s36

.Lic1_s36:
	v_pk_fma_f16 v68, v84, v68, 0 op_sel_hi:[0,1,1]
	v_pk_fma_f16 v69, v84, v69, 0 op_sel_hi:[0,1,1]
	v_pk_fma_f16 v70, v84, v70, 0 op_sel_hi:[0,1,1]
	v_pk_fma_f16 v71, v84, v71, 0 op_sel_hi:[0,1,1]
	s_waitcnt lgkmcnt(6)
	v_pk_fma_f16 v71, v84, v79, v71 op_sel_hi:[0,1,1]
	v_pk_fma_f16 v70, v84, v78, v70 op_sel_hi:[0,1,1]
	v_pk_fma_f16 v69, v84, v77, v69 op_sel_hi:[0,1,1]
	v_pk_fma_f16 v68, v84, v76, v68 op_sel_hi:[0,1,1]
	s_waitcnt lgkmcnt(5)
	v_pk_fma_f16 v68, v84, v72, v68 op_sel_hi:[0,1,1]
	v_pk_fma_f16 v69, v84, v73, v69 op_sel_hi:[0,1,1]
	v_pk_fma_f16 v70, v84, v74, v70 op_sel_hi:[0,1,1]
	v_pk_fma_f16 v71, v84, v75, v71 op_sel_hi:[0,1,1]
	s_branch .Lic1_s37

.Lic1_s37:
	s_waitcnt lgkmcnt(4)
	v_pk_fma_f16 v71, v84, v83, v71 op_sel_hi:[0,1,1]
	v_pk_fma_f16 v70, v84, v82, v70 op_sel_hi:[0,1,1]
	v_pk_fma_f16 v69, v84, v81, v69 op_sel_hi:[0,1,1]
	v_pk_fma_f16 v68, v84, v80, v68 op_sel_hi:[0,1,1]
	s_waitcnt lgkmcnt(3)
	v_pk_fma_f16 v68, v84, v52, v68 op_sel_hi:[0,1,1]
	v_pk_fma_f16 v69, v84, v53, v69 op_sel_hi:[0,1,1]
	v_pk_fma_f16 v70, v84, v54, v70 op_sel_hi:[0,1,1]
	v_pk_fma_f16 v71, v84, v55, v71 op_sel_hi:[0,1,1]
	s_waitcnt lgkmcnt(2)
	v_pk_fma_f16 v71, v84, v63, v71 op_sel_hi:[0,1,1]
	v_pk_fma_f16 v70, v84, v62, v70 op_sel_hi:[0,1,1]
	v_pk_fma_f16 v69, v84, v61, v69 op_sel_hi:[0,1,1]
	s_branch .Lic1_s38

.Lic1_s38:
	v_pk_fma_f16 v68, v84, v60, v68 op_sel_hi:[0,1,1]
	s_waitcnt lgkmcnt(1)
	v_pk_fma_f16 v68, v84, v64, v68 op_sel_hi:[0,1,1]
	v_pk_fma_f16 v69, v84, v65, v69 op_sel_hi:[0,1,1]
	v_pk_fma_f16 v70, v84, v66, v70 op_sel_hi:[0,1,1]
	v_pk_fma_f16 v71, v84, v67, v71 op_sel_hi:[0,1,1]
	s_waitcnt lgkmcnt(0)
	v_pk_fma_f16 v71, v84, v59, v71 op_sel_hi:[0,1,1]
	v_pk_fma_f16 v70, v84, v58, v70 op_sel_hi:[0,1,1]
	v_pk_fma_f16 v69, v84, v57, v69 op_sel_hi:[0,1,1]
	v_pk_fma_f16 v68, v84, v56, v68 op_sel_hi:[0,1,1]
	s_cbranch_vccnz .LBB4_67
	v_pk_fma_f16 v68, v32, v0, v68
	v_pk_fma_f16 v69, v32, v1, v69
	s_branch .Lic1_s39

.Lic1_s39:
	v_pk_fma_f16 v70, v32, v2, v70
	v_pk_fma_f16 v71, v32, v3, v71
	v_pk_fma_f16 v70, v32, v10, v70
	v_pk_fma_f16 v71, v32, v11, v71
	v_pk_fma_f16 v69, v32, v9, v69
	v_pk_fma_f16 v68, v32, v8, v68
	v_pk_fma_f16 v69, v32, v17, v69
	v_pk_fma_f16 v68, v32, v16, v68
	v_pk_fma_f16 v70, v32, v18, v70
	v_pk_fma_f16 v71, v32, v19, v71
	v_pk_fma_f16 v70, v32, v26, v70
	v_pk_fma_f16 v71, v32, v27, v71
	v_pk_fma_f16 v69, v32, v25, v69
	v_pk_fma_f16 v68, v32, v24, v68
.LBB4_67:
	s_andn2_b64 vcc, exec, s[26:27]
	s_branch .Lic1_s40

.Lic1_s40:
	s_cbranch_vccnz .LBB4_69
	v_pk_fma_f16 v68, v32, v4, v68
	v_pk_fma_f16 v69, v32, v5, v69
	v_pk_fma_f16 v70, v32, v6, v70
	v_pk_fma_f16 v71, v32, v7, v71
	v_pk_fma_f16 v70, v32, v14, v70
	v_pk_fma_f16 v71, v32, v15, v71
	v_pk_fma_f16 v69, v32, v13, v69
	v_pk_fma_f16 v68, v32, v12, v68
	v_pk_fma_f16 v69, v32, v21, v69
	v_pk_fma_f16 v68, v32, v20, v68
	v_pk_fma_f16 v70, v32, v22, v70
	v_pk_fma_f16 v71, v32, v23, v71
	v_pk_fma_f16 v70, v32, v30, v70
	s_branch .Lic1_s41

.Lic1_s41:
	v_pk_fma_f16 v71, v32, v31, v71
	v_pk_fma_f16 v69, v32, v29, v69
	v_pk_fma_f16 v68, v32, v28, v68
.LBB4_69:
	v_cmp_lt_i32_e32 vcc, 16, v108
	s_cbranch_vccz .LBB4_80
	v_cmp_lt_i32_e32 vcc, 20, v108
	v_add_u32_dpp v72, v109, v102 row_newbcast:0 row_mask:0xf bank_mask:0x3
	v_add_u32_dpp v72, v109, v102 row_newbcast:8 row_mask:0xf bank_mask:0xc
	v_add_u32_dpp v73, v109, v102 row_newbcast:1 row_mask:0xf bank_mask:0x3
	v_add_u32_dpp v73, v109, v102 row_newbcast:9 row_mask:0xf bank_mask:0xc
	ds_read_b128 v[84:87], v72 offset:52240
	ds_read_b128 v[80:83], v73 offset:52240
	v_add_u32_dpp v72, v109, v102 row_newbcast:2 row_mask:0xf bank_mask:0x3
	v_add_u32_dpp v72, v109, v102 row_newbcast:10 row_mask:0xf bank_mask:0xc
	s_branch .Lic1_s42

.Lic1_s42:
	v_add_u32_dpp v73, v109, v102 row_newbcast:3 row_mask:0xf bank_mask:0x3
	v_add_u32_dpp v73, v109, v102 row_newbcast:11 row_mask:0xf bank_mask:0xc
	ds_read_b128 v[76:79], v72 offset:52240
	ds_read_b128 v[72:75], v73 offset:52240
	s_cmp_lg_u64 vcc, 0
	s_cselect_b64 s[6:7], -1, 0
	s_cbranch_vccz .LBB4_72
	v_add_u32_dpp v52, v109, v102 row_newbcast:4 row_mask:0xf bank_mask:0x3
	v_add_u32_dpp v52, v109, v102 row_newbcast:12 row_mask:0xf bank_mask:0xc
	v_add_u32_dpp v58, v109, v102 row_newbcast:5 row_mask:0xf bank_mask:0x3
	v_add_u32_dpp v58, v109, v102 row_newbcast:13 row_mask:0xf bank_mask:0xc
	v_add_u32_dpp v56, v109, v102 row_newbcast:6 row_mask:0xf bank_mask:0x3
	v_add_u32_dpp v56, v109, v102 row_newbcast:14 row_mask:0xf bank_mask:0xc
	v_add_u32_dpp v57, v109, v102 row_newbcast:7 row_mask:0xf bank_mask:0x3
	s_branch .Lic1_s43

.Lic1_s43:
	v_add_u32_dpp v57, v109, v102 row_newbcast:15 row_mask:0xf bank_mask:0xc
	ds_read_b128 v[52:55], v52 offset:52240
	ds_read_b128 v[60:63], v58 offset:52240
	ds_read_b128 v[64:67], v56 offset:52240
	ds_read_b128 v[56:59], v57 offset:52240
.LBB4_72:
	s_waitcnt lgkmcnt(3)
	v_pk_fma_f16 v68, v32, v84, v68
	v_pk_fma_f16 v69, v32, v85, v69
	v_pk_fma_f16 v70, v32, v86, v70
	v_pk_fma_f16 v71, v32, v87, v71
	s_waitcnt lgkmcnt(2)
	v_pk_fma_f16 v70, v32, v82, v70
	v_pk_fma_f16 v71, v32, v83, v71
	v_pk_fma_f16 v69, v32, v81, v69
	s_branch .Lic1_s44

.Lic1_s44:
	v_pk_fma_f16 v68, v32, v80, v68
	s_waitcnt lgkmcnt(1)
	v_pk_fma_f16 v69, v32, v77, v69
	v_pk_fma_f16 v68, v32, v76, v68
	v_pk_fma_f16 v70, v32, v78, v70
	v_pk_fma_f16 v71, v32, v79, v71
	s_waitcnt lgkmcnt(0)
	v_pk_fma_f16 v70, v32, v74, v70
	v_pk_fma_f16 v71, v32, v75, v71
	v_pk_fma_f16 v69, v32, v73, v69
	s_andn2_b64 vcc, exec, s[6:7]
	v_pk_fma_f16 v68, v32, v72, v68
	s_cbranch_vccnz .LBB4_74
	v_pk_fma_f16 v52, v32, v52, v68
	s_branch .Lic1_s45

.Lic1_s45:
	v_pk_fma_f16 v53, v32, v53, v69
	v_pk_fma_f16 v54, v32, v54, v70
	v_pk_fma_f16 v55, v32, v55, v71
	v_pk_fma_f16 v54, v32, v62, v54
	v_pk_fma_f16 v55, v32, v63, v55
	v_pk_fma_f16 v53, v32, v61, v53
	v_pk_fma_f16 v52, v32, v60, v52
	v_pk_fma_f16 v53, v32, v65, v53
	v_pk_fma_f16 v52, v32, v64, v52
	v_pk_fma_f16 v54, v32, v66, v54
	v_pk_fma_f16 v55, v32, v67, v55
	v_pk_fma_f16 v70, v32, v58, v54
	v_pk_fma_f16 v71, v32, v59, v55
	v_pk_fma_f16 v69, v32, v57, v53
	s_branch .Lic1_s46

.Lic1_s46:
	v_pk_fma_f16 v68, v32, v56, v52

.LBB4_75:
	s_waitcnt lgkmcnt(0)
	s_or_b64 exec, exec, s[6:7]
	s_nop 1
	v_add_u32_dpp v53, v52, v102 row_newbcast:0 row_mask:0xf bank_mask:0x3
	v_add_u32_dpp v53, v52, v102 row_newbcast:8 row_mask:0xf bank_mask:0xc
	v_add_u32_dpp v58, v52, v102 row_newbcast:1 row_mask:0xf bank_mask:0x3
	v_add_u32_dpp v58, v52, v102 row_newbcast:9 row_mask:0xf bank_mask:0xc
	ds_read_b128 v[54:57], v53 offset:52240
	ds_read_b128 v[58:61], v58 offset:52240
	v_add_u32_dpp v53, v52, v102 row_newbcast:2 row_mask:0xf bank_mask:0x3
	s_branch .Lic1_s47

.Lic1_s47:
	v_add_u32_dpp v53, v52, v102 row_newbcast:10 row_mask:0xf bank_mask:0xc
	v_add_u32_dpp v67, v52, v102 row_newbcast:3 row_mask:0xf bank_mask:0x3
	v_add_u32_dpp v67, v52, v102 row_newbcast:11 row_mask:0xf bank_mask:0xc
	v_mov_b32_dpp v76, v52 row_newbcast:5 row_mask:0xf bank_mask:0x3
	v_mov_b32_dpp v76, v52 row_newbcast:13 row_mask:0xf bank_mask:0xc
	ds_read_b128 v[62:65], v53 offset:52240
	ds_read_b128 v[72:75], v67 offset:52240
	v_add_u32_dpp v53, v52, v102 row_newbcast:4 row_mask:0xf bank_mask:0x3
	v_add_u32_dpp v53, v52, v102 row_newbcast:12 row_mask:0xf bank_mask:0xc
	v_mov_b32_dpp v66, v52 row_newbcast:6 row_mask:0xf bank_mask:0x3
	v_mov_b32_dpp v66, v52 row_newbcast:14 row_mask:0xf bank_mask:0xc
	v_mov_b32_dpp v52, v52 row_newbcast:7 row_mask:0xf bank_mask:0x3
	s_nop 1
	v_mov_b32_dpp v52, v52 row_newbcast:15 row_mask:0xf bank_mask:0xc
	s_branch .Lic1_s48

.Lic1_s48:
	v_add_u32_e32 v67, v102, v76
	ds_read_b128 v[76:79], v53 offset:52240
	ds_read_b128 v[80:83], v67 offset:52240
	s_add_i32 s22, s22, 8
	v_add_u32_e32 v53, v102, v66
	v_add_u32_e32 v52, v102, v52
	ds_read_b128 v[84:87], v53 offset:52240
	ds_read_b128 v[110:113], v52 offset:52240
	s_waitcnt lgkmcnt(7)
	v_pk_fma_f16 v52, v32, v54, v68
	v_pk_fma_f16 v53, v32, v55, v69
	v_pk_fma_f16 v54, v32, v56, v70
	v_pk_fma_f16 v55, v32, v57, v71
	s_waitcnt lgkmcnt(6)
	s_branch .Lic1_s49

.Lic1_s49:
	v_pk_fma_f16 v54, v32, v60, v54
	v_pk_fma_f16 v55, v32, v61, v55
	v_pk_fma_f16 v53, v32, v59, v53
	v_pk_fma_f16 v52, v32, v58, v52
	s_waitcnt lgkmcnt(5)
	v_pk_fma_f16 v53, v32, v63, v53
	v_pk_fma_f16 v52, v32, v62, v52
	v_pk_fma_f16 v54, v32, v64, v54
	v_pk_fma_f16 v55, v32, v65, v55
	s_waitcnt lgkmcnt(4)
	v_pk_fma_f16 v54, v32, v74, v54
	v_pk_fma_f16 v55, v32, v75, v55
	v_pk_fma_f16 v53, v32, v73, v53
	v_pk_fma_f16 v52, v32, v72, v52
	s_branch .Lic1_s50

.Lic1_s50:
	s_waitcnt lgkmcnt(3)
	v_pk_fma_f16 v53, v32, v77, v53
	v_pk_fma_f16 v52, v32, v76, v52
	v_pk_fma_f16 v54, v32, v78, v54
	v_pk_fma_f16 v55, v32, v79, v55
	s_waitcnt lgkmcnt(2)
	v_pk_fma_f16 v54, v32, v82, v54
	v_pk_fma_f16 v55, v32, v83, v55
	v_pk_fma_f16 v53, v32, v81, v53
	v_pk_fma_f16 v52, v32, v80, v52
	s_waitcnt lgkmcnt(1)
	v_pk_fma_f16 v53, v32, v85, v53
	v_pk_fma_f16 v52, v32, v84, v52
	v_pk_fma_f16 v54, v32, v86, v54
	s_branch .Lic1_s51

.Lic1_s51:
	v_pk_fma_f16 v55, v32, v87, v55
	s_waitcnt lgkmcnt(0)
	v_pk_fma_f16 v70, v32, v112, v54
	v_pk_fma_f16 v71, v32, v113, v55
	v_pk_fma_f16 v69, v32, v111, v53
	v_pk_fma_f16 v68, v32, v110, v52
.LBB4_76:
	s_waitcnt lgkmcnt(0)
	v_cmp_lt_i32_e32 vcc, s22, v108
	s_cbranch_vccz .LBB4_79
	v_add_u32_e32 v52, s22, v97
	v_cmp_lt_i32_e32 vcc, v52, v108
	v_mov_b32_e32 v52, 0x10000
	s_and_saveexec_b64 s[6:7], vcc
	s_cbranch_execz .LBB4_75
	v_add_u32_e32 v52, s22, v33
	s_branch .Lic1_s52

.Lic1_s52:
	v_ashrrev_i32_e32 v53, 31, v52
	v_lshl_add_u64 v[52:53], v[52:53], 2, s[12:13]
	global_load_dword v52, v[52:53], off
	s_waitcnt vmcnt(0)
	v_lshrrev_b32_e32 v52, 10, v52
	v_and_b32_e32 v52, 0x3fff80, v52
	s_branch .LBB4_75

.LBB4_80:
	ds_write_b128 v104, v[68:71]
	ds_read_b128 v[52:55], v105 offset:128
	ds_read_b128 v[56:59], v103
	ds_read_b128 v[60:63], v105 offset:8832
	s_waitcnt lgkmcnt(1)
	v_mfma_f32_16x16x32_f16 v[36:39], v[52:55], v[56:59], v[36:39]
	s_branch .Lic1_s53

.Lic1_s53:
	ds_read_b128 v[52:55], v105 offset:17536
	s_waitcnt lgkmcnt(1)
	v_mfma_f32_16x16x32_f16 v[40:43], v[60:63], v[56:59], v[40:43]
	s_waitcnt lgkmcnt(0)
	v_mfma_f32_16x16x32_f16 v[44:47], v[52:55], v[56:59], v[44:47]
	ds_read_b128 v[52:55], v105 offset:26240
	s_waitcnt lgkmcnt(0)
	v_mfma_f32_16x16x32_f16 v[48:51], v[52:55], v[56:59], v[48:51]
	ds_read_b128 v[52:55], v105 offset:192
	ds_read_b128 v[56:59], v103 offset:64
	ds_read_b128 v[60:63], v105 offset:8896
	v_cmp_lt_i32_e32 vcc, 8, v35
	s_waitcnt lgkmcnt(1)
	v_mfma_f32_16x16x32_f16 v[36:39], v[52:55], v[56:59], v[36:39]
	s_branch .Lic1_s54

.Lic1_s54:
	ds_read_b128 v[52:55], v105 offset:17600
	v_add_u32_dpp v32, v107, v102 row_newbcast:0 row_mask:0xf bank_mask:0x3
	v_add_u32_dpp v32, v107, v102 row_newbcast:8 row_mask:0xf bank_mask:0xc
	ds_read_b128 v[68:71], v32 offset:52240
	s_waitcnt lgkmcnt(2)
	v_mfma_f32_16x16x32_f16 v[40:43], v[60:63], v[56:59], v[40:43]
	ds_read_b128 v[60:63], v105 offset:26304
	v_add_u32_dpp v33, v107, v102 row_newbcast:1 row_mask:0xf bank_mask:0x3
	v_add_u32_dpp v33, v107, v102 row_newbcast:9 row_mask:0xf bank_mask:0xc
	s_cmp_lg_u64 vcc, 0
	s_waitcnt lgkmcnt(2)
	v_mfma_f32_16x16x32_f16 v[44:47], v[52:55], v[56:59], v[44:47]
	v_add_u32_dpp v32, v107, v102 row_newbcast:2 row_mask:0xf bank_mask:0x3
	v_add_u32_dpp v32, v107, v102 row_newbcast:10 row_mask:0xf bank_mask:0xc
	s_branch .Lic1_s55

.Lic1_s55:
	ds_read_b128 v[76:79], v33 offset:52240
	ds_read_b128 v[72:75], v32 offset:52240
	s_waitcnt lgkmcnt(2)
	v_mfma_f32_16x16x32_f16 v[48:51], v[60:63], v[56:59], v[48:51]
	v_add_u32_dpp v32, v107, v102 row_newbcast:3 row_mask:0xf bank_mask:0x3
	v_add_u32_dpp v32, v107, v102 row_newbcast:11 row_mask:0xf bank_mask:0xc
	v_add_u32_dpp v33, v107, v102 row_newbcast:4 row_mask:0xf bank_mask:0x3
	v_add_u32_dpp v33, v107, v102 row_newbcast:12 row_mask:0xf bank_mask:0xc
	ds_read_b128 v[80:83], v32 offset:52240
	ds_read_b128 v[52:55], v33 offset:52240
	s_cselect_b64 s[22:23], -1, 0
	v_add_u32_dpp v33, v107, v102 row_newbcast:5 row_mask:0xf bank_mask:0x3
	v_add_u32_dpp v33, v107, v102 row_newbcast:13 row_mask:0xf bank_mask:0xc
	v_add_u32_dpp v56, v107, v102 row_newbcast:6 row_mask:0xf bank_mask:0x3
	s_branch .Lic1_s56

.Lic1_s56:
	v_add_u32_dpp v56, v107, v102 row_newbcast:14 row_mask:0xf bank_mask:0xc
	ds_read_b128 v[60:63], v33 offset:52240
	ds_read_b128 v[64:67], v56 offset:52240
	v_add_u32_dpp v32, v107, v102 row_newbcast:7 row_mask:0xf bank_mask:0x3
	v_add_u32_dpp v32, v107, v102 row_newbcast:15 row_mask:0xf bank_mask:0xc
	ds_read_b128 v[56:59], v32 offset:52240
	v_cmp_lt_i32_e64 s[6:7], 12, v35
	s_cbranch_vccz .LBB4_82
	v_add_u32_dpp v0, v106, v102 row_newbcast:0 row_mask:0xf bank_mask:0x3
	v_add_u32_dpp v0, v106, v102 row_newbcast:8 row_mask:0xf bank_mask:0xc
	v_add_u32_dpp v8, v106, v102 row_newbcast:1 row_mask:0xf bank_mask:0x3
	v_add_u32_dpp v8, v106, v102 row_newbcast:9 row_mask:0xf bank_mask:0xc
	v_add_u32_dpp v16, v106, v102 row_newbcast:2 row_mask:0xf bank_mask:0x3
	v_add_u32_dpp v16, v106, v102 row_newbcast:10 row_mask:0xf bank_mask:0xc
	s_branch .Lic1_s57

.Lic1_s57:
	v_add_u32_dpp v24, v106, v102 row_newbcast:3 row_mask:0xf bank_mask:0x3
	v_add_u32_dpp v24, v106, v102 row_newbcast:11 row_mask:0xf bank_mask:0xc
	ds_read_b128 v[0:3], v0 offset:52240
	ds_read_b128 v[8:11], v8 offset:52240
	ds_read_b128 v[16:19], v16 offset:52240
	ds_read_b128 v[24:27], v24 offset:52240
.LBB4_82:
	s_cmp_lg_u64 s[6:7], 0
	s_cselect_b64 s[26:27], -1, 0
	s_cmp_eq_u64 s[6:7], 0
	s_cbranch_scc1 .LBB4_84
	v_add_u32_dpp v4, v106, v102 row_newbcast:4 row_mask:0xf bank_mask:0x3
	v_add_u32_dpp v4, v106, v102 row_newbcast:12 row_mask:0xf bank_mask:0xc
	v_add_u32_dpp v12, v106, v102 row_newbcast:5 row_mask:0xf bank_mask:0x3
	v_add_u32_dpp v12, v106, v102 row_newbcast:13 row_mask:0xf bank_mask:0xc
	s_branch .Lic1_s58

.Lic1_s58:
	v_add_u32_dpp v20, v106, v102 row_newbcast:6 row_mask:0xf bank_mask:0x3
	v_add_u32_dpp v20, v106, v102 row_newbcast:14 row_mask:0xf bank_mask:0xc
	v_add_u32_dpp v28, v106, v102 row_newbcast:7 row_mask:0xf bank_mask:0x3
	v_add_u32_dpp v28, v106, v102 row_newbcast:15 row_mask:0xf bank_mask:0xc
	ds_read_b128 v[4:7], v4 offset:52240
	ds_read_b128 v[12:15], v12 offset:52240
	ds_read_b128 v[20:23], v20 offset:52240
	ds_read_b128 v[28:31], v28 offset:52240
.LBB4_84:
	v_cvt_f32_i32_e32 v32, v35
	v_max_f32_e32 v32, 1.0, v32
	v_div_scale_f32 v33, s[6:7], v32, v32, 1.0
	v_rcp_f32_e32 v84, v33
	v_div_scale_f32 v85, vcc, 1.0, v32, 1.0
	v_fma_f32 v86, -v33, v84, 1.0
	s_branch .Lic1_s59

.Lic1_s59:
	v_fmac_f32_e32 v84, v86, v84
	v_mul_f32_e32 v86, v85, v84
	v_fma_f32 v87, -v33, v86, v85
	v_fmac_f32_e32 v86, v87, v84
	v_fma_f32 v33, -v33, v86, v85
	v_div_fmas_f32 v33, v33, v84, v86
	v_div_fixup_f32 v32, v33, v32, 1.0
	v_cvt_f16_f32_e32 v33, v32
	v_cvt_pk_f16_f32 v32, v32, v32
	s_andn2_b64 vcc, exec, s[22:23]
	v_pk_fma_f16 v68, v33, v68, 0 op_sel_hi:[0,1,1]
	v_pk_fma_f16 v69, v33, v69, 0 op_sel_hi:[0,1,1]
	v_pk_fma_f16 v70, v33, v70, 0 op_sel_hi:[0,1,1]
	v_pk_fma_f16 v71, v33, v71, 0 op_sel_hi:[0,1,1]
	s_branch .Lic1_s60

.Lic1_s60:
	s_waitcnt lgkmcnt(6)
	v_pk_fma_f16 v71, v33, v79, v71 op_sel_hi:[0,1,1]
	v_pk_fma_f16 v70, v33, v78, v70 op_sel_hi:[0,1,1]
	v_pk_fma_f16 v69, v33, v77, v69 op_sel_hi:[0,1,1]
	v_pk_fma_f16 v68, v33, v76, v68 op_sel_hi:[0,1,1]
	s_waitcnt lgkmcnt(5)
	v_pk_fma_f16 v68, v33, v72, v68 op_sel_hi:[0,1,1]
	v_pk_fma_f16 v69, v33, v73, v69 op_sel_hi:[0,1,1]
	v_pk_fma_f16 v70, v33, v74, v70 op_sel_hi:[0,1,1]
	v_pk_fma_f16 v71, v33, v75, v71 op_sel_hi:[0,1,1]
	s_waitcnt lgkmcnt(4)
	v_pk_fma_f16 v71, v33, v83, v71 op_sel_hi:[0,1,1]
	v_pk_fma_f16 v70, v33, v82, v70 op_sel_hi:[0,1,1]
	v_pk_fma_f16 v69, v33, v81, v69 op_sel_hi:[0,1,1]
	s_branch .Lic1_s61

.Lic1_s61:
	v_pk_fma_f16 v68, v33, v80, v68 op_sel_hi:[0,1,1]
	s_waitcnt lgkmcnt(3)
	v_pk_fma_f16 v68, v33, v52, v68 op_sel_hi:[0,1,1]
	v_pk_fma_f16 v69, v33, v53, v69 op_sel_hi:[0,1,1]
	v_pk_fma_f16 v70, v33, v54, v70 op_sel_hi:[0,1,1]
	v_pk_fma_f16 v71, v33, v55, v71 op_sel_hi:[0,1,1]
	s_waitcnt lgkmcnt(2)
	v_pk_fma_f16 v71, v33, v63, v71 op_sel_hi:[0,1,1]
	v_pk_fma_f16 v70, v33, v62, v70 op_sel_hi:[0,1,1]
	v_pk_fma_f16 v69, v33, v61, v69 op_sel_hi:[0,1,1]
	v_pk_fma_f16 v68, v33, v60, v68 op_sel_hi:[0,1,1]
	s_waitcnt lgkmcnt(1)
	v_pk_fma_f16 v68, v33, v64, v68 op_sel_hi:[0,1,1]
	v_pk_fma_f16 v69, v33, v65, v69 op_sel_hi:[0,1,1]
	s_branch .Lic1_s62

.Lic1_s62:
	v_pk_fma_f16 v70, v33, v66, v70 op_sel_hi:[0,1,1]
	v_pk_fma_f16 v71, v33, v67, v71 op_sel_hi:[0,1,1]
	s_waitcnt lgkmcnt(0)
	v_pk_fma_f16 v71, v33, v59, v71 op_sel_hi:[0,1,1]
	v_pk_fma_f16 v70, v33, v58, v70 op_sel_hi:[0,1,1]
	v_pk_fma_f16 v69, v33, v57, v69 op_sel_hi:[0,1,1]
	v_pk_fma_f16 v68, v33, v56, v68 op_sel_hi:[0,1,1]
	s_cbranch_vccnz .LBB4_86
	v_pk_fma_f16 v33, v32, v0, v68
	v_pk_fma_f16 v68, v32, v1, v69
	v_pk_fma_f16 v69, v32, v2, v70
	v_pk_fma_f16 v70, v32, v3, v71
	v_pk_fma_f16 v69, v32, v10, v69
	v_pk_fma_f16 v70, v32, v11, v70
	s_branch .Lic1_s63

.Lic1_s63:
	v_pk_fma_f16 v68, v32, v9, v68
	v_pk_fma_f16 v33, v32, v8, v33
	v_pk_fma_f16 v68, v32, v17, v68
	v_pk_fma_f16 v33, v32, v16, v33
	v_pk_fma_f16 v69, v32, v18, v69
	v_pk_fma_f16 v70, v32, v19, v70
	s_nop 0
	v_pk_fma_f16 v71, v32, v27, v70
	v_pk_fma_f16 v70, v32, v26, v69
	v_pk_fma_f16 v69, v32, v25, v68
	v_pk_fma_f16 v68, v32, v24, v33
.LBB4_86:
	s_andn2_b64 vcc, exec, s[26:27]
	s_cbranch_vccnz .LBB4_88
	v_pk_fma_f16 v33, v32, v4, v68
	s_branch .Lic1_s64

.Lic1_s64:
	v_pk_fma_f16 v68, v32, v5, v69
	v_pk_fma_f16 v69, v32, v6, v70
	v_pk_fma_f16 v70, v32, v7, v71
	v_pk_fma_f16 v69, v32, v14, v69
	v_pk_fma_f16 v70, v32, v15, v70
	v_pk_fma_f16 v68, v32, v13, v68
	v_pk_fma_f16 v33, v32, v12, v33
	v_pk_fma_f16 v68, v32, v21, v68
	v_pk_fma_f16 v33, v32, v20, v33
	v_pk_fma_f16 v69, v32, v22, v69
	v_pk_fma_f16 v70, v32, v23, v70
	s_nop 0
	v_pk_fma_f16 v71, v32, v31, v70
	v_pk_fma_f16 v70, v32, v30, v69
	s_branch .Lic1_s65

.Lic1_s65:
	v_pk_fma_f16 v69, v32, v29, v68
	v_pk_fma_f16 v68, v32, v28, v33
.LBB4_88:
	v_cmp_lt_i32_e32 vcc, 16, v35
	s_cbranch_vccz .LBB4_99
	v_cmp_lt_i32_e32 vcc, 20, v35
	v_add_u32_dpp v33, v95, v102 row_newbcast:0 row_mask:0xf bank_mask:0x3
	v_add_u32_dpp v33, v95, v102 row_newbcast:8 row_mask:0xf bank_mask:0xc
	v_add_u32_dpp v72, v95, v102 row_newbcast:1 row_mask:0xf bank_mask:0x3
	v_add_u32_dpp v72, v95, v102 row_newbcast:9 row_mask:0xf bank_mask:0xc
	ds_read_b128 v[84:87], v33 offset:52240
	ds_read_b128 v[80:83], v72 offset:52240
	v_add_u32_dpp v33, v95, v102 row_newbcast:2 row_mask:0xf bank_mask:0x3
	v_add_u32_dpp v33, v95, v102 row_newbcast:10 row_mask:0xf bank_mask:0xc
	v_add_u32_dpp v72, v95, v102 row_newbcast:3 row_mask:0xf bank_mask:0x3
	s_branch .Lic1_s66

.Lic1_s66:
	v_add_u32_dpp v72, v95, v102 row_newbcast:11 row_mask:0xf bank_mask:0xc
	ds_read_b128 v[76:79], v33 offset:52240
	ds_read_b128 v[72:75], v72 offset:52240
	s_cmp_lg_u64 vcc, 0
	s_cselect_b64 s[6:7], -1, 0
	s_cbranch_vccz .LBB4_91
	v_add_u32_dpp v33, v95, v102 row_newbcast:4 row_mask:0xf bank_mask:0x3
	v_add_u32_dpp v33, v95, v102 row_newbcast:12 row_mask:0xf bank_mask:0xc
	v_add_u32_dpp v58, v95, v102 row_newbcast:5 row_mask:0xf bank_mask:0x3
	v_add_u32_dpp v58, v95, v102 row_newbcast:13 row_mask:0xf bank_mask:0xc
	ds_read_b128 v[52:55], v33 offset:52240
	ds_read_b128 v[60:63], v58 offset:52240
	v_add_u32_dpp v33, v95, v102 row_newbcast:6 row_mask:0xf bank_mask:0x3
	v_add_u32_dpp v33, v95, v102 row_newbcast:14 row_mask:0xf bank_mask:0xc
	s_branch .Lic1_s67

.Lic1_s67:
	v_add_u32_dpp v56, v95, v102 row_newbcast:7 row_mask:0xf bank_mask:0x3
	v_add_u32_dpp v56, v95, v102 row_newbcast:15 row_mask:0xf bank_mask:0xc
	ds_read_b128 v[64:67], v33 offset:52240
	ds_read_b128 v[56:59], v56 offset:52240
.LBB4_91:
	s_waitcnt lgkmcnt(3)
	v_pk_fma_f16 v33, v32, v84, v68
	v_pk_fma_f16 v68, v32, v85, v69
	v_pk_fma_f16 v69, v32, v86, v70
	v_pk_fma_f16 v70, v32, v87, v71
	s_waitcnt lgkmcnt(2)
	v_pk_fma_f16 v69, v32, v82, v69
	v_pk_fma_f16 v70, v32, v83, v70
	v_pk_fma_f16 v68, v32, v81, v68
	v_pk_fma_f16 v33, v32, v80, v33
	s_branch .Lic1_s68

.Lic1_s68:
	s_waitcnt lgkmcnt(1)
	v_pk_fma_f16 v68, v32, v77, v68
	v_pk_fma_f16 v33, v32, v76, v33
	v_pk_fma_f16 v69, v32, v78, v69
	v_pk_fma_f16 v70, v32, v79, v70
	s_andn2_b64 vcc, exec, s[6:7]
	s_waitcnt lgkmcnt(0)
	v_pk_fma_f16 v71, v32, v75, v70
	v_pk_fma_f16 v70, v32, v74, v69
	v_pk_fma_f16 v69, v32, v73, v68
	v_pk_fma_f16 v68, v32, v72, v33
	s_cbranch_vccnz .LBB4_93
	v_pk_fma_f16 v33, v32, v52, v68
	v_pk_fma_f16 v52, v32, v53, v69
	s_branch .Lic1_s69

.Lic1_s69:
	v_pk_fma_f16 v53, v32, v54, v70
	v_pk_fma_f16 v54, v32, v55, v71
	v_pk_fma_f16 v53, v32, v62, v53
	v_pk_fma_f16 v54, v32, v63, v54
	v_pk_fma_f16 v52, v32, v61, v52
	v_pk_fma_f16 v33, v32, v60, v33
	v_pk_fma_f16 v52, v32, v65, v52
	v_pk_fma_f16 v33, v32, v64, v33
	v_pk_fma_f16 v53, v32, v66, v53
	v_pk_fma_f16 v54, v32, v67, v54
	v_pk_fma_f16 v70, v32, v58, v53
	v_pk_fma_f16 v71, v32, v59, v54
	v_pk_fma_f16 v69, v32, v57, v52
	v_pk_fma_f16 v68, v32, v56, v33
.LBB4_93:
	v_add_u32_e32 v33, v97, v34
	s_branch .Lic1_s70

.Lic1_s70:
	s_mov_b32 s22, 24
	s_branch .LBB4_95
.LBB4_94:
	s_waitcnt lgkmcnt(0)
	s_or_b64 exec, exec, s[6:7]
	s_nop 1
	v_mov_b32_dpp v52, v34 row_newbcast:0 row_mask:0xf bank_mask:0x3
	v_mov_b32_dpp v52, v34 row_newbcast:8 row_mask:0xf bank_mask:0xc
	v_mov_b32_dpp v53, v34 row_newbcast:1 row_mask:0xf bank_mask:0x3
	v_mov_b32_dpp v53, v34 row_newbcast:9 row_mask:0xf bank_mask:0xc
	v_mov_b32_dpp v60, v34 row_newbcast:2 row_mask:0xf bank_mask:0x3
	v_mov_b32_dpp v60, v34 row_newbcast:10 row_mask:0xf bank_mask:0xc
	v_mov_b32_dpp v61, v34 row_newbcast:3 row_mask:0xf bank_mask:0x3
	v_mov_b32_dpp v61, v34 row_newbcast:11 row_mask:0xf bank_mask:0xc
	v_mov_b32_dpp v72, v34 row_newbcast:4 row_mask:0xf bank_mask:0x3
	s_branch .Lic1_s71

.Lic1_s71:
	v_mov_b32_dpp v72, v34 row_newbcast:12 row_mask:0xf bank_mask:0xc
	v_mov_b32_dpp v73, v34 row_newbcast:5 row_mask:0xf bank_mask:0x3
	v_mov_b32_dpp v73, v34 row_newbcast:13 row_mask:0xf bank_mask:0xc
	v_mov_b32_dpp v80, v34 row_newbcast:6 row_mask:0xf bank_mask:0x3
	v_mov_b32_dpp v80, v34 row_newbcast:14 row_mask:0xf bank_mask:0xc
	v_mov_b32_dpp v34, v34 row_newbcast:7 row_mask:0xf bank_mask:0x3
	s_nop 1
	v_mov_b32_dpp v34, v34 row_newbcast:15 row_mask:0xf bank_mask:0xc
	v_add_u32_e32 v52, v102, v52
	v_add_u32_e32 v56, v102, v53
	ds_read_b128 v[52:55], v52 offset:52240
	ds_read_b128 v[56:59], v56 offset:52240
	v_add_u32_e32 v60, v102, v60
	v_add_u32_e32 v64, v102, v61
	s_branch .Lic1_s72

.Lic1_s72:
	ds_read_b128 v[60:63], v60 offset:52240
	ds_read_b128 v[64:67], v64 offset:52240
	v_add_u32_e32 v72, v102, v72
	v_add_u32_e32 v76, v102, v73
	v_add_u32_e32 v80, v102, v80
	v_add_u32_e32 v34, v102, v34
	ds_read_b128 v[72:75], v72 offset:52240
	ds_read_b128 v[76:79], v76 offset:52240
	ds_read_b128 v[80:83], v80 offset:52240
	ds_read_b128 v[84:87], v34 offset:52240
	s_waitcnt lgkmcnt(7)
	v_pk_fma_f16 v34, v32, v52, v68
	v_pk_fma_f16 v52, v32, v53, v69
	v_pk_fma_f16 v53, v32, v54, v70
	s_branch .Lic1_s73

.Lic1_s73:
	v_pk_fma_f16 v54, v32, v55, v71
	s_waitcnt lgkmcnt(6)
	v_pk_fma_f16 v53, v32, v58, v53
	v_pk_fma_f16 v54, v32, v59, v54
	v_pk_fma_f16 v52, v32, v57, v52
	v_pk_fma_f16 v34, v32, v56, v34
	s_waitcnt lgkmcnt(5)
	v_pk_fma_f16 v52, v32, v61, v52
	v_pk_fma_f16 v34, v32, v60, v34
	v_pk_fma_f16 v53, v32, v62, v53
	v_pk_fma_f16 v54, v32, v63, v54
	s_waitcnt lgkmcnt(4)
	v_pk_fma_f16 v53, v32, v66, v53
	v_pk_fma_f16 v54, v32, v67, v54
	s_branch .Lic1_s74

.Lic1_s74:
	v_pk_fma_f16 v52, v32, v65, v52
	v_pk_fma_f16 v34, v32, v64, v34
	s_waitcnt lgkmcnt(3)
	v_pk_fma_f16 v52, v32, v73, v52
	v_pk_fma_f16 v34, v32, v72, v34
	v_pk_fma_f16 v53, v32, v74, v53
	v_pk_fma_f16 v54, v32, v75, v54
	s_waitcnt lgkmcnt(2)
	v_pk_fma_f16 v53, v32, v78, v53
	v_pk_fma_f16 v54, v32, v79, v54
	v_pk_fma_f16 v52, v32, v77, v52
	v_pk_fma_f16 v34, v32, v76, v34
	s_waitcnt lgkmcnt(1)
	v_pk_fma_f16 v52, v32, v81, v52
	s_branch .Lic1_s75

.Lic1_s75:
	v_pk_fma_f16 v34, v32, v80, v34
	v_pk_fma_f16 v53, v32, v82, v53
	v_pk_fma_f16 v54, v32, v83, v54
	s_waitcnt lgkmcnt(0)
	v_pk_fma_f16 v70, v32, v86, v53
	v_pk_fma_f16 v71, v32, v87, v54
	v_pk_fma_f16 v69, v32, v85, v52
	v_pk_fma_f16 v68, v32, v84, v34
	s_add_i32 s22, s22, 8
.LBB4_95:
	s_waitcnt lgkmcnt(0)
	v_cmp_lt_i32_e32 vcc, s22, v35
	s_cbranch_vccz .LBB4_98
	v_add_u32_e32 v34, s22, v97
	v_cmp_lt_i32_e32 vcc, v34, v35
	s_branch .Lic1_s76

.Lic1_s76:
	v_mov_b32_e32 v34, 0x10000
	s_and_saveexec_b64 s[6:7], vcc
	s_cbranch_execz .LBB4_94
	v_add_u32_e32 v52, s22, v33
	v_ashrrev_i32_e32 v53, 31, v52
	v_lshl_add_u64 v[52:53], v[52:53], 2, s[12:13]
	global_load_dword v34, v[52:53], off
	s_waitcnt vmcnt(0)
	v_lshrrev_b32_e32 v34, 10, v34
	v_and_b32_e32 v34, 0x3fff80, v34
	s_branch .LBB4_94

.LBB4_99:
	ds_write_b128 v104, v[68:71]
	ds_read_b128 v[32:35], v105 offset:256
	s_branch .Lic1_s77

.Lic1_s77:
	ds_read_b128 v[52:55], v103
	ds_read_b128 v[56:59], v105 offset:8960
	s_waitcnt lgkmcnt(1)
	v_mfma_f32_16x16x32_f16 v[32:35], v[32:35], v[52:55], v[36:39]
	s_nop 2
	ds_read_b128 v[36:39], v105 offset:17664
	s_waitcnt lgkmcnt(1)
	v_mfma_f32_16x16x32_f16 v[40:43], v[56:59], v[52:55], v[40:43]
	s_waitcnt lgkmcnt(0)
	v_mfma_f32_16x16x32_f16 v[44:47], v[36:39], v[52:55], v[44:47]
	ds_read_b128 v[36:39], v105 offset:26368
	s_waitcnt lgkmcnt(0)
	v_mfma_f32_16x16x32_f16 v[52:55], v[36:39], v[52:55], v[48:51]
	ds_read_b128 v[36:39], v105 offset:320
	s_branch .Lic1_s78

.Lic1_s78:
	ds_read_b128 v[56:59], v103 offset:64
	s_nop 0
	ds_read_b128 v[48:51], v105 offset:9024
	ds_read_b128 v[60:63], v105 offset:17728
	ds_read_b128 v[64:67], v105 offset:26432
	s_waitcnt lgkmcnt(3)
	v_mfma_f32_16x16x32_f16 v[32:35], v[36:39], v[56:59], v[32:35]
	s_waitcnt lgkmcnt(2)
	v_mfma_f32_16x16x32_f16 v[36:39], v[48:51], v[56:59], v[40:43]
	v_mov_b32_e32 v48, 0
	v_mov_b32_e32 v49, v48
	v_mov_b32_e32 v50, v48
	s_waitcnt lgkmcnt(1)
	v_mfma_f32_16x16x32_f16 v[40:43], v[60:63], v[56:59], v[44:47]
	s_branch .Lic1_s79

.Lic1_s79:
	v_mov_b32_e32 v51, v48
	s_waitcnt lgkmcnt(0)
	v_mfma_f32_16x16x32_f16 v[44:47], v[64:67], v[56:59], v[52:55]
	s_and_saveexec_b64 s[6:7], s[4:5]
	s_cbranch_execz .LBB4_101
	v_lshlrev_b32_e32 v48, 7, v114
	v_lshl_add_u32 v49, v115, 11, 0
	v_add3_u32 v48, v49, v48, v98
	ds_read_b128 v[48:51], v48 offset:52240
.LBB4_101:
	s_or_b64 exec, exec, s[6:7]
	s_waitcnt lgkmcnt(0)
	ds_write_b128 v104, v[48:51]
	ds_read_b128 v[48:51], v105 offset:384
	ds_read_b128 v[52:55], v103
	s_branch .Lic1_s80

.Lic1_s80:
	ds_read_b128 v[56:59], v105 offset:9088
	s_waitcnt lgkmcnt(1)
	v_mfma_f32_16x16x32_f16 v[32:35], v[48:51], v[52:55], v[32:35]
	ds_read_b128 v[48:51], v105 offset:17792
	s_waitcnt lgkmcnt(1)
	v_mfma_f32_16x16x32_f16 v[36:39], v[56:59], v[52:55], v[36:39]
	s_waitcnt lgkmcnt(0)
	v_mfma_f32_16x16x32_f16 v[56:59], v[48:51], v[52:55], v[40:43]
	s_nop 2
	ds_read_b128 v[40:43], v105 offset:26496
	s_waitcnt lgkmcnt(0)
	v_mfma_f32_16x16x32_f16 v[50:53], v[40:43], v[52:55], v[44:47]
	ds_read_b128 v[40:43], v105 offset:448
	ds_read_b128 v[60:63], v103 offset:64
	s_branch .Lic1_s81

.Lic1_s81:
	ds_read_b128 v[64:67], v105 offset:9152
	v_add_u32_e32 v48, s19, v99
	v_cmp_gt_i32_e32 vcc, s18, v48
	s_and_b64 s[4:5], s[2:3], vcc
	s_waitcnt lgkmcnt(1)
	v_mfma_f32_16x16x32_f16 v[44:47], v[40:43], v[60:63], v[32:35]
	s_mov_b64 s[6:7], s[20:21]
	s_mov_b64 s[22:23], s[24:25]
	s_nop 0
	ds_read_b128 v[32:35], v105 offset:17856
	s_waitcnt lgkmcnt(1)
	v_mfma_f32_16x16x32_f16 v[40:43], v[64:67], v[60:63], v[36:39]
	ds_read_b128 v[64:67], v105 offset:26560
	s_waitcnt lgkmcnt(1)
	s_branch .Lic1_s82

.Lic1_s82:
	v_mfma_f32_16x16x32_f16 v[36:39], v[32:35], v[60:63], v[56:59]
	s_waitcnt lgkmcnt(0)
	v_mfma_f32_16x16x32_f16 v[32:35], v[64:67], v[60:63], v[50:53]
	s_and_saveexec_b64 s[22:23], s[4:5]
	s_xor_b64 s[4:5], exec, s[22:23]
	s_cbranch_execz .LBB4_15
	v_add_u32_e32 v50, 0x1cc90, v88
	ds_read_b128 v[52:55], v50
	v_mov_b32_e32 v56, v89
	s_waitcnt lgkmcnt(0)
	v_add_f32_e32 v44, v44, v52
	v_add_f32_e32 v45, v45, v53
	v_max_f32_e32 v57, 0, v44
	v_max_f32_e32 v58, 0, v45
	s_branch .Lic1_s83

.Lic1_s83:
	v_mul_f32_e32 v44, 0x42800000, v57
	v_mul_f32_e32 v45, 0x42800000, v58
	v_min_f32_e32 v44, 0x43e00000, v44
	v_min_f32_e32 v45, 0x43e00000, v45
	v_add_f32_e32 v46, v46, v54
	v_add_f32_e32 v47, v47, v55
	v_cvt_pk_fp8_f32 v56, v44, v45
	v_max_f32_e32 v46, 0, v46
	v_max_f32_e32 v47, 0, v47
	v_mul_f32_e32 v49, 0x42800000, v46
	v_mul_f32_e32 v44, 0x42800000, v47
	v_min_f32_e32 v45, 0x43e00000, v49
	v_min_f32_e32 v44, 0x43e00000, v44
	v_cvt_pk_fp8_f32 v56, v45, v44 op_sel:[0,0,1]
	s_branch .Lic1_s84

.Lic1_s84:
	v_ashrrev_i32_e32 v49, 31, v48
	v_lshlrev_b64 v[44:45], 6, v[48:49]
	v_lshl_add_u64 v[44:45], v[92:93], 0, v[44:45]
	global_store_dword v[44:45], v56, off
	ds_read_b128 v[52:55], v50 offset:64
	v_mov_b32_e32 v56, v89
	s_waitcnt lgkmcnt(0)
	v_add_f32_e32 v40, v40, v52
	v_add_f32_e32 v41, v41, v53
	v_max_f32_e32 v52, 0, v40
	v_max_f32_e32 v53, 0, v41
	v_mul_f32_e32 v40, 0x42800000, v52
	v_mul_f32_e32 v41, 0x42800000, v53
	v_min_f32_e32 v40, 0x43e00000, v40
	s_branch .Lic1_s85

.Lic1_s85:
	v_min_f32_e32 v41, 0x43e00000, v41
	v_add_f32_e32 v42, v42, v54
	v_add_f32_e32 v43, v43, v55
	v_cvt_pk_fp8_f32 v56, v40, v41
	v_max_f32_e32 v54, 0, v42
	v_max_f32_e32 v55, 0, v43
	v_mul_f32_e32 v42, 0x42800000, v54
	v_mul_f32_e32 v40, 0x42800000, v55
	v_min_f32_e32 v41, 0x43e00000, v42
	v_min_f32_e32 v40, 0x43e00000, v40
	v_cvt_pk_fp8_f32 v56, v41, v40 op_sel:[0,0,1]
	global_store_dword v[44:45], v56, off offset:16
	ds_read_b128 v[40:43], v50 offset:128
	v_mov_b32_e32 v56, v89
	s_branch .Lic1_s86

.Lic1_s86:
	s_waitcnt lgkmcnt(0)
	v_add_f32_e32 v36, v36, v40
	v_add_f32_e32 v37, v37, v41
	v_max_f32_e32 v59, 0, v36
	v_max_f32_e32 v60, 0, v37
	v_mul_f32_e32 v36, 0x42800000, v59
	v_mul_f32_e32 v37, 0x42800000, v60
	v_min_f32_e32 v36, 0x43e00000, v36
	v_min_f32_e32 v37, 0x43e00000, v37
	v_add_f32_e32 v38, v38, v42
	v_add_f32_e32 v39, v39, v43
	v_cvt_pk_fp8_f32 v56, v36, v37
	v_max_f32_e32 v61, 0, v38
	v_max_f32_e32 v62, 0, v39
	s_branch .Lic1_s87

.Lic1_s87:
	v_mul_f32_e32 v38, 0x42800000, v61
	v_mul_f32_e32 v36, 0x42800000, v62
	v_min_f32_e32 v37, 0x43e00000, v38
	v_min_f32_e32 v36, 0x43e00000, v36
	v_cvt_pk_fp8_f32 v56, v37, v36 op_sel:[0,0,1]
	v_lshlrev_b64 v[40:41], 7, v[48:49]
	v_lshl_add_u64 v[40:41], v[90:91], 0, v[40:41]
	v_cvt_pk_f16_f32 v43, v46, v47
	global_store_dword v[44:45], v56, off offset:32
	ds_read_b128 v[36:39], v50 offset:192
	v_cvt_pk_f16_f32 v42, v57, v58
	global_store_dwordx2 v[40:41], v[42:43], off
	v_cvt_pk_f16_f32 v43, v54, v55
	v_cvt_pk_f16_f32 v42, v52, v53
	s_branch .Lic1_s88

.Lic1_s88:
	global_store_dwordx2 v[40:41], v[42:43], off offset:32
	v_cvt_pk_f16_f32 v43, v61, v62
	v_cvt_pk_f16_f32 v42, v59, v60
	global_store_dwordx2 v[40:41], v[42:43], off offset:64
	s_waitcnt lgkmcnt(0)
	v_add_f32_e32 v32, v32, v36
	v_add_f32_e32 v33, v33, v37
	v_add_f32_e32 v34, v34, v38
	v_add_f32_e32 v35, v35, v39
	v_max_f32_e32 v32, 0, v32
	v_max_f32_e32 v36, 0, v33
	v_max_f32_e32 v33, 0, v34
	v_max_f32_e32 v34, 0, v35
	v_mul_f32_e32 v35, 0x42800000, v32
	s_branch .Lic1_s89

.Lic1_s89:
	v_mul_f32_e32 v37, 0x42800000, v36
	v_min_f32_e32 v35, 0x43e00000, v35
	v_min_f32_e32 v37, 0x43e00000, v37
	v_mov_b32_e32 v39, v89
	v_cvt_pk_fp8_f32 v39, v35, v37
	v_mul_f32_e32 v38, 0x42800000, v33
	v_mul_f32_e32 v37, 0x42800000, v34
	v_min_f32_e32 v35, 0x43e00000, v38
	v_min_f32_e32 v37, 0x43e00000, v37
	v_cvt_pk_fp8_f32 v39, v35, v37 op_sel:[0,0,1]
	v_cvt_pk_f16_f32 v33, v33, v34
	v_cvt_pk_f16_f32 v32, v32, v36
	global_store_dwordx2 v[40:41], v[32:33], off offset:96
	global_store_dword v[44:45], v39, off offset:48
	s_branch .Lic1_s90

.Lic1_s90:
	s_branch .LBB4_15
.LBB4_103:
	s_endpgm
	.p2align	8

.Lic2_s67:
	v_add_u32_dpp v58, v28, v81 row_newbcast:5 row_mask:0xf bank_mask:0x3
	v_add_u32_dpp v58, v28, v81 row_newbcast:13 row_mask:0xf bank_mask:0xc
	global_load_dwordx2 v[54:55], v54, s[30:31]
	v_add_u32_dpp v60, v28, v81 row_newbcast:7 row_mask:0xf bank_mask:0x3
	v_add_u32_dpp v60, v28, v81 row_newbcast:15 row_mask:0xf bank_mask:0xc
	global_load_dwordx2 v[58:59], v58, s[30:31]
	v_add_u32_dpp v50, v28, v81 row_newbcast:1 row_mask:0xf bank_mask:0x3
	v_add_u32_dpp v50, v28, v81 row_newbcast:9 row_mask:0xf bank_mask:0xc
	global_load_dwordx2 v[50:51], v50, s[30:31]
	v_add_u32_dpp v29, v28, v81 row_newbcast:2 row_mask:0xf bank_mask:0x3
	v_add_u32_dpp v29, v28, v81 row_newbcast:10 row_mask:0xf bank_mask:0xc
	global_load_dwordx2 v[52:53], v29, s[30:31]
	global_load_dwordx2 v[60:61], v60, s[30:31]
	s_add_i32 s8, s8, 8
	s_branch .Lic2_s68

.Lic2_s68:
	v_add_u32_dpp v29, v28, v81 row_newbcast:4 row_mask:0xf bank_mask:0x3
	v_add_u32_dpp v29, v28, v81 row_newbcast:12 row_mask:0xf bank_mask:0xc
	global_load_dwordx2 v[56:57], v29, s[30:31]
	v_mov_b32_dpp v29, v28 row_newbcast:6 row_mask:0xf bank_mask:0x3
	v_mov_b32_dpp v29, v28 row_newbcast:14 row_mask:0xf bank_mask:0xc
	v_add_u32_e32 v28, v29, v81
	global_load_dwordx2 v[28:29], v28, s[30:31]
	s_waitcnt vmcnt(7)
	v_cvt_scalef32_pk_f16_fp8 v62, v30, 1.0
	v_cvt_scalef32_pk_f16_fp8 v30, v30, 1.0 op_sel:[1,0,0]
	v_cvt_scalef32_pk_f16_fp8 v63, v31, 1.0
	v_cvt_scalef32_pk_f16_fp8 v31, v31, 1.0 op_sel:[1,0,0]
	v_pk_fma_f16 v62, v4, v62, v24
	v_pk_fma_f16 v30, v4, v30, v25
	s_branch .Lic2_s69

.Lic2_s69:
	v_pk_fma_f16 v63, v4, v63, v26
	s_waitcnt vmcnt(4)
	v_cvt_scalef32_pk_f16_fp8 v64, v50, 1.0
	v_cvt_scalef32_pk_f16_fp8 v50, v50, 1.0 op_sel:[1,0,0]
	v_cvt_scalef32_pk_f16_fp8 v65, v51, 1.0
	v_cvt_scalef32_pk_f16_fp8 v51, v51, 1.0 op_sel:[1,0,0]
	v_pk_fma_f16 v31, v4, v31, v27
	s_waitcnt vmcnt(3)
	v_cvt_scalef32_pk_f16_fp8 v66, v52, 1.0
	v_cvt_scalef32_pk_f16_fp8 v52, v52, 1.0 op_sel:[1,0,0]
	v_cvt_scalef32_pk_f16_fp8 v67, v53, 1.0
	v_cvt_scalef32_pk_f16_fp8 v53, v53, 1.0 op_sel:[1,0,0]
	v_pk_fma_f16 v31, v4, v51, v31
	v_pk_fma_f16 v51, v4, v65, v63
	s_branch .Lic2_s70

.Lic2_s70:
	v_pk_fma_f16 v30, v4, v50, v30
	v_pk_fma_f16 v50, v4, v64, v62
	v_cvt_scalef32_pk_f16_fp8 v68, v54, 1.0
	v_cvt_scalef32_pk_f16_fp8 v54, v54, 1.0 op_sel:[1,0,0]
	v_cvt_scalef32_pk_f16_fp8 v69, v55, 1.0
	v_cvt_scalef32_pk_f16_fp8 v55, v55, 1.0 op_sel:[1,0,0]
	v_pk_fma_f16 v50, v4, v66, v50
	v_pk_fma_f16 v30, v4, v52, v30
	v_pk_fma_f16 v51, v4, v67, v51
	v_pk_fma_f16 v31, v4, v53, v31
	s_waitcnt vmcnt(1)
	v_cvt_scalef32_pk_f16_fp8 v70, v56, 1.0
	v_cvt_scalef32_pk_f16_fp8 v56, v56, 1.0 op_sel:[1,0,0]
	v_cvt_scalef32_pk_f16_fp8 v71, v57, 1.0
	s_branch .Lic2_s71

.Lic2_s71:
	v_cvt_scalef32_pk_f16_fp8 v57, v57, 1.0 op_sel:[1,0,0]
	v_pk_fma_f16 v31, v4, v55, v31
	v_pk_fma_f16 v51, v4, v69, v51
	v_pk_fma_f16 v30, v4, v54, v30
	v_pk_fma_f16 v50, v4, v68, v50
	v_cvt_scalef32_pk_f16_fp8 v72, v58, 1.0
	v_cvt_scalef32_pk_f16_fp8 v58, v58, 1.0 op_sel:[1,0,0]
	v_cvt_scalef32_pk_f16_fp8 v73, v59, 1.0
	v_cvt_scalef32_pk_f16_fp8 v59, v59, 1.0 op_sel:[1,0,0]
	v_pk_fma_f16 v50, v4, v70, v50
	v_pk_fma_f16 v30, v4, v56, v30
	v_pk_fma_f16 v51, v4, v71, v51
	v_pk_fma_f16 v31, v4, v57, v31
	s_waitcnt vmcnt(0)
	s_branch .Lic2_s72

.Lic2_s72:
	v_cvt_scalef32_pk_f16_fp8 v89, v28, 1.0
	v_cvt_scalef32_pk_f16_fp8 v28, v28, 1.0 op_sel:[1,0,0]
	v_cvt_scalef32_pk_f16_fp8 v90, v29, 1.0
	v_cvt_scalef32_pk_f16_fp8 v29, v29, 1.0 op_sel:[1,0,0]
	v_pk_fma_f16 v31, v4, v59, v31
	v_pk_fma_f16 v51, v4, v73, v51
	v_pk_fma_f16 v30, v4, v58, v30
	v_pk_fma_f16 v50, v4, v72, v50
	v_cvt_scalef32_pk_f16_fp8 v91, v60, 1.0
	v_cvt_scalef32_pk_f16_fp8 v60, v60, 1.0 op_sel:[1,0,0]
	v_cvt_scalef32_pk_f16_fp8 v92, v61, 1.0
	v_cvt_scalef32_pk_f16_fp8 v61, v61, 1.0 op_sel:[1,0,0]
	v_pk_fma_f16 v50, v4, v89, v50
	v_pk_fma_f16 v28, v4, v28, v30
	s_branch .Lic2_s73

.Lic2_s73:
	v_pk_fma_f16 v30, v4, v90, v51
	v_pk_fma_f16 v29, v4, v29, v31
	v_pk_fma_f16 v30, v4, v92, v30
	v_pk_fma_f16 v31, v4, v61, v29
	v_pk_fma_f16 v29, v4, v60, v28
	v_pk_fma_f16 v28, v4, v91, v50
.LBB5_80:
	s_waitcnt lgkmcnt(0)
	s_nop 0
	v_mov_b64_e32 v[24:25], v[28:29]
	v_mov_b64_e32 v[26:27], v[30:31]
	v_cmp_lt_i32_e32 vcc, s8, v87
	s_cbranch_vccz .LBB5_83
	v_add_u32_e32 v28, s8, v75
	v_cmp_lt_i32_e32 vcc, v28, v87
	s_branch .Lic2_s74

.Lic2_s74:
	v_mov_b32_e32 v28, 0x61a800
	s_and_saveexec_b64 s[6:7], vcc
	s_cbranch_execz .LBB5_79
	v_add_u32_e32 v28, s8, v5
	v_ashrrev_i32_e32 v29, 31, v28
	v_lshl_add_u64 v[28:29], v[28:29], 2, s[26:27]
	global_load_dword v28, v[28:29], off
	s_waitcnt vmcnt(0)
	v_lshlrev_b32_e32 v28, 6, v28
	v_and_b32_e32 v28, 0x7fffc0, v28
	s_branch .LBB5_79
.LBB5_83:
	s_cbranch_execz .LBB5_80
	ds_write_b128 v82, v[24:27]
	ds_read_b128 v[24:27], v83 offset:128
	s_branch .Lic2_s75

.Lic2_s75:
	ds_read_b128 v[28:31], v80
	ds_read_b128 v[50:53], v83 offset:8832
	s_waitcnt lgkmcnt(1)
	v_mfma_f32_16x16x32_f16 v[8:11], v[24:27], v[28:31], v[8:11]
	ds_read_b128 v[24:27], v83 offset:17536
	s_waitcnt lgkmcnt(1)
	v_mfma_f32_16x16x32_f16 v[12:15], v[50:53], v[28:31], v[12:15]
	s_waitcnt lgkmcnt(0)
	v_mfma_f32_16x16x32_f16 v[16:19], v[24:27], v[28:31], v[16:19]
	ds_read_b128 v[24:27], v83 offset:26240
	s_waitcnt lgkmcnt(0)
	v_mfma_f32_16x16x32_f16 v[20:23], v[24:27], v[28:31], v[20:23]
	ds_read_b128 v[24:27], v83 offset:192
	ds_read_b128 v[90:93], v80 offset:64
	s_branch .Lic2_s76

.Lic2_s76:
	ds_read_b128 v[28:31], v83 offset:8896
	ds_read_b128 v[94:97], v83 offset:17600
	s_waitcnt lgkmcnt(2)
	v_mfma_f32_16x16x32_f16 v[8:11], v[24:27], v[90:93], v[8:11]
	s_waitcnt lgkmcnt(1)
	v_mfma_f32_16x16x32_f16 v[12:15], v[28:31], v[90:93], v[12:15]
	v_add_u32_dpp v4, v88, v81 row_newbcast:0 row_mask:0xf bank_mask:0x3
	v_add_u32_dpp v4, v88, v81 row_newbcast:8 row_mask:0xf bank_mask:0xc
	v_add_u32_dpp v5, v88, v81 row_newbcast:1 row_mask:0xf bank_mask:0x3
	v_add_u32_dpp v5, v88, v81 row_newbcast:9 row_mask:0xf bank_mask:0xc
	v_add_u32_dpp v24, v88, v81 row_newbcast:2 row_mask:0xf bank_mask:0x3
	v_add_u32_dpp v24, v88, v81 row_newbcast:10 row_mask:0xf bank_mask:0xc
	v_add_u32_dpp v25, v88, v81 row_newbcast:3 row_mask:0xf bank_mask:0x3
	v_add_u32_dpp v25, v88, v81 row_newbcast:11 row_mask:0xf bank_mask:0xc
	s_branch .Lic2_s77

.Lic2_s77:
	global_load_dwordx2 v[70:71], v4, s[30:31]
	global_load_dwordx2 v[66:67], v5, s[30:31]
	global_load_dwordx2 v[62:63], v24, s[30:31]
	global_load_dwordx2 v[56:57], v25, s[30:31]
	v_add_u32_dpp v4, v88, v81 row_newbcast:4 row_mask:0xf bank_mask:0x3
	v_add_u32_dpp v4, v88, v81 row_newbcast:12 row_mask:0xf bank_mask:0xc
	v_add_u32_dpp v5, v88, v81 row_newbcast:5 row_mask:0xf bank_mask:0x3
	v_add_u32_dpp v5, v88, v81 row_newbcast:13 row_mask:0xf bank_mask:0xc
	v_add_u32_dpp v24, v88, v81 row_newbcast:6 row_mask:0xf bank_mask:0x3
	v_add_u32_dpp v24, v88, v81 row_newbcast:14 row_mask:0xf bank_mask:0xc
	v_add_u32_dpp v25, v88, v81 row_newbcast:7 row_mask:0xf bank_mask:0x3
	v_add_u32_dpp v25, v88, v81 row_newbcast:15 row_mask:0xf bank_mask:0xc
	global_load_dwordx2 v[68:69], v4, s[30:31]
	global_load_dwordx2 v[64:65], v5, s[30:31]
	s_branch .Lic2_s78

.Lic2_s78:
	global_load_dwordx2 v[58:59], v24, s[30:31]
	global_load_dwordx2 v[52:53], v25, s[30:31]
	v_add_u32_dpp v4, v86, v81 row_newbcast:0 row_mask:0xf bank_mask:0x3
	v_add_u32_dpp v4, v86, v81 row_newbcast:8 row_mask:0xf bank_mask:0xc
	v_add_u32_dpp v5, v86, v81 row_newbcast:1 row_mask:0xf bank_mask:0x3
	v_add_u32_dpp v5, v86, v81 row_newbcast:9 row_mask:0xf bank_mask:0xc
	v_add_u32_dpp v24, v86, v81 row_newbcast:2 row_mask:0xf bank_mask:0x3
	v_add_u32_dpp v24, v86, v81 row_newbcast:10 row_mask:0xf bank_mask:0xc
	v_add_u32_dpp v25, v86, v81 row_newbcast:3 row_mask:0xf bank_mask:0x3
	v_add_u32_dpp v25, v86, v81 row_newbcast:11 row_mask:0xf bank_mask:0xc
	global_load_dwordx2 v[60:61], v4, s[30:31]
	global_load_dwordx2 v[54:55], v5, s[30:31]
	global_load_dwordx2 v[50:51], v24, s[30:31]
	global_load_dwordx2 v[30:31], v25, s[30:31]
	s_branch .Lic2_s79

.Lic2_s79:
	v_add_u32_dpp v4, v86, v81 row_newbcast:4 row_mask:0xf bank_mask:0x3
	v_add_u32_dpp v4, v86, v81 row_newbcast:12 row_mask:0xf bank_mask:0xc
	v_add_u32_dpp v5, v86, v81 row_newbcast:5 row_mask:0xf bank_mask:0x3
	v_add_u32_dpp v5, v86, v81 row_newbcast:13 row_mask:0xf bank_mask:0xc
	v_add_u32_dpp v24, v86, v81 row_newbcast:6 row_mask:0xf bank_mask:0x3
	v_add_u32_dpp v24, v86, v81 row_newbcast:14 row_mask:0xf bank_mask:0xc
	v_add_u32_dpp v72, v86, v81 row_newbcast:7 row_mask:0xf bank_mask:0x3
	v_add_u32_dpp v72, v86, v81 row_newbcast:15 row_mask:0xf bank_mask:0xc
	global_load_dwordx2 v[28:29], v4, s[30:31]
	global_load_dwordx2 v[26:27], v5, s[30:31]
	s_nop 0
	global_load_dwordx2 v[24:25], v24, s[30:31]
	s_nop 0
	global_load_dwordx2 v[4:5], v72, s[30:31]
	s_branch .Lic2_s80

.Lic2_s80:
	ds_read_b128 v[86:89], v83 offset:26304
	s_waitcnt lgkmcnt(1)
	v_mfma_f32_16x16x32_f16 v[16:19], v[94:97], v[90:93], v[16:19]
	v_cmp_lt_i32_e32 vcc, 16, v85
	s_cmp_lg_u64 vcc, 0
	s_cselect_b64 s[36:37], -1, 0
	s_waitcnt lgkmcnt(0)
	v_mfma_f32_16x16x32_f16 v[20:23], v[86:89], v[90:93], v[20:23]
	v_cmp_lt_i32_e64 s[10:11], 18, v85
	v_cmp_lt_i32_e64 s[8:9], 20, v85
	v_cmp_lt_i32_e64 s[6:7], 22, v85
	s_cbranch_vccz .LBB5_86
	v_add_u32_dpp v34, v7, v81 row_newbcast:0 row_mask:0xf bank_mask:0x3
	v_add_u32_dpp v34, v7, v81 row_newbcast:8 row_mask:0xf bank_mask:0xc
	s_branch .Lic2_s81

.Lic2_s81:
	v_add_u32_dpp v38, v7, v81 row_newbcast:1 row_mask:0xf bank_mask:0x3
	v_add_u32_dpp v38, v7, v81 row_newbcast:9 row_mask:0xf bank_mask:0xc
	global_load_dwordx2 v[34:35], v34, s[30:31]
	s_nop 0
	global_load_dwordx2 v[38:39], v38, s[30:31]
.LBB5_86:
	s_cmp_lg_u64 s[10:11], 0
	s_cselect_b64 s[34:35], -1, 0
	s_cmp_eq_u64 s[10:11], 0
	s_cbranch_scc1 .LBB5_88
	v_add_u32_dpp v36, v7, v81 row_newbcast:2 row_mask:0xf bank_mask:0x3
	v_add_u32_dpp v36, v7, v81 row_newbcast:10 row_mask:0xf bank_mask:0xc
	v_add_u32_dpp v42, v7, v81 row_newbcast:3 row_mask:0xf bank_mask:0x3
	v_add_u32_dpp v42, v7, v81 row_newbcast:11 row_mask:0xf bank_mask:0xc
	global_load_dwordx2 v[36:37], v36, s[30:31]
	s_branch .Lic2_s82

.Lic2_s82:
	s_nop 0
	global_load_dwordx2 v[42:43], v42, s[30:31]
.LBB5_88:
	s_cmp_lg_u64 s[8:9], 0
	s_cselect_b64 s[10:11], -1, 0
	s_cmp_eq_u64 s[8:9], 0
	s_cbranch_scc1 .LBB5_90
	v_add_u32_dpp v40, v7, v81 row_newbcast:4 row_mask:0xf bank_mask:0x3
	v_add_u32_dpp v40, v7, v81 row_newbcast:12 row_mask:0xf bank_mask:0xc
	v_add_u32_dpp v46, v7, v81 row_newbcast:5 row_mask:0xf bank_mask:0x3
	v_add_u32_dpp v46, v7, v81 row_newbcast:13 row_mask:0xf bank_mask:0xc
	global_load_dwordx2 v[40:41], v40, s[30:31]
	s_nop 0
	global_load_dwordx2 v[46:47], v46, s[30:31]
.LBB5_90:
	s_cmp_lg_u64 s[6:7], 0
	s_branch .Lic2_s83

.Lic2_s83:
	s_cselect_b64 s[8:9], -1, 0
	s_cmp_eq_u64 s[6:7], 0
	s_cbranch_scc1 .LBB5_92
	v_mov_b32_dpp v44, v7 row_newbcast:6 row_mask:0xf bank_mask:0x3
	v_mov_b32_dpp v44, v7 row_newbcast:14 row_mask:0xf bank_mask:0xc
	v_mov_b32_dpp v7, v7 row_newbcast:7 row_mask:0xf bank_mask:0x3
	s_nop 1
	v_mov_b32_dpp v7, v7 row_newbcast:15 row_mask:0xf bank_mask:0xc
	v_add_u32_e32 v44, v44, v81
	v_add_u32_e32 v7, v7, v81
	global_load_dwordx2 v[44:45], v44, s[30:31]
	s_nop 0
	global_load_dwordx2 v[48:49], v7, s[30:31]
.LBB5_92:
	v_cvt_f32_i32_e32 v7, v85
	s_branch .Lic2_s84

.Lic2_s84:
	s_waitcnt vmcnt(15)
	v_cvt_scalef32_pk_f16_fp8 v86, v70, 1.0
	v_cvt_scalef32_pk_f16_fp8 v70, v70, 1.0 op_sel:[1,0,0]
	v_max_f32_e32 v7, 1.0, v7
	v_div_scale_f32 v72, s[6:7], v7, v7, 1.0
	v_rcp_f32_e32 v73, v72
	v_div_scale_f32 v87, vcc, 1.0, v7, 1.0
	v_fma_f32 v88, -v72, v73, 1.0
	v_fmac_f32_e32 v73, v88, v73
	v_mul_f32_e32 v88, v87, v73
	v_fma_f32 v89, -v72, v88, v87
	v_fmac_f32_e32 v88, v89, v73
	v_fma_f32 v72, -v72, v88, v87
	v_div_fmas_f32 v72, v72, v73, v88
	s_branch .Lic2_s85

.Lic2_s85:
	v_div_fixup_f32 v7, v72, v7, 1.0
	v_mul_f32_e32 v72, 0x3c800000, v7
	v_fma_mixlo_f16 v7, v7, s29, 0
	v_cvt_scalef32_pk_f16_fp8 v73, v71, 1.0
	v_cvt_scalef32_pk_f16_fp8 v71, v71, 1.0 op_sel:[1,0,0]
	v_pk_fma_f16 v86, v7, v86, 0 op_sel_hi:[0,1,1]
	v_pk_fma_f16 v70, v7, v70, 0 op_sel_hi:[0,1,1]
	v_pk_fma_f16 v73, v7, v73, 0 op_sel_hi:[0,1,1]
	v_pk_fma_f16 v71, v7, v71, 0 op_sel_hi:[0,1,1]
	s_waitcnt vmcnt(14)
	v_cvt_scalef32_pk_f16_fp8 v87, v66, 1.0
	v_cvt_scalef32_pk_f16_fp8 v66, v66, 1.0 op_sel:[1,0,0]
	v_cvt_scalef32_pk_f16_fp8 v88, v67, 1.0
	v_cvt_scalef32_pk_f16_fp8 v67, v67, 1.0 op_sel:[1,0,0]
	s_branch .Lic2_s86

.Lic2_s86:
	v_pk_fma_f16 v67, v7, v67, v71 op_sel_hi:[0,1,1]
	v_pk_fma_f16 v71, v7, v88, v73 op_sel_hi:[0,1,1]
	v_pk_fma_f16 v66, v7, v66, v70 op_sel_hi:[0,1,1]
	v_pk_fma_f16 v70, v7, v87, v86 op_sel_hi:[0,1,1]
	s_waitcnt vmcnt(13)
	v_cvt_scalef32_pk_f16_fp8 v73, v62, 1.0
	v_cvt_scalef32_pk_f16_fp8 v62, v62, 1.0 op_sel:[1,0,0]
	v_cvt_scalef32_pk_f16_fp8 v86, v63, 1.0
	v_cvt_scalef32_pk_f16_fp8 v63, v63, 1.0 op_sel:[1,0,0]
	v_pk_fma_f16 v70, v7, v73, v70 op_sel_hi:[0,1,1]
	v_pk_fma_f16 v62, v7, v62, v66 op_sel_hi:[0,1,1]
	v_pk_fma_f16 v66, v7, v86, v71 op_sel_hi:[0,1,1]
	v_pk_fma_f16 v63, v7, v63, v67 op_sel_hi:[0,1,1]
	s_waitcnt vmcnt(12)
	s_branch .Lic2_s87

.Lic2_s87:
	v_cvt_scalef32_pk_f16_fp8 v67, v56, 1.0
	v_cvt_scalef32_pk_f16_fp8 v56, v56, 1.0 op_sel:[1,0,0]
	v_cvt_scalef32_pk_f16_fp8 v71, v57, 1.0
	v_cvt_scalef32_pk_f16_fp8 v57, v57, 1.0 op_sel:[1,0,0]
	v_pk_fma_f16 v57, v7, v57, v63 op_sel_hi:[0,1,1]
	v_pk_fma_f16 v63, v7, v71, v66 op_sel_hi:[0,1,1]
	v_pk_fma_f16 v56, v7, v56, v62 op_sel_hi:[0,1,1]
	v_pk_fma_f16 v62, v7, v67, v70 op_sel_hi:[0,1,1]
	s_waitcnt vmcnt(11)
	v_cvt_scalef32_pk_f16_fp8 v66, v68, 1.0
	v_cvt_scalef32_pk_f16_fp8 v67, v68, 1.0 op_sel:[1,0,0]
	v_cvt_scalef32_pk_f16_fp8 v68, v69, 1.0
	v_cvt_scalef32_pk_f16_fp8 v69, v69, 1.0 op_sel:[1,0,0]
	v_pk_fma_f16 v62, v7, v66, v62 op_sel_hi:[0,1,1]
	s_branch .Lic2_s88

.Lic2_s88:
	v_pk_fma_f16 v56, v7, v67, v56 op_sel_hi:[0,1,1]
	v_pk_fma_f16 v63, v7, v68, v63 op_sel_hi:[0,1,1]
	v_pk_fma_f16 v57, v7, v69, v57 op_sel_hi:[0,1,1]
	s_waitcnt vmcnt(10)
	v_cvt_scalef32_pk_f16_fp8 v66, v64, 1.0
	v_cvt_scalef32_pk_f16_fp8 v64, v64, 1.0 op_sel:[1,0,0]
	v_cvt_scalef32_pk_f16_fp8 v67, v65, 1.0
	v_cvt_scalef32_pk_f16_fp8 v65, v65, 1.0 op_sel:[1,0,0]
	v_pk_fma_f16 v57, v7, v65, v57 op_sel_hi:[0,1,1]
	v_pk_fma_f16 v63, v7, v67, v63 op_sel_hi:[0,1,1]
	v_pk_fma_f16 v56, v7, v64, v56 op_sel_hi:[0,1,1]
	v_pk_fma_f16 v62, v7, v66, v62 op_sel_hi:[0,1,1]
	s_waitcnt vmcnt(9)
	v_cvt_scalef32_pk_f16_fp8 v64, v58, 1.0
	s_branch .Lic2_s89

.Lic2_s89:
	v_cvt_scalef32_pk_f16_fp8 v58, v58, 1.0 op_sel:[1,0,0]
	v_cvt_scalef32_pk_f16_fp8 v65, v59, 1.0
	v_cvt_scalef32_pk_f16_fp8 v59, v59, 1.0 op_sel:[1,0,0]
	v_pk_fma_f16 v62, v7, v64, v62 op_sel_hi:[0,1,1]
	v_pk_fma_f16 v56, v7, v58, v56 op_sel_hi:[0,1,1]
	v_pk_fma_f16 v58, v7, v65, v63 op_sel_hi:[0,1,1]
	v_pk_fma_f16 v57, v7, v59, v57 op_sel_hi:[0,1,1]
	s_waitcnt vmcnt(8)
	v_cvt_scalef32_pk_f16_fp8 v59, v52, 1.0
	v_cvt_scalef32_pk_f16_fp8 v52, v52, 1.0 op_sel:[1,0,0]
	v_cvt_scalef32_pk_f16_fp8 v63, v53, 1.0
	v_cvt_scalef32_pk_f16_fp8 v53, v53, 1.0 op_sel:[1,0,0]
	v_pk_fma_f16 v53, v7, v53, v57 op_sel_hi:[0,1,1]
	v_pk_fma_f16 v57, v7, v63, v58 op_sel_hi:[0,1,1]
	s_branch .Lic2_s90

.Lic2_s90:
	v_pk_fma_f16 v52, v7, v52, v56 op_sel_hi:[0,1,1]
	v_pk_fma_f16 v56, v7, v59, v62 op_sel_hi:[0,1,1]
	s_waitcnt vmcnt(7)
	v_cvt_scalef32_pk_f16_fp8 v58, v60, 1.0
	v_cvt_scalef32_pk_f16_fp8 v59, v60, 1.0 op_sel:[1,0,0]
	v_cvt_scalef32_pk_f16_fp8 v60, v61, 1.0
	v_cvt_scalef32_pk_f16_fp8 v61, v61, 1.0 op_sel:[1,0,0]
	v_pk_fma_f16 v56, v7, v58, v56 op_sel_hi:[0,1,1]
	v_pk_fma_f16 v52, v7, v59, v52 op_sel_hi:[0,1,1]
	v_pk_fma_f16 v57, v7, v60, v57 op_sel_hi:[0,1,1]
	v_pk_fma_f16 v53, v7, v61, v53 op_sel_hi:[0,1,1]
	s_waitcnt vmcnt(6)
	v_cvt_scalef32_pk_f16_fp8 v58, v54, 1.0
	v_cvt_scalef32_pk_f16_fp8 v54, v54, 1.0 op_sel:[1,0,0]
	s_branch .Lic2_s91

.Lic2_s91:
	v_cvt_scalef32_pk_f16_fp8 v59, v55, 1.0
	v_cvt_scalef32_pk_f16_fp8 v55, v55, 1.0 op_sel:[1,0,0]
	v_pk_fma_f16 v53, v7, v55, v53 op_sel_hi:[0,1,1]
	v_pk_fma_f16 v55, v7, v59, v57 op_sel_hi:[0,1,1]
	v_pk_fma_f16 v52, v7, v54, v52 op_sel_hi:[0,1,1]
	v_pk_fma_f16 v54, v7, v58, v56 op_sel_hi:[0,1,1]
	s_waitcnt vmcnt(5)
	v_cvt_scalef32_pk_f16_fp8 v56, v50, 1.0
	v_cvt_scalef32_pk_f16_fp8 v50, v50, 1.0 op_sel:[1,0,0]
	v_cvt_scalef32_pk_f16_fp8 v57, v51, 1.0
	v_cvt_scalef32_pk_f16_fp8 v51, v51, 1.0 op_sel:[1,0,0]
	v_pk_fma_f16 v54, v7, v56, v54 op_sel_hi:[0,1,1]
	v_pk_fma_f16 v50, v7, v50, v52 op_sel_hi:[0,1,1]
	v_pk_fma_f16 v52, v7, v57, v55 op_sel_hi:[0,1,1]
	s_branch .Lic2_s92

.Lic2_s92:
	v_pk_fma_f16 v51, v7, v51, v53 op_sel_hi:[0,1,1]
	s_waitcnt vmcnt(4)
	v_cvt_scalef32_pk_f16_fp8 v53, v30, 1.0
	v_cvt_scalef32_pk_f16_fp8 v30, v30, 1.0 op_sel:[1,0,0]
	v_cvt_scalef32_pk_f16_fp8 v55, v31, 1.0
	v_cvt_scalef32_pk_f16_fp8 v31, v31, 1.0 op_sel:[1,0,0]
	v_pk_fma_f16 v31, v7, v31, v51 op_sel_hi:[0,1,1]
	v_pk_fma_f16 v51, v7, v55, v52 op_sel_hi:[0,1,1]
	v_pk_fma_f16 v30, v7, v30, v50 op_sel_hi:[0,1,1]
	v_pk_fma_f16 v50, v7, v53, v54 op_sel_hi:[0,1,1]
	s_waitcnt vmcnt(3)
	v_cvt_scalef32_pk_f16_fp8 v52, v28, 1.0
	v_cvt_scalef32_pk_f16_fp8 v28, v28, 1.0 op_sel:[1,0,0]
	v_cvt_scalef32_pk_f16_fp8 v53, v29, 1.0
	s_branch .Lic2_s93

.Lic2_s93:
	v_cvt_scalef32_pk_f16_fp8 v29, v29, 1.0 op_sel:[1,0,0]
	v_pk_fma_f16 v50, v7, v52, v50 op_sel_hi:[0,1,1]
	v_pk_fma_f16 v28, v7, v28, v30 op_sel_hi:[0,1,1]
	v_pk_fma_f16 v30, v7, v53, v51 op_sel_hi:[0,1,1]
	v_pk_fma_f16 v29, v7, v29, v31 op_sel_hi:[0,1,1]
	s_waitcnt vmcnt(2)
	v_cvt_scalef32_pk_f16_fp8 v31, v26, 1.0
	v_cvt_scalef32_pk_f16_fp8 v26, v26, 1.0 op_sel:[1,0,0]
	v_cvt_scalef32_pk_f16_fp8 v51, v27, 1.0
	v_cvt_scalef32_pk_f16_fp8 v27, v27, 1.0 op_sel:[1,0,0]
	v_pk_fma_f16 v27, v7, v27, v29 op_sel_hi:[0,1,1]
	v_pk_fma_f16 v29, v7, v51, v30 op_sel_hi:[0,1,1]
	v_pk_fma_f16 v26, v7, v26, v28 op_sel_hi:[0,1,1]
	v_pk_fma_f16 v28, v7, v31, v50 op_sel_hi:[0,1,1]
	s_branch .Lic2_s94

.Lic2_s94:
	s_waitcnt vmcnt(1)
	v_cvt_scalef32_pk_f16_fp8 v30, v24, 1.0
	v_cvt_scalef32_pk_f16_fp8 v24, v24, 1.0 op_sel:[1,0,0]
	v_cvt_scalef32_pk_f16_fp8 v31, v25, 1.0
	v_cvt_scalef32_pk_f16_fp8 v25, v25, 1.0 op_sel:[1,0,0]
	v_pk_fma_f16 v28, v7, v30, v28 op_sel_hi:[0,1,1]
	v_pk_fma_f16 v24, v7, v24, v26 op_sel_hi:[0,1,1]
	v_pk_fma_f16 v26, v7, v31, v29 op_sel_hi:[0,1,1]
	v_pk_fma_f16 v25, v7, v25, v27 op_sel_hi:[0,1,1]
	s_waitcnt vmcnt(0)
	v_cvt_scalef32_pk_f16_fp8 v29, v4, 1.0
	v_cvt_scalef32_pk_f16_fp8 v4, v4, 1.0 op_sel:[1,0,0]
	v_cvt_scalef32_pk_f16_fp8 v30, v5, 1.0
	v_cvt_scalef32_pk_f16_fp8 v5, v5, 1.0 op_sel:[1,0,0]
	s_branch .Lic2_s95

.Lic2_s95:
	v_cvt_pk_f16_f32 v72, v72, v72
	v_pk_fma_f16 v27, v7, v5, v25 op_sel_hi:[0,1,1]
	v_pk_fma_f16 v26, v7, v30, v26 op_sel_hi:[0,1,1]
	v_pk_fma_f16 v25, v7, v4, v24 op_sel_hi:[0,1,1]
	s_andn2_b64 vcc, exec, s[36:37]
	v_pk_fma_f16 v24, v7, v29, v28 op_sel_hi:[0,1,1]
	s_cbranch_vccnz .LBB5_94
	v_cvt_scalef32_pk_f16_fp8 v4, v34, 1.0
	v_cvt_scalef32_pk_f16_fp8 v5, v34, 1.0 op_sel:[1,0,0]
	v_cvt_scalef32_pk_f16_fp8 v7, v35, 1.0
	v_cvt_scalef32_pk_f16_fp8 v28, v35, 1.0 op_sel:[1,0,0]
	v_pk_fma_f16 v4, v72, v4, v24
	v_pk_fma_f16 v5, v72, v5, v25
	v_pk_fma_f16 v7, v72, v7, v26
	s_branch .Lic2_s96

.Lic2_s96:
	v_pk_fma_f16 v24, v72, v28, v27
	v_cvt_scalef32_pk_f16_fp8 v28, v38, 1.0
	v_cvt_scalef32_pk_f16_fp8 v25, v38, 1.0 op_sel:[1,0,0]
	v_cvt_scalef32_pk_f16_fp8 v26, v39, 1.0
	v_cvt_scalef32_pk_f16_fp8 v27, v39, 1.0 op_sel:[1,0,0]
	v_pk_fma_f16 v27, v72, v27, v24
	v_pk_fma_f16 v26, v72, v26, v7
	v_pk_fma_f16 v25, v72, v25, v5
	v_pk_fma_f16 v24, v72, v28, v4
.LBB5_94:
	s_andn2_b64 vcc, exec, s[34:35]
	s_cbranch_vccnz .LBB5_96
	v_cvt_scalef32_pk_f16_fp8 v4, v36, 1.0
	v_cvt_scalef32_pk_f16_fp8 v5, v36, 1.0 op_sel:[1,0,0]
	v_cvt_scalef32_pk_f16_fp8 v7, v37, 1.0
	s_branch .Lic2_s97

.Lic2_s97:
	v_cvt_scalef32_pk_f16_fp8 v28, v37, 1.0 op_sel:[1,0,0]
	v_pk_fma_f16 v4, v72, v4, v24
	v_pk_fma_f16 v5, v72, v5, v25
	v_pk_fma_f16 v7, v72, v7, v26
	v_pk_fma_f16 v24, v72, v28, v27
	v_cvt_scalef32_pk_f16_fp8 v28, v42, 1.0
	v_cvt_scalef32_pk_f16_fp8 v25, v42, 1.0 op_sel:[1,0,0]
	v_cvt_scalef32_pk_f16_fp8 v26, v43, 1.0
	v_cvt_scalef32_pk_f16_fp8 v27, v43, 1.0 op_sel:[1,0,0]
	v_pk_fma_f16 v27, v72, v27, v24
	v_pk_fma_f16 v26, v72, v26, v7
	v_pk_fma_f16 v25, v72, v25, v5
	v_pk_fma_f16 v24, v72, v28, v4
.LBB5_96:
	s_andn2_b64 vcc, exec, s[10:11]
	s_branch .Lic2_s98

.Lic2_s98:
	s_cbranch_vccnz .LBB5_98
	v_cvt_scalef32_pk_f16_fp8 v4, v40, 1.0
	v_cvt_scalef32_pk_f16_fp8 v5, v40, 1.0 op_sel:[1,0,0]
	v_cvt_scalef32_pk_f16_fp8 v7, v41, 1.0
	v_cvt_scalef32_pk_f16_fp8 v28, v41, 1.0 op_sel:[1,0,0]
	v_pk_fma_f16 v4, v72, v4, v24
	v_pk_fma_f16 v5, v72, v5, v25
	v_pk_fma_f16 v7, v72, v7, v26
	v_pk_fma_f16 v24, v72, v28, v27
	v_cvt_scalef32_pk_f16_fp8 v28, v46, 1.0
	v_cvt_scalef32_pk_f16_fp8 v25, v46, 1.0 op_sel:[1,0,0]
	v_cvt_scalef32_pk_f16_fp8 v26, v47, 1.0
	v_cvt_scalef32_pk_f16_fp8 v27, v47, 1.0 op_sel:[1,0,0]
	v_pk_fma_f16 v27, v72, v27, v24
	s_branch .Lic2_s99

.Lic2_s99:
	v_pk_fma_f16 v26, v72, v26, v7
	v_pk_fma_f16 v25, v72, v25, v5
	v_pk_fma_f16 v24, v72, v28, v4
.LBB5_98:
	s_andn2_b64 vcc, exec, s[8:9]
	s_cbranch_vccnz .LBB5_100
	v_cvt_scalef32_pk_f16_fp8 v4, v44, 1.0
	v_cvt_scalef32_pk_f16_fp8 v5, v44, 1.0 op_sel:[1,0,0]
	v_cvt_scalef32_pk_f16_fp8 v7, v45, 1.0
	v_cvt_scalef32_pk_f16_fp8 v28, v45, 1.0 op_sel:[1,0,0]
	v_pk_fma_f16 v4, v72, v4, v24
	v_pk_fma_f16 v5, v72, v5, v25
	v_pk_fma_f16 v7, v72, v7, v26
	v_pk_fma_f16 v24, v72, v28, v27
	v_cvt_scalef32_pk_f16_fp8 v28, v48, 1.0
	s_branch .Lic2_s100

.Lic2_s100:
	v_cvt_scalef32_pk_f16_fp8 v25, v48, 1.0 op_sel:[1,0,0]
	v_cvt_scalef32_pk_f16_fp8 v26, v49, 1.0
	v_cvt_scalef32_pk_f16_fp8 v27, v49, 1.0 op_sel:[1,0,0]
	v_pk_fma_f16 v27, v72, v27, v24
	v_pk_fma_f16 v26, v72, v26, v7
	v_pk_fma_f16 v25, v72, v25, v5
	v_pk_fma_f16 v24, v72, v28, v4

.LBB5_101:
	s_waitcnt lgkmcnt(0)
	s_or_b64 exec, exec, s[6:7]
	s_add_i32 s8, s8, 8
	v_add_u32_dpp v25, v24, v81 row_newbcast:0 row_mask:0xf bank_mask:0x3
	s_branch .Lic2_s101

.Lic2_s101:
	v_add_u32_dpp v25, v24, v81 row_newbcast:8 row_mask:0xf bank_mask:0xc
	v_add_u32_dpp v29, v24, v81 row_newbcast:1 row_mask:0xf bank_mask:0x3
	v_add_u32_dpp v29, v24, v81 row_newbcast:9 row_mask:0xf bank_mask:0xc
	global_load_dwordx2 v[26:27], v25, s[30:31]
	global_load_dwordx2 v[30:31], v29, s[30:31]
	v_add_u32_dpp v25, v24, v81 row_newbcast:2 row_mask:0xf bank_mask:0x3
	v_add_u32_dpp v25, v24, v81 row_newbcast:10 row_mask:0xf bank_mask:0xc
	v_add_u32_dpp v29, v24, v81 row_newbcast:3 row_mask:0xf bank_mask:0x3
	v_add_u32_dpp v29, v24, v81 row_newbcast:11 row_mask:0xf bank_mask:0xc
	global_load_dwordx2 v[50:51], v25, s[30:31]
	global_load_dwordx2 v[52:53], v29, s[30:31]
	v_add_u32_dpp v25, v24, v81 row_newbcast:4 row_mask:0xf bank_mask:0x3
	v_add_u32_dpp v25, v24, v81 row_newbcast:12 row_mask:0xf bank_mask:0xc
	v_add_u32_dpp v29, v24, v81 row_newbcast:5 row_mask:0xf bank_mask:0x3
	s_branch .Lic2_s102

.Lic2_s102:
	v_add_u32_dpp v29, v24, v81 row_newbcast:13 row_mask:0xf bank_mask:0xc
	global_load_dwordx2 v[54:55], v25, s[30:31]
	global_load_dwordx2 v[56:57], v29, s[30:31]
	v_mov_b32_dpp v25, v24 row_newbcast:6 row_mask:0xf bank_mask:0x3
	v_mov_b32_dpp v25, v24 row_newbcast:14 row_mask:0xf bank_mask:0xc
	v_mov_b32_dpp v29, v24 row_newbcast:7 row_mask:0xf bank_mask:0x3
	v_mov_b32_dpp v29, v24 row_newbcast:15 row_mask:0xf bank_mask:0xc
	v_add_u32_e32 v24, v25, v81
	global_load_dwordx2 v[24:25], v24, s[30:31]
	v_add_u32_e32 v29, v29, v81
	global_load_dwordx2 v[58:59], v29, s[30:31]
	s_waitcnt vmcnt(7)
	v_cvt_scalef32_pk_f16_fp8 v29, v26, 1.0
	v_cvt_scalef32_pk_f16_fp8 v26, v26, 1.0 op_sel:[1,0,0]
	s_branch .Lic2_s103

.Lic2_s103:
	v_cvt_scalef32_pk_f16_fp8 v60, v27, 1.0
	v_cvt_scalef32_pk_f16_fp8 v27, v27, 1.0 op_sel:[1,0,0]
	s_waitcnt vmcnt(6)
	v_cvt_scalef32_pk_f16_fp8 v61, v30, 1.0
	v_cvt_scalef32_pk_f16_fp8 v30, v30, 1.0 op_sel:[1,0,0]
	v_cvt_scalef32_pk_f16_fp8 v62, v31, 1.0
	v_cvt_scalef32_pk_f16_fp8 v31, v31, 1.0 op_sel:[1,0,0]
	v_pk_fma_f16 v29, v72, v29, v4
	v_pk_fma_f16 v26, v72, v26, v5
	v_pk_fma_f16 v60, v72, v60, v6
	v_pk_fma_f16 v27, v72, v27, v7
	s_waitcnt vmcnt(5)
	v_cvt_scalef32_pk_f16_fp8 v63, v50, 1.0
	v_cvt_scalef32_pk_f16_fp8 v50, v50, 1.0 op_sel:[1,0,0]
	s_branch .Lic2_s104

.Lic2_s104:
	v_cvt_scalef32_pk_f16_fp8 v64, v51, 1.0
	v_cvt_scalef32_pk_f16_fp8 v51, v51, 1.0 op_sel:[1,0,0]
	v_pk_fma_f16 v27, v72, v31, v27
	v_pk_fma_f16 v31, v72, v62, v60
	v_pk_fma_f16 v26, v72, v30, v26
	v_pk_fma_f16 v29, v72, v61, v29
	s_waitcnt vmcnt(4)
	v_cvt_scalef32_pk_f16_fp8 v65, v52, 1.0
	v_cvt_scalef32_pk_f16_fp8 v52, v52, 1.0 op_sel:[1,0,0]
	v_cvt_scalef32_pk_f16_fp8 v66, v53, 1.0
	v_cvt_scalef32_pk_f16_fp8 v53, v53, 1.0 op_sel:[1,0,0]
	v_pk_fma_f16 v29, v72, v63, v29
	v_pk_fma_f16 v26, v72, v50, v26
	v_pk_fma_f16 v30, v72, v64, v31
	s_branch .Lic2_s105

.Lic2_s105:
	v_pk_fma_f16 v27, v72, v51, v27
	s_waitcnt vmcnt(3)
	v_cvt_scalef32_pk_f16_fp8 v67, v54, 1.0
	v_cvt_scalef32_pk_f16_fp8 v54, v54, 1.0 op_sel:[1,0,0]
	v_cvt_scalef32_pk_f16_fp8 v68, v55, 1.0
	v_cvt_scalef32_pk_f16_fp8 v55, v55, 1.0 op_sel:[1,0,0]
	v_pk_fma_f16 v27, v72, v53, v27
	v_pk_fma_f16 v30, v72, v66, v30
	v_pk_fma_f16 v26, v72, v52, v26
	v_pk_fma_f16 v29, v72, v65, v29
	s_waitcnt vmcnt(2)
	v_cvt_scalef32_pk_f16_fp8 v69, v56, 1.0
	v_cvt_scalef32_pk_f16_fp8 v56, v56, 1.0 op_sel:[1,0,0]
	v_cvt_scalef32_pk_f16_fp8 v70, v57, 1.0
	s_branch .Lic2_s106

.Lic2_s106:
	v_cvt_scalef32_pk_f16_fp8 v57, v57, 1.0 op_sel:[1,0,0]
	v_pk_fma_f16 v29, v72, v67, v29
	v_pk_fma_f16 v26, v72, v54, v26
	v_pk_fma_f16 v30, v72, v68, v30
	v_pk_fma_f16 v27, v72, v55, v27
	s_waitcnt vmcnt(1)
	v_cvt_scalef32_pk_f16_fp8 v71, v24, 1.0
	v_cvt_scalef32_pk_f16_fp8 v24, v24, 1.0 op_sel:[1,0,0]
	v_cvt_scalef32_pk_f16_fp8 v73, v25, 1.0
	v_cvt_scalef32_pk_f16_fp8 v25, v25, 1.0 op_sel:[1,0,0]
	v_pk_fma_f16 v27, v72, v57, v27
	v_pk_fma_f16 v30, v72, v70, v30
	v_pk_fma_f16 v26, v72, v56, v26
	v_pk_fma_f16 v29, v72, v69, v29
	s_branch .Lic2_s107

.Lic2_s107:
	s_waitcnt vmcnt(0)
	v_cvt_scalef32_pk_f16_fp8 v86, v58, 1.0
	v_cvt_scalef32_pk_f16_fp8 v58, v58, 1.0 op_sel:[1,0,0]
	v_cvt_scalef32_pk_f16_fp8 v87, v59, 1.0
	v_cvt_scalef32_pk_f16_fp8 v59, v59, 1.0 op_sel:[1,0,0]
	v_pk_fma_f16 v29, v72, v71, v29
	v_pk_fma_f16 v24, v72, v24, v26
	v_pk_fma_f16 v26, v72, v73, v30
	v_pk_fma_f16 v25, v72, v25, v27
	v_pk_fma_f16 v26, v72, v87, v26
	v_pk_fma_f16 v27, v72, v59, v25
	v_pk_fma_f16 v25, v72, v58, v24
	v_pk_fma_f16 v24, v72, v86, v29
.LBB5_102:
	s_waitcnt lgkmcnt(0)
	s_nop 0
	s_branch .Lic2_s108

.Lic2_s108:
	v_mov_b64_e32 v[4:5], v[24:25]
	v_mov_b64_e32 v[6:7], v[26:27]
	v_cmp_lt_i32_e32 vcc, s8, v85
	s_cbranch_vccz .LBB5_105
	v_add_u32_e32 v24, s8, v75
	v_cmp_lt_i32_e32 vcc, v24, v85
	v_mov_b32_e32 v24, 0x61a800
	s_and_saveexec_b64 s[6:7], vcc
	s_cbranch_execz .LBB5_101
	v_add_u32_e32 v24, s8, v28
	v_ashrrev_i32_e32 v25, 31, v24
	v_lshl_add_u64 v[24:25], v[24:25], 2, s[26:27]
	global_load_dword v24, v[24:25], off
	s_waitcnt vmcnt(0)
	s_branch .Lic2_s109

.Lic2_s109:
	v_lshlrev_b32_e32 v24, 6, v24
	v_and_b32_e32 v24, 0x7fffc0, v24
	s_branch .LBB5_101
.LBB5_105:
	s_cbranch_execz .LBB5_102
	ds_write_b128 v82, v[4:7]
	ds_read_b128 v[4:7], v83 offset:256
	ds_read_b128 v[24:27], v80
	ds_read_b128 v[28:31], v83 offset:8960
	s_waitcnt lgkmcnt(1)
	v_mfma_f32_16x16x32_f16 v[4:7], v[4:7], v[24:27], v[8:11]
	s_nop 2
	ds_read_b128 v[8:11], v83 offset:17664
	s_waitcnt lgkmcnt(1)
	v_mfma_f32_16x16x32_f16 v[12:15], v[28:31], v[24:27], v[12:15]
	s_branch .Lic2_s110

.Lic2_s110:
	s_waitcnt lgkmcnt(0)
	v_mfma_f32_16x16x32_f16 v[8:11], v[8:11], v[24:27], v[16:19]
	s_nop 2
	ds_read_b128 v[16:19], v83 offset:26368
	s_waitcnt lgkmcnt(0)
	v_mfma_f32_16x16x32_f16 v[16:19], v[16:19], v[24:27], v[20:23]
	s_nop 2
	ds_read_b128 v[20:23], v83 offset:320
	ds_read_b128 v[24:27], v80 offset:64
	ds_read_b128 v[28:31], v83 offset:9024
	s_waitcnt lgkmcnt(1)
	v_mfma_f32_16x16x32_f16 v[4:7], v[20:23], v[24:27], v[4:7]
	ds_read_b128 v[20:23], v83 offset:17728
	s_waitcnt lgkmcnt(1)
	s_branch .Lic2_s111

.Lic2_s111:
	v_mfma_f32_16x16x32_f16 v[12:15], v[28:31], v[24:27], v[12:15]
	s_waitcnt lgkmcnt(0)
	v_mfma_f32_16x16x32_f16 v[8:11], v[20:23], v[24:27], v[8:11]
	ds_read_b128 v[20:23], v83 offset:26432
	ds_write_b128 v82, v[0:3]
	s_waitcnt lgkmcnt(1)
	v_mfma_f32_16x16x32_f16 v[0:3], v[20:23], v[24:27], v[16:19]
	s_nop 2
	ds_read_b128 v[16:19], v83 offset:384
	ds_read_b128 v[20:23], v80
	ds_read_b128 v[24:27], v83 offset:9088
	s_waitcnt lgkmcnt(1)
	v_mfma_f32_16x16x32_f16 v[4:7], v[16:19], v[20:23], v[4:7]
	ds_read_b128 v[16:19], v83 offset:17792
	s_branch .Lic2_s112

.Lic2_s112:
	s_waitcnt lgkmcnt(1)
	v_mfma_f32_16x16x32_f16 v[12:15], v[24:27], v[20:23], v[12:15]
	s_waitcnt lgkmcnt(0)
	v_mfma_f32_16x16x32_f16 v[8:11], v[16:19], v[20:23], v[8:11]
	ds_read_b128 v[16:19], v83 offset:26496
	s_waitcnt lgkmcnt(0)
	v_mfma_f32_16x16x32_f16 v[0:3], v[16:19], v[20:23], v[0:3]
	ds_read_b128 v[16:19], v83 offset:448
	ds_read_b128 v[20:23], v80 offset:64
	ds_read_b128 v[24:27], v83 offset:9152
	ds_read_b128 v[28:31], v83 offset:17856
	ds_read_b128 v[50:53], v83 offset:26560
	s_mov_b64 s[6:7], s[22:23]
	s_mov_b64 s[8:9], s[18:19]
	s_branch .Lic2_s113

.Lic2_s113:
	s_waitcnt lgkmcnt(1)
	v_mfma_f32_16x16x32_f16 v[8:11], v[28:31], v[20:23], v[8:11]
	s_nop 0
	s_waitcnt lgkmcnt(0)
	v_mfma_f32_16x16x32_f16 v[0:3], v[50:53], v[20:23], v[0:3]
	v_mfma_f32_16x16x32_f16 v[16:19], v[16:19], v[20:23], v[4:7]
	s_nop 2
	v_add_u32_e32 v6, s33, v77
	v_mfma_f32_16x16x32_f16 v[12:15], v[24:27], v[20:23], v[12:15]
	v_cmp_gt_i32_e32 vcc, s28, v6
	ds_read_b128 v[20:23], v32 offset:52240
	ds_read_b128 v[24:27], v32 offset:52496
	ds_read_b128 v[28:31], v32 offset:52752
	s_waitcnt lgkmcnt(2)
	s_branch .Lic2_s114

.Lic2_s114:
	v_add_f32_e32 v7, v16, v20
	s_waitcnt lgkmcnt(1)
	v_mov_b32_e32 v4, v24
	s_waitcnt lgkmcnt(0)
	v_mov_b32_e32 v5, v28
	v_add_f32_e32 v16, v17, v21
	v_add_f32_e32 v17, v18, v22
	v_add_f32_e32 v18, v19, v23
	v_max_f32_e32 v24, 0, v7
	v_max_f32_e32 v62, 0, v16
	v_max_f32_e32 v64, 0, v17
	v_max_f32_e32 v66, 0, v18
	ds_read_b128 v[16:19], v32 offset:52304
	ds_read_b128 v[20:23], v32 offset:52560
	s_branch .Lic2_s115

.Lic2_s115:
	ds_read_b128 v[50:53], v32 offset:52816
	s_waitcnt lgkmcnt(2)
	v_add_f32_e32 v7, v12, v16
	v_add_f32_e32 v12, v13, v17
	v_add_f32_e32 v13, v14, v18
	v_add_f32_e32 v14, v15, v19
	v_max_f32_e32 v68, 0, v7
	v_max_f32_e32 v70, 0, v12
	v_max_f32_e32 v72, 0, v13
	v_max_f32_e32 v86, 0, v14
	ds_read_b128 v[12:15], v32 offset:52368
	ds_read_b128 v[16:19], v32 offset:52624
	ds_read_b128 v[54:57], v32 offset:52880
	v_pk_fma_f32 v[88:89], v[4:5], v[24:25], 0 op_sel_hi:[1,0,0]
	s_branch .Lic2_s116

.Lic2_s116:
	v_mov_b32_e32 v28, v25
	v_mov_b32_e32 v24, v26
	v_mov_b32_e32 v25, v30
	v_mov_b32_e32 v30, v27
	s_waitcnt lgkmcnt(4)
	v_mov_b32_e32 v26, v20
	s_waitcnt lgkmcnt(3)
	v_mov_b32_e32 v27, v50
	v_mov_b32_e32 v50, v21
	v_mov_b32_e32 v20, v22
	v_mov_b32_e32 v21, v52
	v_mov_b32_e32 v52, v23
	v_pk_fma_f32 v[22:23], v[28:29], v[62:63], v[88:89] op_sel_hi:[1,0,1]
	v_mov_b32_e32 v4, v33
	s_branch .Lic2_s117

.Lic2_s117:
	v_pk_fma_f32 v[22:23], v[24:25], v[64:65], v[22:23] op_sel_hi:[1,0,1]
	v_mov_b32_e32 v5, v33
	v_pk_fma_f32 v[22:23], v[30:31], v[66:67], v[22:23] op_sel_hi:[1,0,1]
	s_waitcnt lgkmcnt(2)
	v_add_f32_e32 v7, v8, v12
	v_pk_fma_f32 v[22:23], v[26:27], v[68:69], v[22:23] op_sel_hi:[1,0,1]
	s_waitcnt lgkmcnt(1)
	v_mov_b32_e32 v8, v16
	v_pk_fma_f32 v[22:23], v[50:51], v[70:71], v[22:23] op_sel_hi:[1,0,1]
	v_add_f32_e32 v11, v11, v15
	v_pk_fma_f32 v[20:21], v[20:21], v[72:73], v[22:23] op_sel_hi:[1,0,1]
	v_add_f32_e32 v22, v9, v13
	v_pk_fma_f32 v[20:21], v[52:53], v[86:87], v[20:21] op_sel_hi:[1,0,1]
	v_add_f32_e32 v23, v10, v14
	s_branch .Lic2_s118

.Lic2_s118:
	s_waitcnt lgkmcnt(0)
	v_mov_b32_e32 v9, v54
	v_max_f32_e32 v10, 0, v7
	v_mov_b32_e32 v54, v17
	v_max_f32_e32 v14, 0, v22
	v_pk_fma_f32 v[8:9], v[8:9], v[10:11], v[20:21] op_sel_hi:[1,0,1]
	v_mov_b32_e32 v12, v18
	v_mov_b32_e32 v13, v56
	v_max_f32_e32 v16, 0, v23
	v_pk_fma_f32 v[8:9], v[54:55], v[14:15], v[8:9] op_sel_hi:[1,0,1]
	v_max_f32_e32 v22, 0, v11
	v_pk_fma_f32 v[8:9], v[12:13], v[16:17], v[8:9] op_sel_hi:[1,0,1]
	v_mov_b32_e32 v56, v19
	ds_read_b128 v[10:13], v32 offset:52432
	s_branch .Lic2_s119

.Lic2_s119:
	ds_read_b128 v[14:17], v32 offset:52688
	ds_read_b128 v[18:21], v32 offset:52944
	v_pk_fma_f32 v[22:23], v[56:57], v[22:23], v[8:9] op_sel_hi:[1,0,1]
	v_and_b32_e32 v24, 64, v84
	v_xor_b32_e32 v7, 16, v84
	v_add_u32_e32 v8, 64, v24
	v_cmp_lt_i32_e64 s[6:7], v7, v8
	s_and_b64 s[8:9], s[2:3], vcc
	s_waitcnt lgkmcnt(2)
	v_add_f32_e32 v9, v0, v10
	v_add_f32_e32 v11, v1, v11
	s_waitcnt lgkmcnt(1)
	v_mov_b32_e32 v0, v14
	s_waitcnt lgkmcnt(0)
	s_branch .Lic2_s120

.Lic2_s120:
	v_mov_b32_e32 v1, v18
	v_max_f32_e32 v10, 0, v9
	v_add_f32_e32 v24, v2, v12
	v_add_f32_e32 v13, v3, v13
	v_mov_b32_e32 v18, v15
	v_max_f32_e32 v12, 0, v11
	v_pk_fma_f32 v[0:1], v[0:1], v[10:11], v[22:23] op_sel_hi:[1,0,1]
	v_mov_b32_e32 v2, v16
	v_mov_b32_e32 v3, v20
	v_max_f32_e32 v14, 0, v24
	v_pk_fma_f32 v[0:1], v[18:19], v[12:13], v[0:1] op_sel_hi:[1,0,1]
	v_cndmask_b32_e64 v7, v84, v7, s[6:7]
	v_mov_b32_e32 v20, v17
	v_max_f32_e32 v16, 0, v13
	s_branch .Lic2_s121

.Lic2_s121:
	v_pk_fma_f32 v[0:1], v[2:3], v[14:15], v[0:1] op_sel_hi:[1,0,1]
	v_lshlrev_b32_e32 v7, 2, v7
	v_pk_fma_f32 v[0:1], v[20:21], v[16:17], v[0:1] op_sel_hi:[1,0,1]
	ds_bpermute_b32 v2, v7, v0
	ds_bpermute_b32 v3, v7, v1
	v_xor_b32_e32 v7, 32, v84
	v_cmp_lt_i32_e64 s[6:7], v7, v8
	v_mov_b32_e32 v10, -1
	s_waitcnt lgkmcnt(0)
	v_pk_add_f32 v[0:1], v[0:1], v[2:3]
	v_cndmask_b32_e64 v7, v84, v7, s[6:7]
	v_lshlrev_b32_e32 v7, 2, v7
	ds_bpermute_b32 v2, v7, v0
	ds_bpermute_b32 v3, v7, v1
	s_branch .Lic2_s122

.Lic2_s122:
	v_mov_b32_e32 v7, 0
	s_and_saveexec_b64 s[6:7], s[8:9]
	s_cbranch_execz .LBB5_108
	v_mov_b32_e32 v10, v103
	s_waitcnt lgkmcnt(0)
	v_pk_add_f32 v[4:5], v[0:1], v[2:3]
	v_mov_b32_e32 v7, 1.0
.LBB5_108:
	s_or_b64 exec, exec, s[6:7]
	v_lshlrev_b32_e32 v0, 2, v84
	v_and_b32_e32 v0, 0x100, v0
	ds_bpermute_b32 v9, v0, v10
	s_xor_b64 s[10:11], s[8:9], -1
	s_waitcnt lgkmcnt(0)
	v_cmp_eq_u32_e32 vcc, v10, v9
	s_branch .Lic2_s123

.Lic2_s123:
	s_or_b64 s[10:11], vcc, s[10:11]
	v_cndmask_b32_e64 v0, 0, 1, s[10:11]
	v_cmp_ne_u32_e32 vcc, 0, v0
	s_cmp_lg_u64 vcc, exec
	v_cmp_gt_i32_e64 s[6:7], 0, v9
	s_cselect_b64 s[10:11], -1, 0
	s_or_b64 s[10:11], s[6:7], s[10:11]
	s_mov_b64 s[6:7], 0
	s_and_saveexec_b64 s[34:35], s[10:11]
	s_xor_b64 s[10:11], exec, s[34:35]
	s_cbranch_execnz .LBB5_111
	s_or_saveexec_b64 s[8:9], s[10:11]
	v_mov_b32_e32 v10, 1.0
	s_xor_b64 exec, exec, s[8:9]
	s_branch .Lic2_s124

.Lic2_s124:
	s_cbranch_execnz .LBB5_114

.LBB5_111:
	s_and_b64 s[8:9], s[4:5], s[8:9]
	s_and_saveexec_b64 s[34:35], s[8:9]
	s_xor_b64 s[8:9], exec, s[34:35]
	v_lshlrev_b32_e32 v0, 2, v10
	s_mov_b64 s[6:7], exec
	v_ashrrev_i32_e32 v1, 31, v0
	s_or_b64 exec, exec, s[8:9]
	s_branch .Lic2_s125

.Lic2_s125:
	s_and_b64 s[6:7], s[6:7], exec
	s_or_saveexec_b64 s[8:9], s[10:11]
	v_mov_b32_e32 v10, 1.0
	s_xor_b64 exec, exec, s[8:9]
	s_cbranch_execz .LBB5_110
.LBB5_114:
	v_xor_b32_e32 v0, 1, v84
	v_cmp_lt_i32_e32 vcc, v0, v8
	v_xor_b32_e32 v3, 2, v84
	s_mov_b64 s[10:11], s[6:7]
	v_cndmask_b32_e32 v0, v84, v0, vcc
	v_lshlrev_b32_e32 v1, 2, v0
	ds_bpermute_b32 v2, v1, v7
	ds_bpermute_b32 v0, v1, v4
	ds_bpermute_b32 v1, v1, v5
	s_branch .Lic2_s126

.Lic2_s126:
	v_cmp_lt_i32_e32 vcc, v3, v8
	s_waitcnt lgkmcnt(2)
	v_add_f32_e32 v6, v7, v2
	v_cndmask_b32_e32 v2, v84, v3, vcc
	v_lshlrev_b32_e32 v7, 2, v2
	s_waitcnt lgkmcnt(0)
	v_pk_add_f32 v[0:1], v[4:5], v[0:1]
	ds_bpermute_b32 v2, v7, v0
	ds_bpermute_b32 v3, v7, v1
	ds_bpermute_b32 v4, v7, v6
	s_waitcnt lgkmcnt(1)
	v_pk_add_f32 v[2:3], v[0:1], v[2:3]
	v_xor_b32_e32 v0, 4, v84
	v_cmp_lt_i32_e32 vcc, v0, v8
	s_branch .Lic2_s127

.Lic2_s127:
	s_waitcnt lgkmcnt(0)
	v_add_f32_e32 v11, v6, v4
	v_cndmask_b32_e32 v0, v84, v0, vcc
	v_lshlrev_b32_e32 v0, 2, v0
	ds_bpermute_b32 v6, v0, v2
	ds_bpermute_b32 v7, v0, v3
	ds_bpermute_b32 v8, v0, v11
	s_and_saveexec_b64 s[34:35], s[0:1]
	s_cbranch_execz .LBB5_116
	s_waitcnt lgkmcnt(0)
	v_add_f32_e32 v10, v11, v8
	v_pk_add_f32 v[4:5], v[2:3], v[6:7]
	v_lshlrev_b32_e32 v0, 2, v9
	v_mov_b32_e32 v1, v33
	s_branch .Lic2_s128

.Lic2_s128:
	s_or_b64 s[10:11], s[6:7], exec
